# P12 hand-written combine: four trips unrolled, next trip's index + residual loads issued one trip ahead (double-buffered residual registers)
# speedup vs baseline: 1.0192x; 1.0008x over previous
; __global__ void __launch_bounds__(512, 2) fwd_kernel(Params p) {
;     ...
;         for (int it0 = GT(); it0 < NI; it0 += UN * NGT) {
;             int mm[UN], cc[UN], ee[UN][4], rk[UN][4]; u32x4 xa[UN], xb[UN], y[UN][4];
; #pragma unroll
;             for (int u = 0; u < UN; ++u) { const int it = it0 + u * NGT < NI ? it0 + u * NGT : it0; mm[u] = it >> 7; cc[u] = (it & 127) * 16;
;                 const i32x4 e4 = *(const i32x4*)(tok_e + mm[u] * 4), r4 = *(const i32x4*)(tok_rank + mm[u] * 4);
; #pragma unroll
;                 for (int k = 0; k < 4; ++k) { ee[u][k] = e4[k]; rk[u][k] = r4[k]; }
;                 const bf16_t* xp = X1 + (size_t)mm[u] * DM + cc[u]; xa[u] = *(const u32x4*)xp; xb[u] = *(const u32x4*)(xp + 8); }
; #pragma unroll
;             for (int u = 0; u < UN; ++u)
; #pragma unroll
;                 for (int k = 0; k < 4; ++k) { const int pos = ts[ee[u][k]] * 256 + rk[u][k]; y[u][k] = *(const u32x4*)(Yb + (size_t)pos * DM + cc[u]); }
.LBB0_1194:
	s_or_b64 exec, exec, s[2:3]
	s_waitcnt lgkmcnt(0)
	s_barrier
	v_mbcnt_lo_u32_b32 v0, -1, 0
	v_mbcnt_hi_u32_b32 v0, -1, v0
	v_readlane_b32 s0, v252, 3
	s_nop 1
	v_add_u32_e32 v0, s0, v0
	v_readlane_b32 s0, v252, 7
	s_mov_b32 s11, 0x200000
	s_waitcnt vmcnt(9) lgkmcnt(0)
	v_add_u32_e32 v88, s0, v0
	v_cmp_gt_i32_e32 vcc, s11, v88
	s_barrier
	s_and_saveexec_b64 s[0:1], vcc
	s_cbranch_execz .LBB0_1207
	s_cmpk_lg_i32 s33, 0x100
	s_cbranch_scc1 .Lp12n_orig
	s_load_dwordx2 s[4:5], s[88:89], 0xb0
	s_mov_b32 s10, 0x3d800000
	s_mov_b32 s11, 0x3d800000
	s_add_i32 s23, 0, 0x25100
	v_and_b32_e32 v1, 63, v0
	v_bfe_u32 v2, v88, 6, 1
	v_lshrrev_b32_e32 v3, 7, v88
	v_lshlrev_b32_e32 v4, 2, v1
	v_lshl_or_b32 v4, v2, 10, v4
	v_lshlrev_b32_e32 v5, 3, v1
	v_lshl_or_b32 v5, v2, 11, v5
	v_lshlrev_b32_e32 v6, 4, v1
	v_lshl_or_b32 v6, v2, 12, v6
	v_mov_b32_e32 v192, v3
	v_lshlrev_b32_e32 v196, 4, v192
	v_add_u32_e32 v193, 0x400, v3
	v_lshlrev_b32_e32 v197, 4, v193
	v_add_u32_e32 v194, 0x800, v3
	v_lshlrev_b32_e32 v198, 4, v194
	v_add_u32_e32 v195, 0xc00, v3
	v_lshlrev_b32_e32 v199, 4, v195
	global_load_dwordx4 v[8:11], v196, s[16:17]
	global_load_dwordx4 v[12:15], v197, s[16:17]
	global_load_dwordx4 v[16:19], v198, s[16:17]
	global_load_dwordx4 v[20:23], v199, s[16:17]
	global_load_dwordx4 v[24:27], v196, s[18:19]
	global_load_dwordx4 v[28:31], v197, s[18:19]
	global_load_dwordx4 v[32:35], v198, s[18:19]
	global_load_dwordx4 v[36:39], v199, s[18:19]
	v_lshl_add_u32 v196, v192, 12, v5
	global_load_dwordx2 v[40:41], v196, s[14:15]
	global_load_dwordx2 v[42:43], v196, s[14:15] offset:512
	global_load_dwordx2 v[44:45], v196, s[14:15] offset:1024
	global_load_dwordx2 v[46:47], v196, s[14:15] offset:1536
	v_lshl_add_u32 v197, v193, 12, v5
	global_load_dwordx2 v[48:49], v197, s[14:15]
	global_load_dwordx2 v[50:51], v197, s[14:15] offset:512
	global_load_dwordx2 v[52:53], v197, s[14:15] offset:1024
	global_load_dwordx2 v[54:55], v197, s[14:15] offset:1536
	v_lshl_add_u32 v198, v194, 12, v5
	global_load_dwordx2 v[56:57], v198, s[14:15]
	global_load_dwordx2 v[58:59], v198, s[14:15] offset:512
	global_load_dwordx2 v[60:61], v198, s[14:15] offset:1024
	global_load_dwordx2 v[62:63], v198, s[14:15] offset:1536
	v_lshl_add_u32 v199, v195, 12, v5
	global_load_dwordx2 v[64:65], v199, s[14:15]
	global_load_dwordx2 v[66:67], v199, s[14:15] offset:512
	global_load_dwordx2 v[68:69], v199, s[14:15] offset:1024
	global_load_dwordx2 v[70:71], v199, s[14:15] offset:1536
	s_waitcnt lgkmcnt(0)
	s_waitcnt vmcnt(16)
	v_lshl_add_u32 v200, v8, 2, s23
	v_lshl_add_u32 v201, v9, 2, s23
	v_lshl_add_u32 v202, v10, 2, s23
	v_lshl_add_u32 v203, v11, 2, s23
	v_lshl_add_u32 v204, v12, 2, s23
	v_lshl_add_u32 v205, v13, 2, s23
	v_lshl_add_u32 v206, v14, 2, s23
	v_lshl_add_u32 v207, v15, 2, s23
	v_lshl_add_u32 v208, v16, 2, s23
	v_lshl_add_u32 v209, v17, 2, s23
	v_lshl_add_u32 v210, v18, 2, s23
	v_lshl_add_u32 v211, v19, 2, s23
	v_lshl_add_u32 v212, v20, 2, s23
	v_lshl_add_u32 v213, v21, 2, s23
	v_lshl_add_u32 v214, v22, 2, s23
	v_lshl_add_u32 v215, v23, 2, s23
	ds_read_b32 v136, v200
	ds_read_b32 v137, v201
	ds_read_b32 v138, v202
	ds_read_b32 v139, v203
	ds_read_b32 v140, v204
	ds_read_b32 v141, v205
	ds_read_b32 v142, v206
	ds_read_b32 v143, v207
	ds_read_b32 v144, v208
	ds_read_b32 v145, v209
	ds_read_b32 v146, v210
	ds_read_b32 v147, v211
	ds_read_b32 v148, v212
	ds_read_b32 v149, v213
	ds_read_b32 v150, v214
	ds_read_b32 v151, v215
	v_mov_b32_e32 v192, v3
	v_lshl_add_u32 v156, v192, 13, v6
	v_add_u32_e32 v193, 0x400, v3
	v_lshl_add_u32 v157, v193, 13, v6
	v_add_u32_e32 v194, 0x800, v3
	v_lshl_add_u32 v158, v194, 13, v6
	v_add_u32_e32 v195, 0xc00, v3
	v_lshl_add_u32 v159, v195, 13, v6
	s_waitcnt lgkmcnt(12)
	v_lshl_add_u32 v136, v136, 8, v24
	v_lshl_add_u32 v137, v137, 8, v25
	v_lshl_add_u32 v138, v138, 8, v26
	v_lshl_add_u32 v139, v139, 8, v27
	v_lshl_add_u32 v136, v136, 11, v4
	v_lshl_add_u32 v137, v137, 11, v4
	v_lshl_add_u32 v138, v138, 11, v4
	v_lshl_add_u32 v139, v139, 11, v4
	global_load_dword v72, v136, s[6:7]
	global_load_dword v73, v136, s[6:7] offset:256
	global_load_dword v74, v136, s[6:7] offset:512
	global_load_dword v75, v136, s[6:7] offset:768
	global_load_dword v76, v137, s[6:7]
	global_load_dword v77, v137, s[6:7] offset:256
	global_load_dword v78, v137, s[6:7] offset:512
	global_load_dword v79, v137, s[6:7] offset:768
	global_load_dword v80, v138, s[6:7]
	global_load_dword v81, v138, s[6:7] offset:256
	global_load_dword v82, v138, s[6:7] offset:512
	global_load_dword v83, v138, s[6:7] offset:768
	global_load_dword v84, v139, s[6:7]
	global_load_dword v85, v139, s[6:7] offset:256
	global_load_dword v86, v139, s[6:7] offset:512
	global_load_dword v87, v139, s[6:7] offset:768
	s_waitcnt lgkmcnt(8)
	v_lshl_add_u32 v140, v140, 8, v28
	v_lshl_add_u32 v141, v141, 8, v29
	v_lshl_add_u32 v142, v142, 8, v30
	v_lshl_add_u32 v143, v143, 8, v31
	v_lshl_add_u32 v140, v140, 11, v4
	v_lshl_add_u32 v141, v141, 11, v4
	v_lshl_add_u32 v142, v142, 11, v4
	v_lshl_add_u32 v143, v143, 11, v4
	global_load_dword v88, v140, s[6:7]
	global_load_dword v89, v140, s[6:7] offset:256
	global_load_dword v90, v140, s[6:7] offset:512
	global_load_dword v91, v140, s[6:7] offset:768
	global_load_dword v92, v141, s[6:7]
	global_load_dword v93, v141, s[6:7] offset:256
	global_load_dword v94, v141, s[6:7] offset:512
	global_load_dword v95, v141, s[6:7] offset:768
	global_load_dword v96, v142, s[6:7]
	global_load_dword v97, v142, s[6:7] offset:256
	global_load_dword v98, v142, s[6:7] offset:512
	global_load_dword v99, v142, s[6:7] offset:768
	global_load_dword v100, v143, s[6:7]
	global_load_dword v101, v143, s[6:7] offset:256
	global_load_dword v102, v143, s[6:7] offset:512
	global_load_dword v103, v143, s[6:7] offset:768
	s_waitcnt lgkmcnt(4)
; __device__ __forceinline__ float bf_lo(unsigned w) { return __uint_as_float(w << 16); }
; __device__ __forceinline__ float bf_hi(unsigned w) { return __uint_as_float(w & 0xffff0000u); }
; __global__ void __launch_bounds__(512, 2) fwd_kernel(Params p) {
;     ...
;                 for (int k = 0; k < 4; ++k) { const int pos = ts[ee[u][k]] * 256 + rk[u][k]; y[u][k] = *(const u32x4*)(Yb + (size_t)pos * DM + cc[u]); }
; #pragma unroll
;             for (int u = 0; u < UN; ++u) {
;                 f32x4 a[4];
;                 a[0] = (f32x4){bf_lo(xa[u].x), bf_hi(xa[u].x), bf_lo(xa[u].y), bf_hi(xa[u].y)}; a[1] = (f32x4){bf_lo(xa[u].z), bf_hi(xa[u].z), bf_lo(xa[u].w), bf_hi(xa[u].w)};
;                 a[2] = (f32x4){bf_lo(xb[u].x), bf_hi(xb[u].x), bf_lo(xb[u].y), bf_hi(xb[u].y)}; a[3] = (f32x4){bf_lo(xb[u].z), bf_hi(xb[u].z), bf_lo(xb[u].w), bf_hi(xb[u].w)};
; #pragma unroll
;                 for (int k = 0; k < 4; ++k)
; #pragma unroll
;                     for (int q = 0; q < 4; ++q) { const f32x2 lo = __builtin_amdgcn_cvt_pk_f32_fp8((int)y[u][k][q], false), hi = __builtin_amdgcn_cvt_pk_f32_fp8((int)y[u][k][q], true);
;                         a[q].x += lo.x * (1.0f / Y8_SCALE); a[q].y += lo.y * (1.0f / Y8_SCALE); a[q].z += hi.x * (1.0f / Y8_SCALE); a[q].w += hi.y * (1.0f / Y8_SCALE); }
;                 if (it0 + u * NGT < NI) { float* op = p.out + (size_t)mm[u] * DM + cc[u];
; #pragma unroll
;                     for (int q = 0; q < 4; ++q) *(f32x4*)(op + 4 * q) = a[q]; }
	v_lshl_add_u32 v144, v144, 8, v32
	v_lshl_add_u32 v145, v145, 8, v33
	v_lshl_add_u32 v146, v146, 8, v34
	v_lshl_add_u32 v147, v147, 8, v35
	v_lshl_add_u32 v144, v144, 11, v4
	v_lshl_add_u32 v145, v145, 11, v4
	v_lshl_add_u32 v146, v146, 11, v4
	v_lshl_add_u32 v147, v147, 11, v4
	global_load_dword v104, v144, s[6:7]
	global_load_dword v105, v144, s[6:7] offset:256
	global_load_dword v106, v144, s[6:7] offset:512
	global_load_dword v107, v144, s[6:7] offset:768
	global_load_dword v108, v145, s[6:7]
	global_load_dword v109, v145, s[6:7] offset:256
	global_load_dword v110, v145, s[6:7] offset:512
	global_load_dword v111, v145, s[6:7] offset:768
	global_load_dword v112, v146, s[6:7]
	global_load_dword v113, v146, s[6:7] offset:256
	global_load_dword v114, v146, s[6:7] offset:512
	global_load_dword v115, v146, s[6:7] offset:768
	global_load_dword v116, v147, s[6:7]
	global_load_dword v117, v147, s[6:7] offset:256
	global_load_dword v118, v147, s[6:7] offset:512
	global_load_dword v119, v147, s[6:7] offset:768
	s_waitcnt lgkmcnt(0)
	v_lshl_add_u32 v148, v148, 8, v36
	v_lshl_add_u32 v149, v149, 8, v37
	v_lshl_add_u32 v150, v150, 8, v38
	v_lshl_add_u32 v151, v151, 8, v39
	v_lshl_add_u32 v148, v148, 11, v4
	v_lshl_add_u32 v149, v149, 11, v4
	v_lshl_add_u32 v150, v150, 11, v4
	v_lshl_add_u32 v151, v151, 11, v4
	global_load_dword v120, v148, s[6:7]
	global_load_dword v121, v148, s[6:7] offset:256
	global_load_dword v122, v148, s[6:7] offset:512
	global_load_dword v123, v148, s[6:7] offset:768
	global_load_dword v124, v149, s[6:7]
	global_load_dword v125, v149, s[6:7] offset:256
	global_load_dword v126, v149, s[6:7] offset:512
	global_load_dword v127, v149, s[6:7] offset:768
	global_load_dword v128, v150, s[6:7]
	global_load_dword v129, v150, s[6:7] offset:256
	global_load_dword v130, v150, s[6:7] offset:512
	global_load_dword v131, v150, s[6:7] offset:768
	global_load_dword v132, v151, s[6:7]
	global_load_dword v133, v151, s[6:7] offset:256
	global_load_dword v134, v151, s[6:7] offset:512
	global_load_dword v135, v151, s[6:7] offset:768
	s_waitcnt vmcnt(48)
	v_lshlrev_b32_e32 v176, 16, v40
	v_and_b32_e32 v177, 0xffff0000, v40
	v_lshlrev_b32_e32 v178, 16, v41
	v_and_b32_e32 v179, 0xffff0000, v41
	v_cvt_pk_f32_fp8_e32 v[160:161], v72
	v_cvt_pk_f32_fp8_sdwa v[162:163], v72 src0_sel:WORD_1
	v_pk_fma_f32 v[176:177], v[160:161], s[10:11], v[176:177] op_sel_hi:[1,0,1]
	v_pk_fma_f32 v[178:179], v[162:163], s[10:11], v[178:179] op_sel_hi:[1,0,1]
	v_cvt_pk_f32_fp8_e32 v[164:165], v76
	v_cvt_pk_f32_fp8_sdwa v[166:167], v76 src0_sel:WORD_1
	v_pk_fma_f32 v[176:177], v[164:165], s[10:11], v[176:177] op_sel_hi:[1,0,1]
	v_pk_fma_f32 v[178:179], v[166:167], s[10:11], v[178:179] op_sel_hi:[1,0,1]
	v_cvt_pk_f32_fp8_e32 v[168:169], v80
	v_cvt_pk_f32_fp8_sdwa v[170:171], v80 src0_sel:WORD_1
	v_pk_fma_f32 v[176:177], v[168:169], s[10:11], v[176:177] op_sel_hi:[1,0,1]
	v_pk_fma_f32 v[178:179], v[170:171], s[10:11], v[178:179] op_sel_hi:[1,0,1]
	v_cvt_pk_f32_fp8_e32 v[172:173], v84
	v_cvt_pk_f32_fp8_sdwa v[174:175], v84 src0_sel:WORD_1
	v_pk_fma_f32 v[176:177], v[172:173], s[10:11], v[176:177] op_sel_hi:[1,0,1]
	v_pk_fma_f32 v[178:179], v[174:175], s[10:11], v[178:179] op_sel_hi:[1,0,1]
	global_store_dwordx4 v156, v[176:179], s[4:5]
	v_lshlrev_b32_e32 v180, 16, v42
	v_and_b32_e32 v181, 0xffff0000, v42
	v_lshlrev_b32_e32 v182, 16, v43
	v_and_b32_e32 v183, 0xffff0000, v43
	v_cvt_pk_f32_fp8_e32 v[160:161], v73
	v_cvt_pk_f32_fp8_sdwa v[162:163], v73 src0_sel:WORD_1
	v_pk_fma_f32 v[180:181], v[160:161], s[10:11], v[180:181] op_sel_hi:[1,0,1]
	v_pk_fma_f32 v[182:183], v[162:163], s[10:11], v[182:183] op_sel_hi:[1,0,1]
	v_cvt_pk_f32_fp8_e32 v[164:165], v77
	v_cvt_pk_f32_fp8_sdwa v[166:167], v77 src0_sel:WORD_1
	v_pk_fma_f32 v[180:181], v[164:165], s[10:11], v[180:181] op_sel_hi:[1,0,1]
	v_pk_fma_f32 v[182:183], v[166:167], s[10:11], v[182:183] op_sel_hi:[1,0,1]
	v_cvt_pk_f32_fp8_e32 v[168:169], v81
	v_cvt_pk_f32_fp8_sdwa v[170:171], v81 src0_sel:WORD_1
	v_pk_fma_f32 v[180:181], v[168:169], s[10:11], v[180:181] op_sel_hi:[1,0,1]
	v_pk_fma_f32 v[182:183], v[170:171], s[10:11], v[182:183] op_sel_hi:[1,0,1]
	v_cvt_pk_f32_fp8_e32 v[172:173], v85
	v_cvt_pk_f32_fp8_sdwa v[174:175], v85 src0_sel:WORD_1
	v_pk_fma_f32 v[180:181], v[172:173], s[10:11], v[180:181] op_sel_hi:[1,0,1]
	v_pk_fma_f32 v[182:183], v[174:175], s[10:11], v[182:183] op_sel_hi:[1,0,1]
	global_store_dwordx4 v156, v[180:183], s[4:5] offset:1024
	v_lshlrev_b32_e32 v184, 16, v44
	v_and_b32_e32 v185, 0xffff0000, v44
	v_lshlrev_b32_e32 v186, 16, v45
	v_and_b32_e32 v187, 0xffff0000, v45
	v_cvt_pk_f32_fp8_e32 v[160:161], v74
	v_cvt_pk_f32_fp8_sdwa v[162:163], v74 src0_sel:WORD_1
	v_pk_fma_f32 v[184:185], v[160:161], s[10:11], v[184:185] op_sel_hi:[1,0,1]
	v_pk_fma_f32 v[186:187], v[162:163], s[10:11], v[186:187] op_sel_hi:[1,0,1]
	v_cvt_pk_f32_fp8_e32 v[164:165], v78
	v_cvt_pk_f32_fp8_sdwa v[166:167], v78 src0_sel:WORD_1
	v_pk_fma_f32 v[184:185], v[164:165], s[10:11], v[184:185] op_sel_hi:[1,0,1]
	v_pk_fma_f32 v[186:187], v[166:167], s[10:11], v[186:187] op_sel_hi:[1,0,1]
	v_cvt_pk_f32_fp8_e32 v[168:169], v82
	v_cvt_pk_f32_fp8_sdwa v[170:171], v82 src0_sel:WORD_1
	v_pk_fma_f32 v[184:185], v[168:169], s[10:11], v[184:185] op_sel_hi:[1,0,1]
	v_pk_fma_f32 v[186:187], v[170:171], s[10:11], v[186:187] op_sel_hi:[1,0,1]
	v_cvt_pk_f32_fp8_e32 v[172:173], v86
	v_cvt_pk_f32_fp8_sdwa v[174:175], v86 src0_sel:WORD_1
	v_pk_fma_f32 v[184:185], v[172:173], s[10:11], v[184:185] op_sel_hi:[1,0,1]
	v_pk_fma_f32 v[186:187], v[174:175], s[10:11], v[186:187] op_sel_hi:[1,0,1]
	global_store_dwordx4 v156, v[184:187], s[4:5] offset:2048
; __device__ __forceinline__ float bf_lo(unsigned w) { return __uint_as_float(w << 16); }
; __device__ __forceinline__ float bf_hi(unsigned w) { return __uint_as_float(w & 0xffff0000u); }
; __global__ void __launch_bounds__(512, 2) fwd_kernel(Params p) {
;     ...
;         for (int it0 = GT(); it0 < NI; it0 += UN * NGT) {
;             int mm[UN], cc[UN], ee[UN][4], rk[UN][4]; u32x4 xa[UN], xb[UN], y[UN][4];
; #pragma unroll
;             for (int u = 0; u < UN; ++u) { const int it = it0 + u * NGT < NI ? it0 + u * NGT : it0; mm[u] = it >> 7; cc[u] = (it & 127) * 16;
;                 const i32x4 e4 = *(const i32x4*)(tok_e + mm[u] * 4), r4 = *(const i32x4*)(tok_rank + mm[u] * 4);
; #pragma unroll
;                 for (int k = 0; k < 4; ++k) { ee[u][k] = e4[k]; rk[u][k] = r4[k]; }
;                 const bf16_t* xp = X1 + (size_t)mm[u] * DM + cc[u]; xa[u] = *(const u32x4*)xp; xb[u] = *(const u32x4*)(xp + 8); }
; #pragma unroll
;             for (int u = 0; u < UN; ++u)
; #pragma unroll
;                 for (int k = 0; k < 4; ++k) { const int pos = ts[ee[u][k]] * 256 + rk[u][k]; y[u][k] = *(const u32x4*)(Yb + (size_t)pos * DM + cc[u]); }
; #pragma unroll
;             for (int u = 0; u < UN; ++u) {
;                 f32x4 a[4];
;                 a[0] = (f32x4){bf_lo(xa[u].x), bf_hi(xa[u].x), bf_lo(xa[u].y), bf_hi(xa[u].y)}; a[1] = (f32x4){bf_lo(xa[u].z), bf_hi(xa[u].z), bf_lo(xa[u].w), bf_hi(xa[u].w)};
;                 a[2] = (f32x4){bf_lo(xb[u].x), bf_hi(xb[u].x), bf_lo(xb[u].y), bf_hi(xb[u].y)}; a[3] = (f32x4){bf_lo(xb[u].z), bf_hi(xb[u].z), bf_lo(xb[u].w), bf_hi(xb[u].w)};
; #pragma unroll
;                 for (int k = 0; k < 4; ++k)
; #pragma unroll
;                     for (int q = 0; q < 4; ++q) { const f32x2 lo = __builtin_amdgcn_cvt_pk_f32_fp8((int)y[u][k][q], false), hi = __builtin_amdgcn_cvt_pk_f32_fp8((int)y[u][k][q], true);
;                         a[q].x += lo.x * (1.0f / Y8_SCALE); a[q].y += lo.y * (1.0f / Y8_SCALE); a[q].z += hi.x * (1.0f / Y8_SCALE); a[q].w += hi.y * (1.0f / Y8_SCALE); }
;                 if (it0 + u * NGT < NI) { float* op = p.out + (size_t)mm[u] * DM + cc[u];
; #pragma unroll
;                     for (int q = 0; q < 4; ++q) *(f32x4*)(op + 4 * q) = a[q]; }
	v_lshlrev_b32_e32 v188, 16, v46
	v_and_b32_e32 v189, 0xffff0000, v46
	v_lshlrev_b32_e32 v190, 16, v47
	v_and_b32_e32 v191, 0xffff0000, v47
	v_cvt_pk_f32_fp8_e32 v[160:161], v75
	v_cvt_pk_f32_fp8_sdwa v[162:163], v75 src0_sel:WORD_1
	v_pk_fma_f32 v[188:189], v[160:161], s[10:11], v[188:189] op_sel_hi:[1,0,1]
	v_pk_fma_f32 v[190:191], v[162:163], s[10:11], v[190:191] op_sel_hi:[1,0,1]
	v_cvt_pk_f32_fp8_e32 v[164:165], v79
	v_cvt_pk_f32_fp8_sdwa v[166:167], v79 src0_sel:WORD_1
	v_pk_fma_f32 v[188:189], v[164:165], s[10:11], v[188:189] op_sel_hi:[1,0,1]
	v_pk_fma_f32 v[190:191], v[166:167], s[10:11], v[190:191] op_sel_hi:[1,0,1]
	v_cvt_pk_f32_fp8_e32 v[168:169], v83
	v_cvt_pk_f32_fp8_sdwa v[170:171], v83 src0_sel:WORD_1
	v_pk_fma_f32 v[188:189], v[168:169], s[10:11], v[188:189] op_sel_hi:[1,0,1]
	v_pk_fma_f32 v[190:191], v[170:171], s[10:11], v[190:191] op_sel_hi:[1,0,1]
	v_cvt_pk_f32_fp8_e32 v[172:173], v87
	v_cvt_pk_f32_fp8_sdwa v[174:175], v87 src0_sel:WORD_1
	v_pk_fma_f32 v[188:189], v[172:173], s[10:11], v[188:189] op_sel_hi:[1,0,1]
	v_pk_fma_f32 v[190:191], v[174:175], s[10:11], v[190:191] op_sel_hi:[1,0,1]
	global_store_dwordx4 v156, v[188:191], s[4:5] offset:3072
	v_add_u32_e32 v192, 0x1000, v3
	v_lshlrev_b32_e32 v196, 4, v192
	v_add_u32_e32 v193, 0x1400, v3
	v_lshlrev_b32_e32 v197, 4, v193
	v_add_u32_e32 v194, 0x1800, v3
	v_lshlrev_b32_e32 v198, 4, v194
	v_add_u32_e32 v195, 0x1c00, v3
	v_lshlrev_b32_e32 v199, 4, v195
	global_load_dwordx4 v[8:11], v196, s[16:17]
	global_load_dwordx4 v[12:15], v197, s[16:17]
	global_load_dwordx4 v[16:19], v198, s[16:17]
	global_load_dwordx4 v[20:23], v199, s[16:17]
	global_load_dwordx4 v[24:27], v196, s[18:19]
	global_load_dwordx4 v[28:31], v197, s[18:19]
	global_load_dwordx4 v[32:35], v198, s[18:19]
	global_load_dwordx4 v[36:39], v199, s[18:19]
	v_lshl_add_u32 v196, v192, 12, v5
	global_load_dwordx2 v[216:217], v196, s[14:15]
	global_load_dwordx2 v[218:219], v196, s[14:15] offset:512
	global_load_dwordx2 v[220:221], v196, s[14:15] offset:1024
	global_load_dwordx2 v[222:223], v196, s[14:15] offset:1536
	v_lshl_add_u32 v197, v193, 12, v5
	global_load_dwordx2 v[224:225], v197, s[14:15]
	global_load_dwordx2 v[226:227], v197, s[14:15] offset:512
	global_load_dwordx2 v[228:229], v197, s[14:15] offset:1024
	global_load_dwordx2 v[230:231], v197, s[14:15] offset:1536
	v_lshl_add_u32 v198, v194, 12, v5
	global_load_dwordx2 v[232:233], v198, s[14:15]
	global_load_dwordx2 v[234:235], v198, s[14:15] offset:512
	global_load_dwordx2 v[236:237], v198, s[14:15] offset:1024
	global_load_dwordx2 v[238:239], v198, s[14:15] offset:1536
	v_lshl_add_u32 v199, v195, 12, v5
	global_load_dwordx2 v[240:241], v199, s[14:15]
	global_load_dwordx2 v[242:243], v199, s[14:15] offset:512
	global_load_dwordx2 v[244:245], v199, s[14:15] offset:1024
	global_load_dwordx2 v[246:247], v199, s[14:15] offset:1536
	s_waitcnt vmcnt(60)
	v_lshlrev_b32_e32 v176, 16, v48
	v_and_b32_e32 v177, 0xffff0000, v48
	v_lshlrev_b32_e32 v178, 16, v49
	v_and_b32_e32 v179, 0xffff0000, v49
	v_cvt_pk_f32_fp8_e32 v[160:161], v88
	v_cvt_pk_f32_fp8_sdwa v[162:163], v88 src0_sel:WORD_1
	v_pk_fma_f32 v[176:177], v[160:161], s[10:11], v[176:177] op_sel_hi:[1,0,1]
	v_pk_fma_f32 v[178:179], v[162:163], s[10:11], v[178:179] op_sel_hi:[1,0,1]
	v_cvt_pk_f32_fp8_e32 v[164:165], v92
	v_cvt_pk_f32_fp8_sdwa v[166:167], v92 src0_sel:WORD_1
	v_pk_fma_f32 v[176:177], v[164:165], s[10:11], v[176:177] op_sel_hi:[1,0,1]
	v_pk_fma_f32 v[178:179], v[166:167], s[10:11], v[178:179] op_sel_hi:[1,0,1]
	v_cvt_pk_f32_fp8_e32 v[168:169], v96
	v_cvt_pk_f32_fp8_sdwa v[170:171], v96 src0_sel:WORD_1
	v_pk_fma_f32 v[176:177], v[168:169], s[10:11], v[176:177] op_sel_hi:[1,0,1]
	v_pk_fma_f32 v[178:179], v[170:171], s[10:11], v[178:179] op_sel_hi:[1,0,1]
	v_cvt_pk_f32_fp8_e32 v[172:173], v100
	v_cvt_pk_f32_fp8_sdwa v[174:175], v100 src0_sel:WORD_1
	v_pk_fma_f32 v[176:177], v[172:173], s[10:11], v[176:177] op_sel_hi:[1,0,1]
	v_pk_fma_f32 v[178:179], v[174:175], s[10:11], v[178:179] op_sel_hi:[1,0,1]
	global_store_dwordx4 v157, v[176:179], s[4:5]
	v_lshlrev_b32_e32 v180, 16, v50
	v_and_b32_e32 v181, 0xffff0000, v50
	v_lshlrev_b32_e32 v182, 16, v51
	v_and_b32_e32 v183, 0xffff0000, v51
	v_cvt_pk_f32_fp8_e32 v[160:161], v89
	v_cvt_pk_f32_fp8_sdwa v[162:163], v89 src0_sel:WORD_1
	v_pk_fma_f32 v[180:181], v[160:161], s[10:11], v[180:181] op_sel_hi:[1,0,1]
	v_pk_fma_f32 v[182:183], v[162:163], s[10:11], v[182:183] op_sel_hi:[1,0,1]
	v_cvt_pk_f32_fp8_e32 v[164:165], v93
	v_cvt_pk_f32_fp8_sdwa v[166:167], v93 src0_sel:WORD_1
	v_pk_fma_f32 v[180:181], v[164:165], s[10:11], v[180:181] op_sel_hi:[1,0,1]
	v_pk_fma_f32 v[182:183], v[166:167], s[10:11], v[182:183] op_sel_hi:[1,0,1]
	v_cvt_pk_f32_fp8_e32 v[168:169], v97
	v_cvt_pk_f32_fp8_sdwa v[170:171], v97 src0_sel:WORD_1
	v_pk_fma_f32 v[180:181], v[168:169], s[10:11], v[180:181] op_sel_hi:[1,0,1]
	v_pk_fma_f32 v[182:183], v[170:171], s[10:11], v[182:183] op_sel_hi:[1,0,1]
	v_cvt_pk_f32_fp8_e32 v[172:173], v101
	v_cvt_pk_f32_fp8_sdwa v[174:175], v101 src0_sel:WORD_1
	v_pk_fma_f32 v[180:181], v[172:173], s[10:11], v[180:181] op_sel_hi:[1,0,1]
	v_pk_fma_f32 v[182:183], v[174:175], s[10:11], v[182:183] op_sel_hi:[1,0,1]
	global_store_dwordx4 v157, v[180:183], s[4:5] offset:1024
	v_lshlrev_b32_e32 v184, 16, v52
	v_and_b32_e32 v185, 0xffff0000, v52
	v_lshlrev_b32_e32 v186, 16, v53
	v_and_b32_e32 v187, 0xffff0000, v53
	v_cvt_pk_f32_fp8_e32 v[160:161], v90
	v_cvt_pk_f32_fp8_sdwa v[162:163], v90 src0_sel:WORD_1
	v_pk_fma_f32 v[184:185], v[160:161], s[10:11], v[184:185] op_sel_hi:[1,0,1]
	v_pk_fma_f32 v[186:187], v[162:163], s[10:11], v[186:187] op_sel_hi:[1,0,1]
; __device__ __forceinline__ float bf_lo(unsigned w) { return __uint_as_float(w << 16); }
; __device__ __forceinline__ float bf_hi(unsigned w) { return __uint_as_float(w & 0xffff0000u); }
; __global__ void __launch_bounds__(512, 2) fwd_kernel(Params p) {
;     ...
;             for (int u = 0; u < UN; ++u) {
;                 f32x4 a[4];
;                 a[0] = (f32x4){bf_lo(xa[u].x), bf_hi(xa[u].x), bf_lo(xa[u].y), bf_hi(xa[u].y)}; a[1] = (f32x4){bf_lo(xa[u].z), bf_hi(xa[u].z), bf_lo(xa[u].w), bf_hi(xa[u].w)};
;                 a[2] = (f32x4){bf_lo(xb[u].x), bf_hi(xb[u].x), bf_lo(xb[u].y), bf_hi(xb[u].y)}; a[3] = (f32x4){bf_lo(xb[u].z), bf_hi(xb[u].z), bf_lo(xb[u].w), bf_hi(xb[u].w)};
; #pragma unroll
;                 for (int k = 0; k < 4; ++k)
; #pragma unroll
;                     for (int q = 0; q < 4; ++q) { const f32x2 lo = __builtin_amdgcn_cvt_pk_f32_fp8((int)y[u][k][q], false), hi = __builtin_amdgcn_cvt_pk_f32_fp8((int)y[u][k][q], true);
;                         a[q].x += lo.x * (1.0f / Y8_SCALE); a[q].y += lo.y * (1.0f / Y8_SCALE); a[q].z += hi.x * (1.0f / Y8_SCALE); a[q].w += hi.y * (1.0f / Y8_SCALE); }
;                 if (it0 + u * NGT < NI) { float* op = p.out + (size_t)mm[u] * DM + cc[u];
; #pragma unroll
;                     for (int q = 0; q < 4; ++q) *(f32x4*)(op + 4 * q) = a[q]; }
	v_cvt_pk_f32_fp8_e32 v[164:165], v94
	v_cvt_pk_f32_fp8_sdwa v[166:167], v94 src0_sel:WORD_1
	v_pk_fma_f32 v[184:185], v[164:165], s[10:11], v[184:185] op_sel_hi:[1,0,1]
	v_pk_fma_f32 v[186:187], v[166:167], s[10:11], v[186:187] op_sel_hi:[1,0,1]
	v_cvt_pk_f32_fp8_e32 v[168:169], v98
	v_cvt_pk_f32_fp8_sdwa v[170:171], v98 src0_sel:WORD_1
	v_pk_fma_f32 v[184:185], v[168:169], s[10:11], v[184:185] op_sel_hi:[1,0,1]
	v_pk_fma_f32 v[186:187], v[170:171], s[10:11], v[186:187] op_sel_hi:[1,0,1]
	v_cvt_pk_f32_fp8_e32 v[172:173], v102
	v_cvt_pk_f32_fp8_sdwa v[174:175], v102 src0_sel:WORD_1
	v_pk_fma_f32 v[184:185], v[172:173], s[10:11], v[184:185] op_sel_hi:[1,0,1]
	v_pk_fma_f32 v[186:187], v[174:175], s[10:11], v[186:187] op_sel_hi:[1,0,1]
	global_store_dwordx4 v157, v[184:187], s[4:5] offset:2048
	v_lshlrev_b32_e32 v188, 16, v54
	v_and_b32_e32 v189, 0xffff0000, v54
	v_lshlrev_b32_e32 v190, 16, v55
	v_and_b32_e32 v191, 0xffff0000, v55
	v_cvt_pk_f32_fp8_e32 v[160:161], v91
	v_cvt_pk_f32_fp8_sdwa v[162:163], v91 src0_sel:WORD_1
	v_pk_fma_f32 v[188:189], v[160:161], s[10:11], v[188:189] op_sel_hi:[1,0,1]
	v_pk_fma_f32 v[190:191], v[162:163], s[10:11], v[190:191] op_sel_hi:[1,0,1]
	v_cvt_pk_f32_fp8_e32 v[164:165], v95
	v_cvt_pk_f32_fp8_sdwa v[166:167], v95 src0_sel:WORD_1
	v_pk_fma_f32 v[188:189], v[164:165], s[10:11], v[188:189] op_sel_hi:[1,0,1]
	v_pk_fma_f32 v[190:191], v[166:167], s[10:11], v[190:191] op_sel_hi:[1,0,1]
	v_cvt_pk_f32_fp8_e32 v[168:169], v99
	v_cvt_pk_f32_fp8_sdwa v[170:171], v99 src0_sel:WORD_1
	v_pk_fma_f32 v[188:189], v[168:169], s[10:11], v[188:189] op_sel_hi:[1,0,1]
	v_pk_fma_f32 v[190:191], v[170:171], s[10:11], v[190:191] op_sel_hi:[1,0,1]
	v_cvt_pk_f32_fp8_e32 v[172:173], v103
	v_cvt_pk_f32_fp8_sdwa v[174:175], v103 src0_sel:WORD_1
	v_pk_fma_f32 v[188:189], v[172:173], s[10:11], v[188:189] op_sel_hi:[1,0,1]
	v_pk_fma_f32 v[190:191], v[174:175], s[10:11], v[190:191] op_sel_hi:[1,0,1]
	global_store_dwordx4 v157, v[188:191], s[4:5] offset:3072
	s_waitcnt vmcnt(48)
	v_lshlrev_b32_e32 v176, 16, v56
	v_and_b32_e32 v177, 0xffff0000, v56
	v_lshlrev_b32_e32 v178, 16, v57
	v_and_b32_e32 v179, 0xffff0000, v57
	v_cvt_pk_f32_fp8_e32 v[160:161], v104
	v_cvt_pk_f32_fp8_sdwa v[162:163], v104 src0_sel:WORD_1
	v_pk_fma_f32 v[176:177], v[160:161], s[10:11], v[176:177] op_sel_hi:[1,0,1]
	v_pk_fma_f32 v[178:179], v[162:163], s[10:11], v[178:179] op_sel_hi:[1,0,1]
	v_cvt_pk_f32_fp8_e32 v[164:165], v108
	v_cvt_pk_f32_fp8_sdwa v[166:167], v108 src0_sel:WORD_1
	v_pk_fma_f32 v[176:177], v[164:165], s[10:11], v[176:177] op_sel_hi:[1,0,1]
	v_pk_fma_f32 v[178:179], v[166:167], s[10:11], v[178:179] op_sel_hi:[1,0,1]
	v_cvt_pk_f32_fp8_e32 v[168:169], v112
	v_cvt_pk_f32_fp8_sdwa v[170:171], v112 src0_sel:WORD_1
	v_pk_fma_f32 v[176:177], v[168:169], s[10:11], v[176:177] op_sel_hi:[1,0,1]
	v_pk_fma_f32 v[178:179], v[170:171], s[10:11], v[178:179] op_sel_hi:[1,0,1]
	v_cvt_pk_f32_fp8_e32 v[172:173], v116
	v_cvt_pk_f32_fp8_sdwa v[174:175], v116 src0_sel:WORD_1
	v_pk_fma_f32 v[176:177], v[172:173], s[10:11], v[176:177] op_sel_hi:[1,0,1]
	v_pk_fma_f32 v[178:179], v[174:175], s[10:11], v[178:179] op_sel_hi:[1,0,1]
	global_store_dwordx4 v158, v[176:179], s[4:5]
	v_lshlrev_b32_e32 v180, 16, v58
	v_and_b32_e32 v181, 0xffff0000, v58
	v_lshlrev_b32_e32 v182, 16, v59
	v_and_b32_e32 v183, 0xffff0000, v59
	v_cvt_pk_f32_fp8_e32 v[160:161], v105
	v_cvt_pk_f32_fp8_sdwa v[162:163], v105 src0_sel:WORD_1
	v_pk_fma_f32 v[180:181], v[160:161], s[10:11], v[180:181] op_sel_hi:[1,0,1]
	v_pk_fma_f32 v[182:183], v[162:163], s[10:11], v[182:183] op_sel_hi:[1,0,1]
	v_cvt_pk_f32_fp8_e32 v[164:165], v109
	v_cvt_pk_f32_fp8_sdwa v[166:167], v109 src0_sel:WORD_1
	v_pk_fma_f32 v[180:181], v[164:165], s[10:11], v[180:181] op_sel_hi:[1,0,1]
	v_pk_fma_f32 v[182:183], v[166:167], s[10:11], v[182:183] op_sel_hi:[1,0,1]
	v_cvt_pk_f32_fp8_e32 v[168:169], v113
	v_cvt_pk_f32_fp8_sdwa v[170:171], v113 src0_sel:WORD_1
	v_pk_fma_f32 v[180:181], v[168:169], s[10:11], v[180:181] op_sel_hi:[1,0,1]
	v_pk_fma_f32 v[182:183], v[170:171], s[10:11], v[182:183] op_sel_hi:[1,0,1]
	v_cvt_pk_f32_fp8_e32 v[172:173], v117
	v_cvt_pk_f32_fp8_sdwa v[174:175], v117 src0_sel:WORD_1
	v_pk_fma_f32 v[180:181], v[172:173], s[10:11], v[180:181] op_sel_hi:[1,0,1]
	v_pk_fma_f32 v[182:183], v[174:175], s[10:11], v[182:183] op_sel_hi:[1,0,1]
	global_store_dwordx4 v158, v[180:183], s[4:5] offset:1024
	v_lshlrev_b32_e32 v184, 16, v60
	v_and_b32_e32 v185, 0xffff0000, v60
	v_lshlrev_b32_e32 v186, 16, v61
	v_and_b32_e32 v187, 0xffff0000, v61
	v_cvt_pk_f32_fp8_e32 v[160:161], v106
	v_cvt_pk_f32_fp8_sdwa v[162:163], v106 src0_sel:WORD_1
	v_pk_fma_f32 v[184:185], v[160:161], s[10:11], v[184:185] op_sel_hi:[1,0,1]
	v_pk_fma_f32 v[186:187], v[162:163], s[10:11], v[186:187] op_sel_hi:[1,0,1]
	v_cvt_pk_f32_fp8_e32 v[164:165], v110
	v_cvt_pk_f32_fp8_sdwa v[166:167], v110 src0_sel:WORD_1
	v_pk_fma_f32 v[184:185], v[164:165], s[10:11], v[184:185] op_sel_hi:[1,0,1]
	v_pk_fma_f32 v[186:187], v[166:167], s[10:11], v[186:187] op_sel_hi:[1,0,1]
	v_cvt_pk_f32_fp8_e32 v[168:169], v114
	v_cvt_pk_f32_fp8_sdwa v[170:171], v114 src0_sel:WORD_1
	v_pk_fma_f32 v[184:185], v[168:169], s[10:11], v[184:185] op_sel_hi:[1,0,1]
	v_pk_fma_f32 v[186:187], v[170:171], s[10:11], v[186:187] op_sel_hi:[1,0,1]
	v_cvt_pk_f32_fp8_e32 v[172:173], v118
	v_cvt_pk_f32_fp8_sdwa v[174:175], v118 src0_sel:WORD_1
	v_pk_fma_f32 v[184:185], v[172:173], s[10:11], v[184:185] op_sel_hi:[1,0,1]
	v_pk_fma_f32 v[186:187], v[174:175], s[10:11], v[186:187] op_sel_hi:[1,0,1]
	global_store_dwordx4 v158, v[184:187], s[4:5] offset:2048
	v_lshlrev_b32_e32 v188, 16, v62
	v_and_b32_e32 v189, 0xffff0000, v62
	v_lshlrev_b32_e32 v190, 16, v63
	v_and_b32_e32 v191, 0xffff0000, v63
	v_cvt_pk_f32_fp8_e32 v[160:161], v107
	v_cvt_pk_f32_fp8_sdwa v[162:163], v107 src0_sel:WORD_1
	v_pk_fma_f32 v[188:189], v[160:161], s[10:11], v[188:189] op_sel_hi:[1,0,1]
	v_pk_fma_f32 v[190:191], v[162:163], s[10:11], v[190:191] op_sel_hi:[1,0,1]
	v_cvt_pk_f32_fp8_e32 v[164:165], v111
	v_cvt_pk_f32_fp8_sdwa v[166:167], v111 src0_sel:WORD_1
	v_pk_fma_f32 v[188:189], v[164:165], s[10:11], v[188:189] op_sel_hi:[1,0,1]
	v_pk_fma_f32 v[190:191], v[166:167], s[10:11], v[190:191] op_sel_hi:[1,0,1]
	v_cvt_pk_f32_fp8_e32 v[168:169], v115
	v_cvt_pk_f32_fp8_sdwa v[170:171], v115 src0_sel:WORD_1
	v_pk_fma_f32 v[188:189], v[168:169], s[10:11], v[188:189] op_sel_hi:[1,0,1]
	v_pk_fma_f32 v[190:191], v[170:171], s[10:11], v[190:191] op_sel_hi:[1,0,1]
	v_cvt_pk_f32_fp8_e32 v[172:173], v119
	v_cvt_pk_f32_fp8_sdwa v[174:175], v119 src0_sel:WORD_1
	v_pk_fma_f32 v[188:189], v[172:173], s[10:11], v[188:189] op_sel_hi:[1,0,1]
	v_pk_fma_f32 v[190:191], v[174:175], s[10:11], v[190:191] op_sel_hi:[1,0,1]
	global_store_dwordx4 v158, v[188:191], s[4:5] offset:3072
	s_waitcnt vmcnt(36)
; __device__ __forceinline__ float bf_lo(unsigned w) { return __uint_as_float(w << 16); }
; __device__ __forceinline__ float bf_hi(unsigned w) { return __uint_as_float(w & 0xffff0000u); }
; __global__ void __launch_bounds__(512, 2) fwd_kernel(Params p) {
;     ...
;                 for (int k = 0; k < 4; ++k) { const int pos = ts[ee[u][k]] * 256 + rk[u][k]; y[u][k] = *(const u32x4*)(Yb + (size_t)pos * DM + cc[u]); }
; #pragma unroll
;             for (int u = 0; u < UN; ++u) {
;                 f32x4 a[4];
;                 a[0] = (f32x4){bf_lo(xa[u].x), bf_hi(xa[u].x), bf_lo(xa[u].y), bf_hi(xa[u].y)}; a[1] = (f32x4){bf_lo(xa[u].z), bf_hi(xa[u].z), bf_lo(xa[u].w), bf_hi(xa[u].w)};
;                 a[2] = (f32x4){bf_lo(xb[u].x), bf_hi(xb[u].x), bf_lo(xb[u].y), bf_hi(xb[u].y)}; a[3] = (f32x4){bf_lo(xb[u].z), bf_hi(xb[u].z), bf_lo(xb[u].w), bf_hi(xb[u].w)};
; #pragma unroll
;                 for (int k = 0; k < 4; ++k)
; #pragma unroll
;                     for (int q = 0; q < 4; ++q) { const f32x2 lo = __builtin_amdgcn_cvt_pk_f32_fp8((int)y[u][k][q], false), hi = __builtin_amdgcn_cvt_pk_f32_fp8((int)y[u][k][q], true);
;                         a[q].x += lo.x * (1.0f / Y8_SCALE); a[q].y += lo.y * (1.0f / Y8_SCALE); a[q].z += hi.x * (1.0f / Y8_SCALE); a[q].w += hi.y * (1.0f / Y8_SCALE); }
;                 if (it0 + u * NGT < NI) { float* op = p.out + (size_t)mm[u] * DM + cc[u];
; #pragma unroll
;                     for (int q = 0; q < 4; ++q) *(f32x4*)(op + 4 * q) = a[q]; }
	v_lshlrev_b32_e32 v176, 16, v64
	v_and_b32_e32 v177, 0xffff0000, v64
	v_lshlrev_b32_e32 v178, 16, v65
	v_and_b32_e32 v179, 0xffff0000, v65
	v_cvt_pk_f32_fp8_e32 v[160:161], v120
	v_cvt_pk_f32_fp8_sdwa v[162:163], v120 src0_sel:WORD_1
	v_pk_fma_f32 v[176:177], v[160:161], s[10:11], v[176:177] op_sel_hi:[1,0,1]
	v_pk_fma_f32 v[178:179], v[162:163], s[10:11], v[178:179] op_sel_hi:[1,0,1]
	v_cvt_pk_f32_fp8_e32 v[164:165], v124
	v_cvt_pk_f32_fp8_sdwa v[166:167], v124 src0_sel:WORD_1
	v_pk_fma_f32 v[176:177], v[164:165], s[10:11], v[176:177] op_sel_hi:[1,0,1]
	v_pk_fma_f32 v[178:179], v[166:167], s[10:11], v[178:179] op_sel_hi:[1,0,1]
	v_cvt_pk_f32_fp8_e32 v[168:169], v128
	v_cvt_pk_f32_fp8_sdwa v[170:171], v128 src0_sel:WORD_1
	v_pk_fma_f32 v[176:177], v[168:169], s[10:11], v[176:177] op_sel_hi:[1,0,1]
	v_pk_fma_f32 v[178:179], v[170:171], s[10:11], v[178:179] op_sel_hi:[1,0,1]
	v_cvt_pk_f32_fp8_e32 v[172:173], v132
	v_cvt_pk_f32_fp8_sdwa v[174:175], v132 src0_sel:WORD_1
	v_pk_fma_f32 v[176:177], v[172:173], s[10:11], v[176:177] op_sel_hi:[1,0,1]
	v_pk_fma_f32 v[178:179], v[174:175], s[10:11], v[178:179] op_sel_hi:[1,0,1]
	global_store_dwordx4 v159, v[176:179], s[4:5]
	v_lshlrev_b32_e32 v180, 16, v66
	v_and_b32_e32 v181, 0xffff0000, v66
	v_lshlrev_b32_e32 v182, 16, v67
	v_and_b32_e32 v183, 0xffff0000, v67
	v_cvt_pk_f32_fp8_e32 v[160:161], v121
	v_cvt_pk_f32_fp8_sdwa v[162:163], v121 src0_sel:WORD_1
	v_pk_fma_f32 v[180:181], v[160:161], s[10:11], v[180:181] op_sel_hi:[1,0,1]
	v_pk_fma_f32 v[182:183], v[162:163], s[10:11], v[182:183] op_sel_hi:[1,0,1]
	v_cvt_pk_f32_fp8_e32 v[164:165], v125
	v_cvt_pk_f32_fp8_sdwa v[166:167], v125 src0_sel:WORD_1
	v_pk_fma_f32 v[180:181], v[164:165], s[10:11], v[180:181] op_sel_hi:[1,0,1]
	v_pk_fma_f32 v[182:183], v[166:167], s[10:11], v[182:183] op_sel_hi:[1,0,1]
	v_cvt_pk_f32_fp8_e32 v[168:169], v129
	v_cvt_pk_f32_fp8_sdwa v[170:171], v129 src0_sel:WORD_1
	v_pk_fma_f32 v[180:181], v[168:169], s[10:11], v[180:181] op_sel_hi:[1,0,1]
	v_pk_fma_f32 v[182:183], v[170:171], s[10:11], v[182:183] op_sel_hi:[1,0,1]
	v_cvt_pk_f32_fp8_e32 v[172:173], v133
	v_cvt_pk_f32_fp8_sdwa v[174:175], v133 src0_sel:WORD_1
	v_pk_fma_f32 v[180:181], v[172:173], s[10:11], v[180:181] op_sel_hi:[1,0,1]
	v_pk_fma_f32 v[182:183], v[174:175], s[10:11], v[182:183] op_sel_hi:[1,0,1]
	global_store_dwordx4 v159, v[180:183], s[4:5] offset:1024
	v_lshlrev_b32_e32 v184, 16, v68
	v_and_b32_e32 v185, 0xffff0000, v68
	v_lshlrev_b32_e32 v186, 16, v69
	v_and_b32_e32 v187, 0xffff0000, v69
	v_cvt_pk_f32_fp8_e32 v[160:161], v122
	v_cvt_pk_f32_fp8_sdwa v[162:163], v122 src0_sel:WORD_1
	v_pk_fma_f32 v[184:185], v[160:161], s[10:11], v[184:185] op_sel_hi:[1,0,1]
	v_pk_fma_f32 v[186:187], v[162:163], s[10:11], v[186:187] op_sel_hi:[1,0,1]
	v_cvt_pk_f32_fp8_e32 v[164:165], v126
	v_cvt_pk_f32_fp8_sdwa v[166:167], v126 src0_sel:WORD_1
	v_pk_fma_f32 v[184:185], v[164:165], s[10:11], v[184:185] op_sel_hi:[1,0,1]
	v_pk_fma_f32 v[186:187], v[166:167], s[10:11], v[186:187] op_sel_hi:[1,0,1]
	v_cvt_pk_f32_fp8_e32 v[168:169], v130
	v_cvt_pk_f32_fp8_sdwa v[170:171], v130 src0_sel:WORD_1
	v_pk_fma_f32 v[184:185], v[168:169], s[10:11], v[184:185] op_sel_hi:[1,0,1]
	v_pk_fma_f32 v[186:187], v[170:171], s[10:11], v[186:187] op_sel_hi:[1,0,1]
	v_cvt_pk_f32_fp8_e32 v[172:173], v134
	v_cvt_pk_f32_fp8_sdwa v[174:175], v134 src0_sel:WORD_1
	v_pk_fma_f32 v[184:185], v[172:173], s[10:11], v[184:185] op_sel_hi:[1,0,1]
	v_pk_fma_f32 v[186:187], v[174:175], s[10:11], v[186:187] op_sel_hi:[1,0,1]
	global_store_dwordx4 v159, v[184:187], s[4:5] offset:2048
	v_lshlrev_b32_e32 v188, 16, v70
	v_and_b32_e32 v189, 0xffff0000, v70
	v_lshlrev_b32_e32 v190, 16, v71
	v_and_b32_e32 v191, 0xffff0000, v71
	v_cvt_pk_f32_fp8_e32 v[160:161], v123
	v_cvt_pk_f32_fp8_sdwa v[162:163], v123 src0_sel:WORD_1
	v_pk_fma_f32 v[188:189], v[160:161], s[10:11], v[188:189] op_sel_hi:[1,0,1]
	v_pk_fma_f32 v[190:191], v[162:163], s[10:11], v[190:191] op_sel_hi:[1,0,1]
	v_cvt_pk_f32_fp8_e32 v[164:165], v127
	v_cvt_pk_f32_fp8_sdwa v[166:167], v127 src0_sel:WORD_1
	v_pk_fma_f32 v[188:189], v[164:165], s[10:11], v[188:189] op_sel_hi:[1,0,1]
	v_pk_fma_f32 v[190:191], v[166:167], s[10:11], v[190:191] op_sel_hi:[1,0,1]
	v_cvt_pk_f32_fp8_e32 v[168:169], v131
	v_cvt_pk_f32_fp8_sdwa v[170:171], v131 src0_sel:WORD_1
	v_pk_fma_f32 v[188:189], v[168:169], s[10:11], v[188:189] op_sel_hi:[1,0,1]
	v_pk_fma_f32 v[190:191], v[170:171], s[10:11], v[190:191] op_sel_hi:[1,0,1]
	v_cvt_pk_f32_fp8_e32 v[172:173], v135
	v_cvt_pk_f32_fp8_sdwa v[174:175], v135 src0_sel:WORD_1
	v_pk_fma_f32 v[188:189], v[172:173], s[10:11], v[188:189] op_sel_hi:[1,0,1]
	v_pk_fma_f32 v[190:191], v[174:175], s[10:11], v[190:191] op_sel_hi:[1,0,1]
	global_store_dwordx4 v159, v[188:191], s[4:5] offset:3072
	s_waitcnt vmcnt(28)
	v_lshl_add_u32 v200, v8, 2, s23
	v_lshl_add_u32 v201, v9, 2, s23
	v_lshl_add_u32 v202, v10, 2, s23
	v_lshl_add_u32 v203, v11, 2, s23
	v_lshl_add_u32 v204, v12, 2, s23
	v_lshl_add_u32 v205, v13, 2, s23
	v_lshl_add_u32 v206, v14, 2, s23
	v_lshl_add_u32 v207, v15, 2, s23
	v_lshl_add_u32 v208, v16, 2, s23
	v_lshl_add_u32 v209, v17, 2, s23
	v_lshl_add_u32 v210, v18, 2, s23
	v_lshl_add_u32 v211, v19, 2, s23
	v_lshl_add_u32 v212, v20, 2, s23
	v_lshl_add_u32 v213, v21, 2, s23
	v_lshl_add_u32 v214, v22, 2, s23
	v_lshl_add_u32 v215, v23, 2, s23
	ds_read_b32 v136, v200
	ds_read_b32 v137, v201
	ds_read_b32 v138, v202
	ds_read_b32 v139, v203
	ds_read_b32 v140, v204
	ds_read_b32 v141, v205
	ds_read_b32 v142, v206
	ds_read_b32 v143, v207
	ds_read_b32 v144, v208
	ds_read_b32 v145, v209
	ds_read_b32 v146, v210
	ds_read_b32 v147, v211
	ds_read_b32 v148, v212
	ds_read_b32 v149, v213
	ds_read_b32 v150, v214
	ds_read_b32 v151, v215
	v_add_u32_e32 v192, 0x1000, v3
	v_lshl_add_u32 v156, v192, 13, v6
	v_add_u32_e32 v193, 0x1400, v3
	v_lshl_add_u32 v157, v193, 13, v6
	v_add_u32_e32 v194, 0x1800, v3
	v_lshl_add_u32 v158, v194, 13, v6
	v_add_u32_e32 v195, 0x1c00, v3
	v_lshl_add_u32 v159, v195, 13, v6
	s_waitcnt lgkmcnt(12)
; __device__ __forceinline__ float bf_lo(unsigned w) { return __uint_as_float(w << 16); }
; __device__ __forceinline__ float bf_hi(unsigned w) { return __uint_as_float(w & 0xffff0000u); }
; __global__ void __launch_bounds__(512, 2) fwd_kernel(Params p) {
;     ...
;                 for (int k = 0; k < 4; ++k) { const int pos = ts[ee[u][k]] * 256 + rk[u][k]; y[u][k] = *(const u32x4*)(Yb + (size_t)pos * DM + cc[u]); }
; #pragma unroll
;             for (int u = 0; u < UN; ++u) {
;                 f32x4 a[4];
;                 a[0] = (f32x4){bf_lo(xa[u].x), bf_hi(xa[u].x), bf_lo(xa[u].y), bf_hi(xa[u].y)}; a[1] = (f32x4){bf_lo(xa[u].z), bf_hi(xa[u].z), bf_lo(xa[u].w), bf_hi(xa[u].w)};
;                 a[2] = (f32x4){bf_lo(xb[u].x), bf_hi(xb[u].x), bf_lo(xb[u].y), bf_hi(xb[u].y)}; a[3] = (f32x4){bf_lo(xb[u].z), bf_hi(xb[u].z), bf_lo(xb[u].w), bf_hi(xb[u].w)};
; #pragma unroll
;                 for (int k = 0; k < 4; ++k)
; #pragma unroll
;                     for (int q = 0; q < 4; ++q) { const f32x2 lo = __builtin_amdgcn_cvt_pk_f32_fp8((int)y[u][k][q], false), hi = __builtin_amdgcn_cvt_pk_f32_fp8((int)y[u][k][q], true);
;                         a[q].x += lo.x * (1.0f / Y8_SCALE); a[q].y += lo.y * (1.0f / Y8_SCALE); a[q].z += hi.x * (1.0f / Y8_SCALE); a[q].w += hi.y * (1.0f / Y8_SCALE); }
;                 if (it0 + u * NGT < NI) { float* op = p.out + (size_t)mm[u] * DM + cc[u];
; #pragma unroll
;                     for (int q = 0; q < 4; ++q) *(f32x4*)(op + 4 * q) = a[q]; }
	v_lshl_add_u32 v136, v136, 8, v24
	v_lshl_add_u32 v137, v137, 8, v25
	v_lshl_add_u32 v138, v138, 8, v26
	v_lshl_add_u32 v139, v139, 8, v27
	v_lshl_add_u32 v136, v136, 11, v4
	v_lshl_add_u32 v137, v137, 11, v4
	v_lshl_add_u32 v138, v138, 11, v4
	v_lshl_add_u32 v139, v139, 11, v4
	global_load_dword v72, v136, s[6:7]
	global_load_dword v73, v136, s[6:7] offset:256
	global_load_dword v74, v136, s[6:7] offset:512
	global_load_dword v75, v136, s[6:7] offset:768
	global_load_dword v76, v137, s[6:7]
	global_load_dword v77, v137, s[6:7] offset:256
	global_load_dword v78, v137, s[6:7] offset:512
	global_load_dword v79, v137, s[6:7] offset:768
	global_load_dword v80, v138, s[6:7]
	global_load_dword v81, v138, s[6:7] offset:256
	global_load_dword v82, v138, s[6:7] offset:512
	global_load_dword v83, v138, s[6:7] offset:768
	global_load_dword v84, v139, s[6:7]
	global_load_dword v85, v139, s[6:7] offset:256
	global_load_dword v86, v139, s[6:7] offset:512
	global_load_dword v87, v139, s[6:7] offset:768
	s_waitcnt lgkmcnt(8)
	v_lshl_add_u32 v140, v140, 8, v28
	v_lshl_add_u32 v141, v141, 8, v29
	v_lshl_add_u32 v142, v142, 8, v30
	v_lshl_add_u32 v143, v143, 8, v31
	v_lshl_add_u32 v140, v140, 11, v4
	v_lshl_add_u32 v141, v141, 11, v4
	v_lshl_add_u32 v142, v142, 11, v4
	v_lshl_add_u32 v143, v143, 11, v4
	global_load_dword v88, v140, s[6:7]
	global_load_dword v89, v140, s[6:7] offset:256
	global_load_dword v90, v140, s[6:7] offset:512
	global_load_dword v91, v140, s[6:7] offset:768
	global_load_dword v92, v141, s[6:7]
	global_load_dword v93, v141, s[6:7] offset:256
	global_load_dword v94, v141, s[6:7] offset:512
	global_load_dword v95, v141, s[6:7] offset:768
	global_load_dword v96, v142, s[6:7]
	global_load_dword v97, v142, s[6:7] offset:256
	global_load_dword v98, v142, s[6:7] offset:512
	global_load_dword v99, v142, s[6:7] offset:768
	global_load_dword v100, v143, s[6:7]
	global_load_dword v101, v143, s[6:7] offset:256
	global_load_dword v102, v143, s[6:7] offset:512
	global_load_dword v103, v143, s[6:7] offset:768
	s_waitcnt lgkmcnt(4)
	v_lshl_add_u32 v144, v144, 8, v32
	v_lshl_add_u32 v145, v145, 8, v33
	v_lshl_add_u32 v146, v146, 8, v34
	v_lshl_add_u32 v147, v147, 8, v35
	v_lshl_add_u32 v144, v144, 11, v4
	v_lshl_add_u32 v145, v145, 11, v4
	v_lshl_add_u32 v146, v146, 11, v4
	v_lshl_add_u32 v147, v147, 11, v4
	global_load_dword v104, v144, s[6:7]
	global_load_dword v105, v144, s[6:7] offset:256
	global_load_dword v106, v144, s[6:7] offset:512
	global_load_dword v107, v144, s[6:7] offset:768
	global_load_dword v108, v145, s[6:7]
	global_load_dword v109, v145, s[6:7] offset:256
	global_load_dword v110, v145, s[6:7] offset:512
	global_load_dword v111, v145, s[6:7] offset:768
	global_load_dword v112, v146, s[6:7]
	global_load_dword v113, v146, s[6:7] offset:256
	global_load_dword v114, v146, s[6:7] offset:512
	global_load_dword v115, v146, s[6:7] offset:768
	global_load_dword v116, v147, s[6:7]
	global_load_dword v117, v147, s[6:7] offset:256
	global_load_dword v118, v147, s[6:7] offset:512
	global_load_dword v119, v147, s[6:7] offset:768
	s_waitcnt lgkmcnt(0)
	v_lshl_add_u32 v148, v148, 8, v36
	v_lshl_add_u32 v149, v149, 8, v37
	v_lshl_add_u32 v150, v150, 8, v38
	v_lshl_add_u32 v151, v151, 8, v39
	v_lshl_add_u32 v148, v148, 11, v4
	v_lshl_add_u32 v149, v149, 11, v4
	v_lshl_add_u32 v150, v150, 11, v4
	v_lshl_add_u32 v151, v151, 11, v4
	global_load_dword v120, v148, s[6:7]
	global_load_dword v121, v148, s[6:7] offset:256
	global_load_dword v122, v148, s[6:7] offset:512
	global_load_dword v123, v148, s[6:7] offset:768
	global_load_dword v124, v149, s[6:7]
	global_load_dword v125, v149, s[6:7] offset:256
	global_load_dword v126, v149, s[6:7] offset:512
	global_load_dword v127, v149, s[6:7] offset:768
	global_load_dword v128, v150, s[6:7]
	global_load_dword v129, v150, s[6:7] offset:256
	global_load_dword v130, v150, s[6:7] offset:512
	global_load_dword v131, v150, s[6:7] offset:768
	global_load_dword v132, v151, s[6:7]
	global_load_dword v133, v151, s[6:7] offset:256
	global_load_dword v134, v151, s[6:7] offset:512
	global_load_dword v135, v151, s[6:7] offset:768
	s_waitcnt vmcnt(48)
	v_lshlrev_b32_e32 v176, 16, v216
	v_and_b32_e32 v177, 0xffff0000, v216
	v_lshlrev_b32_e32 v178, 16, v217
	v_and_b32_e32 v179, 0xffff0000, v217
	v_cvt_pk_f32_fp8_e32 v[160:161], v72
	v_cvt_pk_f32_fp8_sdwa v[162:163], v72 src0_sel:WORD_1
	v_pk_fma_f32 v[176:177], v[160:161], s[10:11], v[176:177] op_sel_hi:[1,0,1]
	v_pk_fma_f32 v[178:179], v[162:163], s[10:11], v[178:179] op_sel_hi:[1,0,1]
	v_cvt_pk_f32_fp8_e32 v[164:165], v76
	v_cvt_pk_f32_fp8_sdwa v[166:167], v76 src0_sel:WORD_1
	v_pk_fma_f32 v[176:177], v[164:165], s[10:11], v[176:177] op_sel_hi:[1,0,1]
	v_pk_fma_f32 v[178:179], v[166:167], s[10:11], v[178:179] op_sel_hi:[1,0,1]
	v_cvt_pk_f32_fp8_e32 v[168:169], v80
	v_cvt_pk_f32_fp8_sdwa v[170:171], v80 src0_sel:WORD_1
	v_pk_fma_f32 v[176:177], v[168:169], s[10:11], v[176:177] op_sel_hi:[1,0,1]
	v_pk_fma_f32 v[178:179], v[170:171], s[10:11], v[178:179] op_sel_hi:[1,0,1]
	v_cvt_pk_f32_fp8_e32 v[172:173], v84
	v_cvt_pk_f32_fp8_sdwa v[174:175], v84 src0_sel:WORD_1
	v_pk_fma_f32 v[176:177], v[172:173], s[10:11], v[176:177] op_sel_hi:[1,0,1]
	v_pk_fma_f32 v[178:179], v[174:175], s[10:11], v[178:179] op_sel_hi:[1,0,1]
	global_store_dwordx4 v156, v[176:179], s[4:5]
	v_lshlrev_b32_e32 v180, 16, v218
	v_and_b32_e32 v181, 0xffff0000, v218
	v_lshlrev_b32_e32 v182, 16, v219
	v_and_b32_e32 v183, 0xffff0000, v219
	v_cvt_pk_f32_fp8_e32 v[160:161], v73
	v_cvt_pk_f32_fp8_sdwa v[162:163], v73 src0_sel:WORD_1
	v_pk_fma_f32 v[180:181], v[160:161], s[10:11], v[180:181] op_sel_hi:[1,0,1]
; __device__ __forceinline__ float bf_lo(unsigned w) { return __uint_as_float(w << 16); }
; __device__ __forceinline__ float bf_hi(unsigned w) { return __uint_as_float(w & 0xffff0000u); }
; __global__ void __launch_bounds__(512, 2) fwd_kernel(Params p) {
;     ...
;         for (int it0 = GT(); it0 < NI; it0 += UN * NGT) {
;             int mm[UN], cc[UN], ee[UN][4], rk[UN][4]; u32x4 xa[UN], xb[UN], y[UN][4];
; #pragma unroll
;             for (int u = 0; u < UN; ++u) { const int it = it0 + u * NGT < NI ? it0 + u * NGT : it0; mm[u] = it >> 7; cc[u] = (it & 127) * 16;
;                 const i32x4 e4 = *(const i32x4*)(tok_e + mm[u] * 4), r4 = *(const i32x4*)(tok_rank + mm[u] * 4);
; #pragma unroll
;                 for (int k = 0; k < 4; ++k) { ee[u][k] = e4[k]; rk[u][k] = r4[k]; }
;                 const bf16_t* xp = X1 + (size_t)mm[u] * DM + cc[u]; xa[u] = *(const u32x4*)xp; xb[u] = *(const u32x4*)(xp + 8); }
; #pragma unroll
;             for (int u = 0; u < UN; ++u)
; #pragma unroll
;                 for (int k = 0; k < 4; ++k) { const int pos = ts[ee[u][k]] * 256 + rk[u][k]; y[u][k] = *(const u32x4*)(Yb + (size_t)pos * DM + cc[u]); }
; #pragma unroll
;             for (int u = 0; u < UN; ++u) {
;                 f32x4 a[4];
;                 a[0] = (f32x4){bf_lo(xa[u].x), bf_hi(xa[u].x), bf_lo(xa[u].y), bf_hi(xa[u].y)}; a[1] = (f32x4){bf_lo(xa[u].z), bf_hi(xa[u].z), bf_lo(xa[u].w), bf_hi(xa[u].w)};
;                 a[2] = (f32x4){bf_lo(xb[u].x), bf_hi(xb[u].x), bf_lo(xb[u].y), bf_hi(xb[u].y)}; a[3] = (f32x4){bf_lo(xb[u].z), bf_hi(xb[u].z), bf_lo(xb[u].w), bf_hi(xb[u].w)};
; #pragma unroll
;                 for (int k = 0; k < 4; ++k)
; #pragma unroll
;                     for (int q = 0; q < 4; ++q) { const f32x2 lo = __builtin_amdgcn_cvt_pk_f32_fp8((int)y[u][k][q], false), hi = __builtin_amdgcn_cvt_pk_f32_fp8((int)y[u][k][q], true);
;                         a[q].x += lo.x * (1.0f / Y8_SCALE); a[q].y += lo.y * (1.0f / Y8_SCALE); a[q].z += hi.x * (1.0f / Y8_SCALE); a[q].w += hi.y * (1.0f / Y8_SCALE); }
;                 if (it0 + u * NGT < NI) { float* op = p.out + (size_t)mm[u] * DM + cc[u];
; #pragma unroll
;                     for (int q = 0; q < 4; ++q) *(f32x4*)(op + 4 * q) = a[q]; }
	v_pk_fma_f32 v[182:183], v[162:163], s[10:11], v[182:183] op_sel_hi:[1,0,1]
	v_cvt_pk_f32_fp8_e32 v[164:165], v77
	v_cvt_pk_f32_fp8_sdwa v[166:167], v77 src0_sel:WORD_1
	v_pk_fma_f32 v[180:181], v[164:165], s[10:11], v[180:181] op_sel_hi:[1,0,1]
	v_pk_fma_f32 v[182:183], v[166:167], s[10:11], v[182:183] op_sel_hi:[1,0,1]
	v_cvt_pk_f32_fp8_e32 v[168:169], v81
	v_cvt_pk_f32_fp8_sdwa v[170:171], v81 src0_sel:WORD_1
	v_pk_fma_f32 v[180:181], v[168:169], s[10:11], v[180:181] op_sel_hi:[1,0,1]
	v_pk_fma_f32 v[182:183], v[170:171], s[10:11], v[182:183] op_sel_hi:[1,0,1]
	v_cvt_pk_f32_fp8_e32 v[172:173], v85
	v_cvt_pk_f32_fp8_sdwa v[174:175], v85 src0_sel:WORD_1
	v_pk_fma_f32 v[180:181], v[172:173], s[10:11], v[180:181] op_sel_hi:[1,0,1]
	v_pk_fma_f32 v[182:183], v[174:175], s[10:11], v[182:183] op_sel_hi:[1,0,1]
	global_store_dwordx4 v156, v[180:183], s[4:5] offset:1024
	v_lshlrev_b32_e32 v184, 16, v220
	v_and_b32_e32 v185, 0xffff0000, v220
	v_lshlrev_b32_e32 v186, 16, v221
	v_and_b32_e32 v187, 0xffff0000, v221
	v_cvt_pk_f32_fp8_e32 v[160:161], v74
	v_cvt_pk_f32_fp8_sdwa v[162:163], v74 src0_sel:WORD_1
	v_pk_fma_f32 v[184:185], v[160:161], s[10:11], v[184:185] op_sel_hi:[1,0,1]
	v_pk_fma_f32 v[186:187], v[162:163], s[10:11], v[186:187] op_sel_hi:[1,0,1]
	v_cvt_pk_f32_fp8_e32 v[164:165], v78
	v_cvt_pk_f32_fp8_sdwa v[166:167], v78 src0_sel:WORD_1
	v_pk_fma_f32 v[184:185], v[164:165], s[10:11], v[184:185] op_sel_hi:[1,0,1]
	v_pk_fma_f32 v[186:187], v[166:167], s[10:11], v[186:187] op_sel_hi:[1,0,1]
	v_cvt_pk_f32_fp8_e32 v[168:169], v82
	v_cvt_pk_f32_fp8_sdwa v[170:171], v82 src0_sel:WORD_1
	v_pk_fma_f32 v[184:185], v[168:169], s[10:11], v[184:185] op_sel_hi:[1,0,1]
	v_pk_fma_f32 v[186:187], v[170:171], s[10:11], v[186:187] op_sel_hi:[1,0,1]
	v_cvt_pk_f32_fp8_e32 v[172:173], v86
	v_cvt_pk_f32_fp8_sdwa v[174:175], v86 src0_sel:WORD_1
	v_pk_fma_f32 v[184:185], v[172:173], s[10:11], v[184:185] op_sel_hi:[1,0,1]
	v_pk_fma_f32 v[186:187], v[174:175], s[10:11], v[186:187] op_sel_hi:[1,0,1]
	global_store_dwordx4 v156, v[184:187], s[4:5] offset:2048
	v_lshlrev_b32_e32 v188, 16, v222
	v_and_b32_e32 v189, 0xffff0000, v222
	v_lshlrev_b32_e32 v190, 16, v223
	v_and_b32_e32 v191, 0xffff0000, v223
	v_cvt_pk_f32_fp8_e32 v[160:161], v75
	v_cvt_pk_f32_fp8_sdwa v[162:163], v75 src0_sel:WORD_1
	v_pk_fma_f32 v[188:189], v[160:161], s[10:11], v[188:189] op_sel_hi:[1,0,1]
	v_pk_fma_f32 v[190:191], v[162:163], s[10:11], v[190:191] op_sel_hi:[1,0,1]
	v_cvt_pk_f32_fp8_e32 v[164:165], v79
	v_cvt_pk_f32_fp8_sdwa v[166:167], v79 src0_sel:WORD_1
	v_pk_fma_f32 v[188:189], v[164:165], s[10:11], v[188:189] op_sel_hi:[1,0,1]
	v_pk_fma_f32 v[190:191], v[166:167], s[10:11], v[190:191] op_sel_hi:[1,0,1]
	v_cvt_pk_f32_fp8_e32 v[168:169], v83
	v_cvt_pk_f32_fp8_sdwa v[170:171], v83 src0_sel:WORD_1
	v_pk_fma_f32 v[188:189], v[168:169], s[10:11], v[188:189] op_sel_hi:[1,0,1]
	v_pk_fma_f32 v[190:191], v[170:171], s[10:11], v[190:191] op_sel_hi:[1,0,1]
	v_cvt_pk_f32_fp8_e32 v[172:173], v87
	v_cvt_pk_f32_fp8_sdwa v[174:175], v87 src0_sel:WORD_1
	v_pk_fma_f32 v[188:189], v[172:173], s[10:11], v[188:189] op_sel_hi:[1,0,1]
	v_pk_fma_f32 v[190:191], v[174:175], s[10:11], v[190:191] op_sel_hi:[1,0,1]
	global_store_dwordx4 v156, v[188:191], s[4:5] offset:3072
	v_add_u32_e32 v192, 0x2000, v3
	v_lshlrev_b32_e32 v196, 4, v192
	v_add_u32_e32 v193, 0x2400, v3
	v_lshlrev_b32_e32 v197, 4, v193
	v_add_u32_e32 v194, 0x2800, v3
	v_lshlrev_b32_e32 v198, 4, v194
	v_add_u32_e32 v195, 0x2c00, v3
	v_lshlrev_b32_e32 v199, 4, v195
	global_load_dwordx4 v[8:11], v196, s[16:17]
	global_load_dwordx4 v[12:15], v197, s[16:17]
	global_load_dwordx4 v[16:19], v198, s[16:17]
	global_load_dwordx4 v[20:23], v199, s[16:17]
	global_load_dwordx4 v[24:27], v196, s[18:19]
	global_load_dwordx4 v[28:31], v197, s[18:19]
	global_load_dwordx4 v[32:35], v198, s[18:19]
	global_load_dwordx4 v[36:39], v199, s[18:19]
	v_lshl_add_u32 v196, v192, 12, v5
	global_load_dwordx2 v[40:41], v196, s[14:15]
	global_load_dwordx2 v[42:43], v196, s[14:15] offset:512
	global_load_dwordx2 v[44:45], v196, s[14:15] offset:1024
	global_load_dwordx2 v[46:47], v196, s[14:15] offset:1536
	v_lshl_add_u32 v197, v193, 12, v5
	global_load_dwordx2 v[48:49], v197, s[14:15]
	global_load_dwordx2 v[50:51], v197, s[14:15] offset:512
	global_load_dwordx2 v[52:53], v197, s[14:15] offset:1024
	global_load_dwordx2 v[54:55], v197, s[14:15] offset:1536
	v_lshl_add_u32 v198, v194, 12, v5
	global_load_dwordx2 v[56:57], v198, s[14:15]
	global_load_dwordx2 v[58:59], v198, s[14:15] offset:512
	global_load_dwordx2 v[60:61], v198, s[14:15] offset:1024
	global_load_dwordx2 v[62:63], v198, s[14:15] offset:1536
	v_lshl_add_u32 v199, v195, 12, v5
	global_load_dwordx2 v[64:65], v199, s[14:15]
	global_load_dwordx2 v[66:67], v199, s[14:15] offset:512
	global_load_dwordx2 v[68:69], v199, s[14:15] offset:1024
	global_load_dwordx2 v[70:71], v199, s[14:15] offset:1536
	s_waitcnt vmcnt(60)
; __device__ __forceinline__ float bf_lo(unsigned w) { return __uint_as_float(w << 16); }
; __device__ __forceinline__ float bf_hi(unsigned w) { return __uint_as_float(w & 0xffff0000u); }
; __global__ void __launch_bounds__(512, 2) fwd_kernel(Params p) {
;     ...
;             for (int u = 0; u < UN; ++u) {
;                 f32x4 a[4];
;                 a[0] = (f32x4){bf_lo(xa[u].x), bf_hi(xa[u].x), bf_lo(xa[u].y), bf_hi(xa[u].y)}; a[1] = (f32x4){bf_lo(xa[u].z), bf_hi(xa[u].z), bf_lo(xa[u].w), bf_hi(xa[u].w)};
;                 a[2] = (f32x4){bf_lo(xb[u].x), bf_hi(xb[u].x), bf_lo(xb[u].y), bf_hi(xb[u].y)}; a[3] = (f32x4){bf_lo(xb[u].z), bf_hi(xb[u].z), bf_lo(xb[u].w), bf_hi(xb[u].w)};
; #pragma unroll
;                 for (int k = 0; k < 4; ++k)
; #pragma unroll
;                     for (int q = 0; q < 4; ++q) { const f32x2 lo = __builtin_amdgcn_cvt_pk_f32_fp8((int)y[u][k][q], false), hi = __builtin_amdgcn_cvt_pk_f32_fp8((int)y[u][k][q], true);
;                         a[q].x += lo.x * (1.0f / Y8_SCALE); a[q].y += lo.y * (1.0f / Y8_SCALE); a[q].z += hi.x * (1.0f / Y8_SCALE); a[q].w += hi.y * (1.0f / Y8_SCALE); }
;                 if (it0 + u * NGT < NI) { float* op = p.out + (size_t)mm[u] * DM + cc[u];
; #pragma unroll
;                     for (int q = 0; q < 4; ++q) *(f32x4*)(op + 4 * q) = a[q]; }
	v_lshlrev_b32_e32 v176, 16, v224
	v_and_b32_e32 v177, 0xffff0000, v224
	v_lshlrev_b32_e32 v178, 16, v225
	v_and_b32_e32 v179, 0xffff0000, v225
	v_cvt_pk_f32_fp8_e32 v[160:161], v88
	v_cvt_pk_f32_fp8_sdwa v[162:163], v88 src0_sel:WORD_1
	v_pk_fma_f32 v[176:177], v[160:161], s[10:11], v[176:177] op_sel_hi:[1,0,1]
	v_pk_fma_f32 v[178:179], v[162:163], s[10:11], v[178:179] op_sel_hi:[1,0,1]
	v_cvt_pk_f32_fp8_e32 v[164:165], v92
	v_cvt_pk_f32_fp8_sdwa v[166:167], v92 src0_sel:WORD_1
	v_pk_fma_f32 v[176:177], v[164:165], s[10:11], v[176:177] op_sel_hi:[1,0,1]
	v_pk_fma_f32 v[178:179], v[166:167], s[10:11], v[178:179] op_sel_hi:[1,0,1]
	v_cvt_pk_f32_fp8_e32 v[168:169], v96
	v_cvt_pk_f32_fp8_sdwa v[170:171], v96 src0_sel:WORD_1
	v_pk_fma_f32 v[176:177], v[168:169], s[10:11], v[176:177] op_sel_hi:[1,0,1]
	v_pk_fma_f32 v[178:179], v[170:171], s[10:11], v[178:179] op_sel_hi:[1,0,1]
	v_cvt_pk_f32_fp8_e32 v[172:173], v100
	v_cvt_pk_f32_fp8_sdwa v[174:175], v100 src0_sel:WORD_1
	v_pk_fma_f32 v[176:177], v[172:173], s[10:11], v[176:177] op_sel_hi:[1,0,1]
	v_pk_fma_f32 v[178:179], v[174:175], s[10:11], v[178:179] op_sel_hi:[1,0,1]
	global_store_dwordx4 v157, v[176:179], s[4:5]
	v_lshlrev_b32_e32 v180, 16, v226
	v_and_b32_e32 v181, 0xffff0000, v226
	v_lshlrev_b32_e32 v182, 16, v227
	v_and_b32_e32 v183, 0xffff0000, v227
	v_cvt_pk_f32_fp8_e32 v[160:161], v89
	v_cvt_pk_f32_fp8_sdwa v[162:163], v89 src0_sel:WORD_1
	v_pk_fma_f32 v[180:181], v[160:161], s[10:11], v[180:181] op_sel_hi:[1,0,1]
	v_pk_fma_f32 v[182:183], v[162:163], s[10:11], v[182:183] op_sel_hi:[1,0,1]
	v_cvt_pk_f32_fp8_e32 v[164:165], v93
	v_cvt_pk_f32_fp8_sdwa v[166:167], v93 src0_sel:WORD_1
	v_pk_fma_f32 v[180:181], v[164:165], s[10:11], v[180:181] op_sel_hi:[1,0,1]
	v_pk_fma_f32 v[182:183], v[166:167], s[10:11], v[182:183] op_sel_hi:[1,0,1]
	v_cvt_pk_f32_fp8_e32 v[168:169], v97
	v_cvt_pk_f32_fp8_sdwa v[170:171], v97 src0_sel:WORD_1
	v_pk_fma_f32 v[180:181], v[168:169], s[10:11], v[180:181] op_sel_hi:[1,0,1]
	v_pk_fma_f32 v[182:183], v[170:171], s[10:11], v[182:183] op_sel_hi:[1,0,1]
	v_cvt_pk_f32_fp8_e32 v[172:173], v101
	v_cvt_pk_f32_fp8_sdwa v[174:175], v101 src0_sel:WORD_1
	v_pk_fma_f32 v[180:181], v[172:173], s[10:11], v[180:181] op_sel_hi:[1,0,1]
	v_pk_fma_f32 v[182:183], v[174:175], s[10:11], v[182:183] op_sel_hi:[1,0,1]
	global_store_dwordx4 v157, v[180:183], s[4:5] offset:1024
	v_lshlrev_b32_e32 v184, 16, v228
	v_and_b32_e32 v185, 0xffff0000, v228
	v_lshlrev_b32_e32 v186, 16, v229
	v_and_b32_e32 v187, 0xffff0000, v229
	v_cvt_pk_f32_fp8_e32 v[160:161], v90
	v_cvt_pk_f32_fp8_sdwa v[162:163], v90 src0_sel:WORD_1
	v_pk_fma_f32 v[184:185], v[160:161], s[10:11], v[184:185] op_sel_hi:[1,0,1]
	v_pk_fma_f32 v[186:187], v[162:163], s[10:11], v[186:187] op_sel_hi:[1,0,1]
	v_cvt_pk_f32_fp8_e32 v[164:165], v94
	v_cvt_pk_f32_fp8_sdwa v[166:167], v94 src0_sel:WORD_1
	v_pk_fma_f32 v[184:185], v[164:165], s[10:11], v[184:185] op_sel_hi:[1,0,1]
	v_pk_fma_f32 v[186:187], v[166:167], s[10:11], v[186:187] op_sel_hi:[1,0,1]
	v_cvt_pk_f32_fp8_e32 v[168:169], v98
	v_cvt_pk_f32_fp8_sdwa v[170:171], v98 src0_sel:WORD_1
	v_pk_fma_f32 v[184:185], v[168:169], s[10:11], v[184:185] op_sel_hi:[1,0,1]
	v_pk_fma_f32 v[186:187], v[170:171], s[10:11], v[186:187] op_sel_hi:[1,0,1]
	v_cvt_pk_f32_fp8_e32 v[172:173], v102
	v_cvt_pk_f32_fp8_sdwa v[174:175], v102 src0_sel:WORD_1
	v_pk_fma_f32 v[184:185], v[172:173], s[10:11], v[184:185] op_sel_hi:[1,0,1]
	v_pk_fma_f32 v[186:187], v[174:175], s[10:11], v[186:187] op_sel_hi:[1,0,1]
	global_store_dwordx4 v157, v[184:187], s[4:5] offset:2048
	v_lshlrev_b32_e32 v188, 16, v230
	v_and_b32_e32 v189, 0xffff0000, v230
	v_lshlrev_b32_e32 v190, 16, v231
	v_and_b32_e32 v191, 0xffff0000, v231
	v_cvt_pk_f32_fp8_e32 v[160:161], v91
	v_cvt_pk_f32_fp8_sdwa v[162:163], v91 src0_sel:WORD_1
	v_pk_fma_f32 v[188:189], v[160:161], s[10:11], v[188:189] op_sel_hi:[1,0,1]
	v_pk_fma_f32 v[190:191], v[162:163], s[10:11], v[190:191] op_sel_hi:[1,0,1]
	v_cvt_pk_f32_fp8_e32 v[164:165], v95
	v_cvt_pk_f32_fp8_sdwa v[166:167], v95 src0_sel:WORD_1
	v_pk_fma_f32 v[188:189], v[164:165], s[10:11], v[188:189] op_sel_hi:[1,0,1]
	v_pk_fma_f32 v[190:191], v[166:167], s[10:11], v[190:191] op_sel_hi:[1,0,1]
	v_cvt_pk_f32_fp8_e32 v[168:169], v99
	v_cvt_pk_f32_fp8_sdwa v[170:171], v99 src0_sel:WORD_1
	v_pk_fma_f32 v[188:189], v[168:169], s[10:11], v[188:189] op_sel_hi:[1,0,1]
	v_pk_fma_f32 v[190:191], v[170:171], s[10:11], v[190:191] op_sel_hi:[1,0,1]
	v_cvt_pk_f32_fp8_e32 v[172:173], v103
	v_cvt_pk_f32_fp8_sdwa v[174:175], v103 src0_sel:WORD_1
	v_pk_fma_f32 v[188:189], v[172:173], s[10:11], v[188:189] op_sel_hi:[1,0,1]
	v_pk_fma_f32 v[190:191], v[174:175], s[10:11], v[190:191] op_sel_hi:[1,0,1]
	global_store_dwordx4 v157, v[188:191], s[4:5] offset:3072
	s_waitcnt vmcnt(48)
; __device__ __forceinline__ float bf_lo(unsigned w) { return __uint_as_float(w << 16); }
; __device__ __forceinline__ float bf_hi(unsigned w) { return __uint_as_float(w & 0xffff0000u); }
; __global__ void __launch_bounds__(512, 2) fwd_kernel(Params p) {
;     ...
;             for (int u = 0; u < UN; ++u) {
;                 f32x4 a[4];
;                 a[0] = (f32x4){bf_lo(xa[u].x), bf_hi(xa[u].x), bf_lo(xa[u].y), bf_hi(xa[u].y)}; a[1] = (f32x4){bf_lo(xa[u].z), bf_hi(xa[u].z), bf_lo(xa[u].w), bf_hi(xa[u].w)};
;                 a[2] = (f32x4){bf_lo(xb[u].x), bf_hi(xb[u].x), bf_lo(xb[u].y), bf_hi(xb[u].y)}; a[3] = (f32x4){bf_lo(xb[u].z), bf_hi(xb[u].z), bf_lo(xb[u].w), bf_hi(xb[u].w)};
; #pragma unroll
;                 for (int k = 0; k < 4; ++k)
; #pragma unroll
;                     for (int q = 0; q < 4; ++q) { const f32x2 lo = __builtin_amdgcn_cvt_pk_f32_fp8((int)y[u][k][q], false), hi = __builtin_amdgcn_cvt_pk_f32_fp8((int)y[u][k][q], true);
;                         a[q].x += lo.x * (1.0f / Y8_SCALE); a[q].y += lo.y * (1.0f / Y8_SCALE); a[q].z += hi.x * (1.0f / Y8_SCALE); a[q].w += hi.y * (1.0f / Y8_SCALE); }
;                 if (it0 + u * NGT < NI) { float* op = p.out + (size_t)mm[u] * DM + cc[u];
; #pragma unroll
;                     for (int q = 0; q < 4; ++q) *(f32x4*)(op + 4 * q) = a[q]; }
	v_lshlrev_b32_e32 v176, 16, v232
	v_and_b32_e32 v177, 0xffff0000, v232
	v_lshlrev_b32_e32 v178, 16, v233
	v_and_b32_e32 v179, 0xffff0000, v233
	v_cvt_pk_f32_fp8_e32 v[160:161], v104
	v_cvt_pk_f32_fp8_sdwa v[162:163], v104 src0_sel:WORD_1
	v_pk_fma_f32 v[176:177], v[160:161], s[10:11], v[176:177] op_sel_hi:[1,0,1]
	v_pk_fma_f32 v[178:179], v[162:163], s[10:11], v[178:179] op_sel_hi:[1,0,1]
	v_cvt_pk_f32_fp8_e32 v[164:165], v108
	v_cvt_pk_f32_fp8_sdwa v[166:167], v108 src0_sel:WORD_1
	v_pk_fma_f32 v[176:177], v[164:165], s[10:11], v[176:177] op_sel_hi:[1,0,1]
	v_pk_fma_f32 v[178:179], v[166:167], s[10:11], v[178:179] op_sel_hi:[1,0,1]
	v_cvt_pk_f32_fp8_e32 v[168:169], v112
	v_cvt_pk_f32_fp8_sdwa v[170:171], v112 src0_sel:WORD_1
	v_pk_fma_f32 v[176:177], v[168:169], s[10:11], v[176:177] op_sel_hi:[1,0,1]
	v_pk_fma_f32 v[178:179], v[170:171], s[10:11], v[178:179] op_sel_hi:[1,0,1]
	v_cvt_pk_f32_fp8_e32 v[172:173], v116
	v_cvt_pk_f32_fp8_sdwa v[174:175], v116 src0_sel:WORD_1
	v_pk_fma_f32 v[176:177], v[172:173], s[10:11], v[176:177] op_sel_hi:[1,0,1]
	v_pk_fma_f32 v[178:179], v[174:175], s[10:11], v[178:179] op_sel_hi:[1,0,1]
	global_store_dwordx4 v158, v[176:179], s[4:5]
	v_lshlrev_b32_e32 v180, 16, v234
	v_and_b32_e32 v181, 0xffff0000, v234
	v_lshlrev_b32_e32 v182, 16, v235
	v_and_b32_e32 v183, 0xffff0000, v235
	v_cvt_pk_f32_fp8_e32 v[160:161], v105
	v_cvt_pk_f32_fp8_sdwa v[162:163], v105 src0_sel:WORD_1
	v_pk_fma_f32 v[180:181], v[160:161], s[10:11], v[180:181] op_sel_hi:[1,0,1]
	v_pk_fma_f32 v[182:183], v[162:163], s[10:11], v[182:183] op_sel_hi:[1,0,1]
	v_cvt_pk_f32_fp8_e32 v[164:165], v109
	v_cvt_pk_f32_fp8_sdwa v[166:167], v109 src0_sel:WORD_1
	v_pk_fma_f32 v[180:181], v[164:165], s[10:11], v[180:181] op_sel_hi:[1,0,1]
	v_pk_fma_f32 v[182:183], v[166:167], s[10:11], v[182:183] op_sel_hi:[1,0,1]
	v_cvt_pk_f32_fp8_e32 v[168:169], v113
	v_cvt_pk_f32_fp8_sdwa v[170:171], v113 src0_sel:WORD_1
	v_pk_fma_f32 v[180:181], v[168:169], s[10:11], v[180:181] op_sel_hi:[1,0,1]
	v_pk_fma_f32 v[182:183], v[170:171], s[10:11], v[182:183] op_sel_hi:[1,0,1]
	v_cvt_pk_f32_fp8_e32 v[172:173], v117
	v_cvt_pk_f32_fp8_sdwa v[174:175], v117 src0_sel:WORD_1
	v_pk_fma_f32 v[180:181], v[172:173], s[10:11], v[180:181] op_sel_hi:[1,0,1]
	v_pk_fma_f32 v[182:183], v[174:175], s[10:11], v[182:183] op_sel_hi:[1,0,1]
	global_store_dwordx4 v158, v[180:183], s[4:5] offset:1024
	v_lshlrev_b32_e32 v184, 16, v236
	v_and_b32_e32 v185, 0xffff0000, v236
	v_lshlrev_b32_e32 v186, 16, v237
	v_and_b32_e32 v187, 0xffff0000, v237
	v_cvt_pk_f32_fp8_e32 v[160:161], v106
	v_cvt_pk_f32_fp8_sdwa v[162:163], v106 src0_sel:WORD_1
	v_pk_fma_f32 v[184:185], v[160:161], s[10:11], v[184:185] op_sel_hi:[1,0,1]
	v_pk_fma_f32 v[186:187], v[162:163], s[10:11], v[186:187] op_sel_hi:[1,0,1]
	v_cvt_pk_f32_fp8_e32 v[164:165], v110
	v_cvt_pk_f32_fp8_sdwa v[166:167], v110 src0_sel:WORD_1
	v_pk_fma_f32 v[184:185], v[164:165], s[10:11], v[184:185] op_sel_hi:[1,0,1]
	v_pk_fma_f32 v[186:187], v[166:167], s[10:11], v[186:187] op_sel_hi:[1,0,1]
	v_cvt_pk_f32_fp8_e32 v[168:169], v114
	v_cvt_pk_f32_fp8_sdwa v[170:171], v114 src0_sel:WORD_1
	v_pk_fma_f32 v[184:185], v[168:169], s[10:11], v[184:185] op_sel_hi:[1,0,1]
	v_pk_fma_f32 v[186:187], v[170:171], s[10:11], v[186:187] op_sel_hi:[1,0,1]
	v_cvt_pk_f32_fp8_e32 v[172:173], v118
	v_cvt_pk_f32_fp8_sdwa v[174:175], v118 src0_sel:WORD_1
	v_pk_fma_f32 v[184:185], v[172:173], s[10:11], v[184:185] op_sel_hi:[1,0,1]
	v_pk_fma_f32 v[186:187], v[174:175], s[10:11], v[186:187] op_sel_hi:[1,0,1]
	global_store_dwordx4 v158, v[184:187], s[4:5] offset:2048
	v_lshlrev_b32_e32 v188, 16, v238
	v_and_b32_e32 v189, 0xffff0000, v238
	v_lshlrev_b32_e32 v190, 16, v239
	v_and_b32_e32 v191, 0xffff0000, v239
	v_cvt_pk_f32_fp8_e32 v[160:161], v107
	v_cvt_pk_f32_fp8_sdwa v[162:163], v107 src0_sel:WORD_1
	v_pk_fma_f32 v[188:189], v[160:161], s[10:11], v[188:189] op_sel_hi:[1,0,1]
	v_pk_fma_f32 v[190:191], v[162:163], s[10:11], v[190:191] op_sel_hi:[1,0,1]
	v_cvt_pk_f32_fp8_e32 v[164:165], v111
	v_cvt_pk_f32_fp8_sdwa v[166:167], v111 src0_sel:WORD_1
	v_pk_fma_f32 v[188:189], v[164:165], s[10:11], v[188:189] op_sel_hi:[1,0,1]
	v_pk_fma_f32 v[190:191], v[166:167], s[10:11], v[190:191] op_sel_hi:[1,0,1]
	v_cvt_pk_f32_fp8_e32 v[168:169], v115
	v_cvt_pk_f32_fp8_sdwa v[170:171], v115 src0_sel:WORD_1
	v_pk_fma_f32 v[188:189], v[168:169], s[10:11], v[188:189] op_sel_hi:[1,0,1]
	v_pk_fma_f32 v[190:191], v[170:171], s[10:11], v[190:191] op_sel_hi:[1,0,1]
	v_cvt_pk_f32_fp8_e32 v[172:173], v119
	v_cvt_pk_f32_fp8_sdwa v[174:175], v119 src0_sel:WORD_1
	v_pk_fma_f32 v[188:189], v[172:173], s[10:11], v[188:189] op_sel_hi:[1,0,1]
	v_pk_fma_f32 v[190:191], v[174:175], s[10:11], v[190:191] op_sel_hi:[1,0,1]
	global_store_dwordx4 v158, v[188:191], s[4:5] offset:3072
	s_waitcnt vmcnt(36)
; __device__ __forceinline__ float bf_lo(unsigned w) { return __uint_as_float(w << 16); }
; __device__ __forceinline__ float bf_hi(unsigned w) { return __uint_as_float(w & 0xffff0000u); }
; __global__ void __launch_bounds__(512, 2) fwd_kernel(Params p) {
;     ...
;             for (int u = 0; u < UN; ++u)
; #pragma unroll
;                 for (int k = 0; k < 4; ++k) { const int pos = ts[ee[u][k]] * 256 + rk[u][k]; y[u][k] = *(const u32x4*)(Yb + (size_t)pos * DM + cc[u]); }
; #pragma unroll
;             for (int u = 0; u < UN; ++u) {
;                 f32x4 a[4];
;                 a[0] = (f32x4){bf_lo(xa[u].x), bf_hi(xa[u].x), bf_lo(xa[u].y), bf_hi(xa[u].y)}; a[1] = (f32x4){bf_lo(xa[u].z), bf_hi(xa[u].z), bf_lo(xa[u].w), bf_hi(xa[u].w)};
;                 a[2] = (f32x4){bf_lo(xb[u].x), bf_hi(xb[u].x), bf_lo(xb[u].y), bf_hi(xb[u].y)}; a[3] = (f32x4){bf_lo(xb[u].z), bf_hi(xb[u].z), bf_lo(xb[u].w), bf_hi(xb[u].w)};
; #pragma unroll
;                 for (int k = 0; k < 4; ++k)
; #pragma unroll
;                     for (int q = 0; q < 4; ++q) { const f32x2 lo = __builtin_amdgcn_cvt_pk_f32_fp8((int)y[u][k][q], false), hi = __builtin_amdgcn_cvt_pk_f32_fp8((int)y[u][k][q], true);
;                         a[q].x += lo.x * (1.0f / Y8_SCALE); a[q].y += lo.y * (1.0f / Y8_SCALE); a[q].z += hi.x * (1.0f / Y8_SCALE); a[q].w += hi.y * (1.0f / Y8_SCALE); }
;                 if (it0 + u * NGT < NI) { float* op = p.out + (size_t)mm[u] * DM + cc[u];
; #pragma unroll
;                     for (int q = 0; q < 4; ++q) *(f32x4*)(op + 4 * q) = a[q]; }
	v_lshlrev_b32_e32 v176, 16, v240
	v_and_b32_e32 v177, 0xffff0000, v240
	v_lshlrev_b32_e32 v178, 16, v241
	v_and_b32_e32 v179, 0xffff0000, v241
	v_cvt_pk_f32_fp8_e32 v[160:161], v120
	v_cvt_pk_f32_fp8_sdwa v[162:163], v120 src0_sel:WORD_1
	v_pk_fma_f32 v[176:177], v[160:161], s[10:11], v[176:177] op_sel_hi:[1,0,1]
	v_pk_fma_f32 v[178:179], v[162:163], s[10:11], v[178:179] op_sel_hi:[1,0,1]
	v_cvt_pk_f32_fp8_e32 v[164:165], v124
	v_cvt_pk_f32_fp8_sdwa v[166:167], v124 src0_sel:WORD_1
	v_pk_fma_f32 v[176:177], v[164:165], s[10:11], v[176:177] op_sel_hi:[1,0,1]
	v_pk_fma_f32 v[178:179], v[166:167], s[10:11], v[178:179] op_sel_hi:[1,0,1]
	v_cvt_pk_f32_fp8_e32 v[168:169], v128
	v_cvt_pk_f32_fp8_sdwa v[170:171], v128 src0_sel:WORD_1
	v_pk_fma_f32 v[176:177], v[168:169], s[10:11], v[176:177] op_sel_hi:[1,0,1]
	v_pk_fma_f32 v[178:179], v[170:171], s[10:11], v[178:179] op_sel_hi:[1,0,1]
	v_cvt_pk_f32_fp8_e32 v[172:173], v132
	v_cvt_pk_f32_fp8_sdwa v[174:175], v132 src0_sel:WORD_1
	v_pk_fma_f32 v[176:177], v[172:173], s[10:11], v[176:177] op_sel_hi:[1,0,1]
	v_pk_fma_f32 v[178:179], v[174:175], s[10:11], v[178:179] op_sel_hi:[1,0,1]
	global_store_dwordx4 v159, v[176:179], s[4:5]
	v_lshlrev_b32_e32 v180, 16, v242
	v_and_b32_e32 v181, 0xffff0000, v242
	v_lshlrev_b32_e32 v182, 16, v243
	v_and_b32_e32 v183, 0xffff0000, v243
	v_cvt_pk_f32_fp8_e32 v[160:161], v121
	v_cvt_pk_f32_fp8_sdwa v[162:163], v121 src0_sel:WORD_1
	v_pk_fma_f32 v[180:181], v[160:161], s[10:11], v[180:181] op_sel_hi:[1,0,1]
	v_pk_fma_f32 v[182:183], v[162:163], s[10:11], v[182:183] op_sel_hi:[1,0,1]
	v_cvt_pk_f32_fp8_e32 v[164:165], v125
	v_cvt_pk_f32_fp8_sdwa v[166:167], v125 src0_sel:WORD_1
	v_pk_fma_f32 v[180:181], v[164:165], s[10:11], v[180:181] op_sel_hi:[1,0,1]
	v_pk_fma_f32 v[182:183], v[166:167], s[10:11], v[182:183] op_sel_hi:[1,0,1]
	v_cvt_pk_f32_fp8_e32 v[168:169], v129
	v_cvt_pk_f32_fp8_sdwa v[170:171], v129 src0_sel:WORD_1
	v_pk_fma_f32 v[180:181], v[168:169], s[10:11], v[180:181] op_sel_hi:[1,0,1]
	v_pk_fma_f32 v[182:183], v[170:171], s[10:11], v[182:183] op_sel_hi:[1,0,1]
	v_cvt_pk_f32_fp8_e32 v[172:173], v133
	v_cvt_pk_f32_fp8_sdwa v[174:175], v133 src0_sel:WORD_1
	v_pk_fma_f32 v[180:181], v[172:173], s[10:11], v[180:181] op_sel_hi:[1,0,1]
	v_pk_fma_f32 v[182:183], v[174:175], s[10:11], v[182:183] op_sel_hi:[1,0,1]
	global_store_dwordx4 v159, v[180:183], s[4:5] offset:1024
	v_lshlrev_b32_e32 v184, 16, v244
	v_and_b32_e32 v185, 0xffff0000, v244
	v_lshlrev_b32_e32 v186, 16, v245
	v_and_b32_e32 v187, 0xffff0000, v245
	v_cvt_pk_f32_fp8_e32 v[160:161], v122
	v_cvt_pk_f32_fp8_sdwa v[162:163], v122 src0_sel:WORD_1
	v_pk_fma_f32 v[184:185], v[160:161], s[10:11], v[184:185] op_sel_hi:[1,0,1]
	v_pk_fma_f32 v[186:187], v[162:163], s[10:11], v[186:187] op_sel_hi:[1,0,1]
	v_cvt_pk_f32_fp8_e32 v[164:165], v126
	v_cvt_pk_f32_fp8_sdwa v[166:167], v126 src0_sel:WORD_1
	v_pk_fma_f32 v[184:185], v[164:165], s[10:11], v[184:185] op_sel_hi:[1,0,1]
	v_pk_fma_f32 v[186:187], v[166:167], s[10:11], v[186:187] op_sel_hi:[1,0,1]
	v_cvt_pk_f32_fp8_e32 v[168:169], v130
	v_cvt_pk_f32_fp8_sdwa v[170:171], v130 src0_sel:WORD_1
	v_pk_fma_f32 v[184:185], v[168:169], s[10:11], v[184:185] op_sel_hi:[1,0,1]
	v_pk_fma_f32 v[186:187], v[170:171], s[10:11], v[186:187] op_sel_hi:[1,0,1]
	v_cvt_pk_f32_fp8_e32 v[172:173], v134
	v_cvt_pk_f32_fp8_sdwa v[174:175], v134 src0_sel:WORD_1
	v_pk_fma_f32 v[184:185], v[172:173], s[10:11], v[184:185] op_sel_hi:[1,0,1]
	v_pk_fma_f32 v[186:187], v[174:175], s[10:11], v[186:187] op_sel_hi:[1,0,1]
	global_store_dwordx4 v159, v[184:187], s[4:5] offset:2048
	v_lshlrev_b32_e32 v188, 16, v246
	v_and_b32_e32 v189, 0xffff0000, v246
	v_lshlrev_b32_e32 v190, 16, v247
	v_and_b32_e32 v191, 0xffff0000, v247
	v_cvt_pk_f32_fp8_e32 v[160:161], v123
	v_cvt_pk_f32_fp8_sdwa v[162:163], v123 src0_sel:WORD_1
	v_pk_fma_f32 v[188:189], v[160:161], s[10:11], v[188:189] op_sel_hi:[1,0,1]
	v_pk_fma_f32 v[190:191], v[162:163], s[10:11], v[190:191] op_sel_hi:[1,0,1]
	v_cvt_pk_f32_fp8_e32 v[164:165], v127
	v_cvt_pk_f32_fp8_sdwa v[166:167], v127 src0_sel:WORD_1
	v_pk_fma_f32 v[188:189], v[164:165], s[10:11], v[188:189] op_sel_hi:[1,0,1]
	v_pk_fma_f32 v[190:191], v[166:167], s[10:11], v[190:191] op_sel_hi:[1,0,1]
	v_cvt_pk_f32_fp8_e32 v[168:169], v131
	v_cvt_pk_f32_fp8_sdwa v[170:171], v131 src0_sel:WORD_1
	v_pk_fma_f32 v[188:189], v[168:169], s[10:11], v[188:189] op_sel_hi:[1,0,1]
	v_pk_fma_f32 v[190:191], v[170:171], s[10:11], v[190:191] op_sel_hi:[1,0,1]
	v_cvt_pk_f32_fp8_e32 v[172:173], v135
	v_cvt_pk_f32_fp8_sdwa v[174:175], v135 src0_sel:WORD_1
	v_pk_fma_f32 v[188:189], v[172:173], s[10:11], v[188:189] op_sel_hi:[1,0,1]
	v_pk_fma_f32 v[190:191], v[174:175], s[10:11], v[190:191] op_sel_hi:[1,0,1]
	global_store_dwordx4 v159, v[188:191], s[4:5] offset:3072
	s_waitcnt vmcnt(28)
	v_lshl_add_u32 v200, v8, 2, s23
	v_lshl_add_u32 v201, v9, 2, s23
	v_lshl_add_u32 v202, v10, 2, s23
	v_lshl_add_u32 v203, v11, 2, s23
	v_lshl_add_u32 v204, v12, 2, s23
	v_lshl_add_u32 v205, v13, 2, s23
	v_lshl_add_u32 v206, v14, 2, s23
	v_lshl_add_u32 v207, v15, 2, s23
	v_lshl_add_u32 v208, v16, 2, s23
	v_lshl_add_u32 v209, v17, 2, s23
	v_lshl_add_u32 v210, v18, 2, s23
	v_lshl_add_u32 v211, v19, 2, s23
	v_lshl_add_u32 v212, v20, 2, s23
	v_lshl_add_u32 v213, v21, 2, s23
	v_lshl_add_u32 v214, v22, 2, s23
	v_lshl_add_u32 v215, v23, 2, s23
	ds_read_b32 v136, v200
	ds_read_b32 v137, v201
	ds_read_b32 v138, v202
	ds_read_b32 v139, v203
	ds_read_b32 v140, v204
	ds_read_b32 v141, v205
	ds_read_b32 v142, v206
	ds_read_b32 v143, v207
	ds_read_b32 v144, v208
	ds_read_b32 v145, v209
	ds_read_b32 v146, v210
	ds_read_b32 v147, v211
	ds_read_b32 v148, v212
	ds_read_b32 v149, v213
	ds_read_b32 v150, v214
	ds_read_b32 v151, v215
	v_add_u32_e32 v192, 0x2000, v3
	v_lshl_add_u32 v156, v192, 13, v6
	v_add_u32_e32 v193, 0x2400, v3
	v_lshl_add_u32 v157, v193, 13, v6
	v_add_u32_e32 v194, 0x2800, v3
	v_lshl_add_u32 v158, v194, 13, v6
	v_add_u32_e32 v195, 0x2c00, v3
	v_lshl_add_u32 v159, v195, 13, v6
	s_waitcnt lgkmcnt(12)
; __device__ __forceinline__ float bf_lo(unsigned w) { return __uint_as_float(w << 16); }
; __device__ __forceinline__ float bf_hi(unsigned w) { return __uint_as_float(w & 0xffff0000u); }
; __global__ void __launch_bounds__(512, 2) fwd_kernel(Params p) {
;     ...
;             for (int u = 0; u < UN; ++u)
; #pragma unroll
;                 for (int k = 0; k < 4; ++k) { const int pos = ts[ee[u][k]] * 256 + rk[u][k]; y[u][k] = *(const u32x4*)(Yb + (size_t)pos * DM + cc[u]); }
; #pragma unroll
;             for (int u = 0; u < UN; ++u) {
;                 f32x4 a[4];
;                 a[0] = (f32x4){bf_lo(xa[u].x), bf_hi(xa[u].x), bf_lo(xa[u].y), bf_hi(xa[u].y)}; a[1] = (f32x4){bf_lo(xa[u].z), bf_hi(xa[u].z), bf_lo(xa[u].w), bf_hi(xa[u].w)};
;                 a[2] = (f32x4){bf_lo(xb[u].x), bf_hi(xb[u].x), bf_lo(xb[u].y), bf_hi(xb[u].y)}; a[3] = (f32x4){bf_lo(xb[u].z), bf_hi(xb[u].z), bf_lo(xb[u].w), bf_hi(xb[u].w)};
; #pragma unroll
;                 for (int k = 0; k < 4; ++k)
; #pragma unroll
;                     for (int q = 0; q < 4; ++q) { const f32x2 lo = __builtin_amdgcn_cvt_pk_f32_fp8((int)y[u][k][q], false), hi = __builtin_amdgcn_cvt_pk_f32_fp8((int)y[u][k][q], true);
;                         a[q].x += lo.x * (1.0f / Y8_SCALE); a[q].y += lo.y * (1.0f / Y8_SCALE); a[q].z += hi.x * (1.0f / Y8_SCALE); a[q].w += hi.y * (1.0f / Y8_SCALE); }
;                 if (it0 + u * NGT < NI) { float* op = p.out + (size_t)mm[u] * DM + cc[u];
; #pragma unroll
;                     for (int q = 0; q < 4; ++q) *(f32x4*)(op + 4 * q) = a[q]; }
	v_lshl_add_u32 v136, v136, 8, v24
	v_lshl_add_u32 v137, v137, 8, v25
	v_lshl_add_u32 v138, v138, 8, v26
	v_lshl_add_u32 v139, v139, 8, v27
	v_lshl_add_u32 v136, v136, 11, v4
	v_lshl_add_u32 v137, v137, 11, v4
	v_lshl_add_u32 v138, v138, 11, v4
	v_lshl_add_u32 v139, v139, 11, v4
	global_load_dword v72, v136, s[6:7]
	global_load_dword v73, v136, s[6:7] offset:256
	global_load_dword v74, v136, s[6:7] offset:512
	global_load_dword v75, v136, s[6:7] offset:768
	global_load_dword v76, v137, s[6:7]
	global_load_dword v77, v137, s[6:7] offset:256
	global_load_dword v78, v137, s[6:7] offset:512
	global_load_dword v79, v137, s[6:7] offset:768
	global_load_dword v80, v138, s[6:7]
	global_load_dword v81, v138, s[6:7] offset:256
	global_load_dword v82, v138, s[6:7] offset:512
	global_load_dword v83, v138, s[6:7] offset:768
	global_load_dword v84, v139, s[6:7]
	global_load_dword v85, v139, s[6:7] offset:256
	global_load_dword v86, v139, s[6:7] offset:512
	global_load_dword v87, v139, s[6:7] offset:768
	s_waitcnt lgkmcnt(8)
	v_lshl_add_u32 v140, v140, 8, v28
	v_lshl_add_u32 v141, v141, 8, v29
	v_lshl_add_u32 v142, v142, 8, v30
	v_lshl_add_u32 v143, v143, 8, v31
	v_lshl_add_u32 v140, v140, 11, v4
	v_lshl_add_u32 v141, v141, 11, v4
	v_lshl_add_u32 v142, v142, 11, v4
	v_lshl_add_u32 v143, v143, 11, v4
	global_load_dword v88, v140, s[6:7]
	global_load_dword v89, v140, s[6:7] offset:256
	global_load_dword v90, v140, s[6:7] offset:512
	global_load_dword v91, v140, s[6:7] offset:768
	global_load_dword v92, v141, s[6:7]
	global_load_dword v93, v141, s[6:7] offset:256
	global_load_dword v94, v141, s[6:7] offset:512
	global_load_dword v95, v141, s[6:7] offset:768
	global_load_dword v96, v142, s[6:7]
	global_load_dword v97, v142, s[6:7] offset:256
	global_load_dword v98, v142, s[6:7] offset:512
	global_load_dword v99, v142, s[6:7] offset:768
	global_load_dword v100, v143, s[6:7]
	global_load_dword v101, v143, s[6:7] offset:256
	global_load_dword v102, v143, s[6:7] offset:512
	global_load_dword v103, v143, s[6:7] offset:768
	s_waitcnt lgkmcnt(4)
	v_lshl_add_u32 v144, v144, 8, v32
	v_lshl_add_u32 v145, v145, 8, v33
	v_lshl_add_u32 v146, v146, 8, v34
	v_lshl_add_u32 v147, v147, 8, v35
	v_lshl_add_u32 v144, v144, 11, v4
	v_lshl_add_u32 v145, v145, 11, v4
	v_lshl_add_u32 v146, v146, 11, v4
	v_lshl_add_u32 v147, v147, 11, v4
	global_load_dword v104, v144, s[6:7]
	global_load_dword v105, v144, s[6:7] offset:256
	global_load_dword v106, v144, s[6:7] offset:512
	global_load_dword v107, v144, s[6:7] offset:768
	global_load_dword v108, v145, s[6:7]
	global_load_dword v109, v145, s[6:7] offset:256
	global_load_dword v110, v145, s[6:7] offset:512
	global_load_dword v111, v145, s[6:7] offset:768
	global_load_dword v112, v146, s[6:7]
	global_load_dword v113, v146, s[6:7] offset:256
	global_load_dword v114, v146, s[6:7] offset:512
	global_load_dword v115, v146, s[6:7] offset:768
	global_load_dword v116, v147, s[6:7]
	global_load_dword v117, v147, s[6:7] offset:256
	global_load_dword v118, v147, s[6:7] offset:512
	global_load_dword v119, v147, s[6:7] offset:768
	s_waitcnt lgkmcnt(0)
	v_lshl_add_u32 v148, v148, 8, v36
	v_lshl_add_u32 v149, v149, 8, v37
	v_lshl_add_u32 v150, v150, 8, v38
	v_lshl_add_u32 v151, v151, 8, v39
	v_lshl_add_u32 v148, v148, 11, v4
	v_lshl_add_u32 v149, v149, 11, v4
	v_lshl_add_u32 v150, v150, 11, v4
	v_lshl_add_u32 v151, v151, 11, v4
	global_load_dword v120, v148, s[6:7]
	global_load_dword v121, v148, s[6:7] offset:256
	global_load_dword v122, v148, s[6:7] offset:512
	global_load_dword v123, v148, s[6:7] offset:768
	global_load_dword v124, v149, s[6:7]
	global_load_dword v125, v149, s[6:7] offset:256
	global_load_dword v126, v149, s[6:7] offset:512
	global_load_dword v127, v149, s[6:7] offset:768
	global_load_dword v128, v150, s[6:7]
	global_load_dword v129, v150, s[6:7] offset:256
	global_load_dword v130, v150, s[6:7] offset:512
	global_load_dword v131, v150, s[6:7] offset:768
	global_load_dword v132, v151, s[6:7]
	global_load_dword v133, v151, s[6:7] offset:256
	global_load_dword v134, v151, s[6:7] offset:512
	global_load_dword v135, v151, s[6:7] offset:768
	s_waitcnt vmcnt(48)
	v_lshlrev_b32_e32 v176, 16, v40
	v_and_b32_e32 v177, 0xffff0000, v40
	v_lshlrev_b32_e32 v178, 16, v41
	v_and_b32_e32 v179, 0xffff0000, v41
	v_cvt_pk_f32_fp8_e32 v[160:161], v72
	v_cvt_pk_f32_fp8_sdwa v[162:163], v72 src0_sel:WORD_1
	v_pk_fma_f32 v[176:177], v[160:161], s[10:11], v[176:177] op_sel_hi:[1,0,1]
	v_pk_fma_f32 v[178:179], v[162:163], s[10:11], v[178:179] op_sel_hi:[1,0,1]
	v_cvt_pk_f32_fp8_e32 v[164:165], v76
	v_cvt_pk_f32_fp8_sdwa v[166:167], v76 src0_sel:WORD_1
	v_pk_fma_f32 v[176:177], v[164:165], s[10:11], v[176:177] op_sel_hi:[1,0,1]
	v_pk_fma_f32 v[178:179], v[166:167], s[10:11], v[178:179] op_sel_hi:[1,0,1]
	v_cvt_pk_f32_fp8_e32 v[168:169], v80
	v_cvt_pk_f32_fp8_sdwa v[170:171], v80 src0_sel:WORD_1
	v_pk_fma_f32 v[176:177], v[168:169], s[10:11], v[176:177] op_sel_hi:[1,0,1]
	v_pk_fma_f32 v[178:179], v[170:171], s[10:11], v[178:179] op_sel_hi:[1,0,1]
	v_cvt_pk_f32_fp8_e32 v[172:173], v84
	v_cvt_pk_f32_fp8_sdwa v[174:175], v84 src0_sel:WORD_1
	v_pk_fma_f32 v[176:177], v[172:173], s[10:11], v[176:177] op_sel_hi:[1,0,1]
	v_pk_fma_f32 v[178:179], v[174:175], s[10:11], v[178:179] op_sel_hi:[1,0,1]
	global_store_dwordx4 v156, v[176:179], s[4:5]
	v_lshlrev_b32_e32 v180, 16, v42
	v_and_b32_e32 v181, 0xffff0000, v42
	v_lshlrev_b32_e32 v182, 16, v43
	v_and_b32_e32 v183, 0xffff0000, v43
	v_cvt_pk_f32_fp8_e32 v[160:161], v73
	v_cvt_pk_f32_fp8_sdwa v[162:163], v73 src0_sel:WORD_1
	v_pk_fma_f32 v[180:181], v[160:161], s[10:11], v[180:181] op_sel_hi:[1,0,1]
; __device__ __forceinline__ float bf_lo(unsigned w) { return __uint_as_float(w << 16); }
; __device__ __forceinline__ float bf_hi(unsigned w) { return __uint_as_float(w & 0xffff0000u); }
; __global__ void __launch_bounds__(512, 2) fwd_kernel(Params p) {
;     ...
;             for (int u = 0; u < UN; ++u) { const int it = it0 + u * NGT < NI ? it0 + u * NGT : it0; mm[u] = it >> 7; cc[u] = (it & 127) * 16;
;                 const i32x4 e4 = *(const i32x4*)(tok_e + mm[u] * 4), r4 = *(const i32x4*)(tok_rank + mm[u] * 4);
; #pragma unroll
;                 for (int k = 0; k < 4; ++k) { ee[u][k] = e4[k]; rk[u][k] = r4[k]; }
;                 const bf16_t* xp = X1 + (size_t)mm[u] * DM + cc[u]; xa[u] = *(const u32x4*)xp; xb[u] = *(const u32x4*)(xp + 8); }
;     ...
;             for (int u = 0; u < UN; ++u) {
;                 f32x4 a[4];
;                 a[0] = (f32x4){bf_lo(xa[u].x), bf_hi(xa[u].x), bf_lo(xa[u].y), bf_hi(xa[u].y)}; a[1] = (f32x4){bf_lo(xa[u].z), bf_hi(xa[u].z), bf_lo(xa[u].w), bf_hi(xa[u].w)};
;                 a[2] = (f32x4){bf_lo(xb[u].x), bf_hi(xb[u].x), bf_lo(xb[u].y), bf_hi(xb[u].y)}; a[3] = (f32x4){bf_lo(xb[u].z), bf_hi(xb[u].z), bf_lo(xb[u].w), bf_hi(xb[u].w)};
; #pragma unroll
;                 for (int k = 0; k < 4; ++k)
; #pragma unroll
;                     for (int q = 0; q < 4; ++q) { const f32x2 lo = __builtin_amdgcn_cvt_pk_f32_fp8((int)y[u][k][q], false), hi = __builtin_amdgcn_cvt_pk_f32_fp8((int)y[u][k][q], true);
;                         a[q].x += lo.x * (1.0f / Y8_SCALE); a[q].y += lo.y * (1.0f / Y8_SCALE); a[q].z += hi.x * (1.0f / Y8_SCALE); a[q].w += hi.y * (1.0f / Y8_SCALE); }
;                 if (it0 + u * NGT < NI) { float* op = p.out + (size_t)mm[u] * DM + cc[u];
; #pragma unroll
;                     for (int q = 0; q < 4; ++q) *(f32x4*)(op + 4 * q) = a[q]; }
	v_pk_fma_f32 v[182:183], v[162:163], s[10:11], v[182:183] op_sel_hi:[1,0,1]
	v_cvt_pk_f32_fp8_e32 v[164:165], v77
	v_cvt_pk_f32_fp8_sdwa v[166:167], v77 src0_sel:WORD_1
	v_pk_fma_f32 v[180:181], v[164:165], s[10:11], v[180:181] op_sel_hi:[1,0,1]
	v_pk_fma_f32 v[182:183], v[166:167], s[10:11], v[182:183] op_sel_hi:[1,0,1]
	v_cvt_pk_f32_fp8_e32 v[168:169], v81
	v_cvt_pk_f32_fp8_sdwa v[170:171], v81 src0_sel:WORD_1
	v_pk_fma_f32 v[180:181], v[168:169], s[10:11], v[180:181] op_sel_hi:[1,0,1]
	v_pk_fma_f32 v[182:183], v[170:171], s[10:11], v[182:183] op_sel_hi:[1,0,1]
	v_cvt_pk_f32_fp8_e32 v[172:173], v85
	v_cvt_pk_f32_fp8_sdwa v[174:175], v85 src0_sel:WORD_1
	v_pk_fma_f32 v[180:181], v[172:173], s[10:11], v[180:181] op_sel_hi:[1,0,1]
	v_pk_fma_f32 v[182:183], v[174:175], s[10:11], v[182:183] op_sel_hi:[1,0,1]
	global_store_dwordx4 v156, v[180:183], s[4:5] offset:1024
	v_lshlrev_b32_e32 v184, 16, v44
	v_and_b32_e32 v185, 0xffff0000, v44
	v_lshlrev_b32_e32 v186, 16, v45
	v_and_b32_e32 v187, 0xffff0000, v45
	v_cvt_pk_f32_fp8_e32 v[160:161], v74
	v_cvt_pk_f32_fp8_sdwa v[162:163], v74 src0_sel:WORD_1
	v_pk_fma_f32 v[184:185], v[160:161], s[10:11], v[184:185] op_sel_hi:[1,0,1]
	v_pk_fma_f32 v[186:187], v[162:163], s[10:11], v[186:187] op_sel_hi:[1,0,1]
	v_cvt_pk_f32_fp8_e32 v[164:165], v78
	v_cvt_pk_f32_fp8_sdwa v[166:167], v78 src0_sel:WORD_1
	v_pk_fma_f32 v[184:185], v[164:165], s[10:11], v[184:185] op_sel_hi:[1,0,1]
	v_pk_fma_f32 v[186:187], v[166:167], s[10:11], v[186:187] op_sel_hi:[1,0,1]
	v_cvt_pk_f32_fp8_e32 v[168:169], v82
	v_cvt_pk_f32_fp8_sdwa v[170:171], v82 src0_sel:WORD_1
	v_pk_fma_f32 v[184:185], v[168:169], s[10:11], v[184:185] op_sel_hi:[1,0,1]
	v_pk_fma_f32 v[186:187], v[170:171], s[10:11], v[186:187] op_sel_hi:[1,0,1]
	v_cvt_pk_f32_fp8_e32 v[172:173], v86
	v_cvt_pk_f32_fp8_sdwa v[174:175], v86 src0_sel:WORD_1
	v_pk_fma_f32 v[184:185], v[172:173], s[10:11], v[184:185] op_sel_hi:[1,0,1]
	v_pk_fma_f32 v[186:187], v[174:175], s[10:11], v[186:187] op_sel_hi:[1,0,1]
	global_store_dwordx4 v156, v[184:187], s[4:5] offset:2048
	v_lshlrev_b32_e32 v188, 16, v46
	v_and_b32_e32 v189, 0xffff0000, v46
	v_lshlrev_b32_e32 v190, 16, v47
	v_and_b32_e32 v191, 0xffff0000, v47
	v_cvt_pk_f32_fp8_e32 v[160:161], v75
	v_cvt_pk_f32_fp8_sdwa v[162:163], v75 src0_sel:WORD_1
	v_pk_fma_f32 v[188:189], v[160:161], s[10:11], v[188:189] op_sel_hi:[1,0,1]
	v_pk_fma_f32 v[190:191], v[162:163], s[10:11], v[190:191] op_sel_hi:[1,0,1]
	v_cvt_pk_f32_fp8_e32 v[164:165], v79
	v_cvt_pk_f32_fp8_sdwa v[166:167], v79 src0_sel:WORD_1
	v_pk_fma_f32 v[188:189], v[164:165], s[10:11], v[188:189] op_sel_hi:[1,0,1]
	v_pk_fma_f32 v[190:191], v[166:167], s[10:11], v[190:191] op_sel_hi:[1,0,1]
	v_cvt_pk_f32_fp8_e32 v[168:169], v83
	v_cvt_pk_f32_fp8_sdwa v[170:171], v83 src0_sel:WORD_1
	v_pk_fma_f32 v[188:189], v[168:169], s[10:11], v[188:189] op_sel_hi:[1,0,1]
	v_pk_fma_f32 v[190:191], v[170:171], s[10:11], v[190:191] op_sel_hi:[1,0,1]
	v_cvt_pk_f32_fp8_e32 v[172:173], v87
	v_cvt_pk_f32_fp8_sdwa v[174:175], v87 src0_sel:WORD_1
	v_pk_fma_f32 v[188:189], v[172:173], s[10:11], v[188:189] op_sel_hi:[1,0,1]
	v_pk_fma_f32 v[190:191], v[174:175], s[10:11], v[190:191] op_sel_hi:[1,0,1]
	global_store_dwordx4 v156, v[188:191], s[4:5] offset:3072
	v_add_u32_e32 v192, 0x3000, v3
	v_lshlrev_b32_e32 v196, 4, v192
	v_add_u32_e32 v193, 0x3400, v3
	v_lshlrev_b32_e32 v197, 4, v193
	v_add_u32_e32 v194, 0x3800, v3
	v_lshlrev_b32_e32 v198, 4, v194
	v_add_u32_e32 v195, 0x3c00, v3
	v_lshlrev_b32_e32 v199, 4, v195
	global_load_dwordx4 v[8:11], v196, s[16:17]
	global_load_dwordx4 v[12:15], v197, s[16:17]
	global_load_dwordx4 v[16:19], v198, s[16:17]
	global_load_dwordx4 v[20:23], v199, s[16:17]
	global_load_dwordx4 v[24:27], v196, s[18:19]
	global_load_dwordx4 v[28:31], v197, s[18:19]
	global_load_dwordx4 v[32:35], v198, s[18:19]
	global_load_dwordx4 v[36:39], v199, s[18:19]
	v_lshl_add_u32 v196, v192, 12, v5
	global_load_dwordx2 v[216:217], v196, s[14:15]
	global_load_dwordx2 v[218:219], v196, s[14:15] offset:512
	global_load_dwordx2 v[220:221], v196, s[14:15] offset:1024
	global_load_dwordx2 v[222:223], v196, s[14:15] offset:1536
	v_lshl_add_u32 v197, v193, 12, v5
	global_load_dwordx2 v[224:225], v197, s[14:15]
	global_load_dwordx2 v[226:227], v197, s[14:15] offset:512
	global_load_dwordx2 v[228:229], v197, s[14:15] offset:1024
	global_load_dwordx2 v[230:231], v197, s[14:15] offset:1536
	v_lshl_add_u32 v198, v194, 12, v5
	global_load_dwordx2 v[232:233], v198, s[14:15]
	global_load_dwordx2 v[234:235], v198, s[14:15] offset:512
	global_load_dwordx2 v[236:237], v198, s[14:15] offset:1024
	global_load_dwordx2 v[238:239], v198, s[14:15] offset:1536
	v_lshl_add_u32 v199, v195, 12, v5
	global_load_dwordx2 v[240:241], v199, s[14:15]
	global_load_dwordx2 v[242:243], v199, s[14:15] offset:512
	global_load_dwordx2 v[244:245], v199, s[14:15] offset:1024
	global_load_dwordx2 v[246:247], v199, s[14:15] offset:1536
	s_waitcnt vmcnt(60)
; __device__ __forceinline__ float bf_lo(unsigned w) { return __uint_as_float(w << 16); }
; __device__ __forceinline__ float bf_hi(unsigned w) { return __uint_as_float(w & 0xffff0000u); }
; __global__ void __launch_bounds__(512, 2) fwd_kernel(Params p) {
;     ...
;             for (int u = 0; u < UN; ++u) {
;                 f32x4 a[4];
;                 a[0] = (f32x4){bf_lo(xa[u].x), bf_hi(xa[u].x), bf_lo(xa[u].y), bf_hi(xa[u].y)}; a[1] = (f32x4){bf_lo(xa[u].z), bf_hi(xa[u].z), bf_lo(xa[u].w), bf_hi(xa[u].w)};
;                 a[2] = (f32x4){bf_lo(xb[u].x), bf_hi(xb[u].x), bf_lo(xb[u].y), bf_hi(xb[u].y)}; a[3] = (f32x4){bf_lo(xb[u].z), bf_hi(xb[u].z), bf_lo(xb[u].w), bf_hi(xb[u].w)};
; #pragma unroll
;                 for (int k = 0; k < 4; ++k)
; #pragma unroll
;                     for (int q = 0; q < 4; ++q) { const f32x2 lo = __builtin_amdgcn_cvt_pk_f32_fp8((int)y[u][k][q], false), hi = __builtin_amdgcn_cvt_pk_f32_fp8((int)y[u][k][q], true);
;                         a[q].x += lo.x * (1.0f / Y8_SCALE); a[q].y += lo.y * (1.0f / Y8_SCALE); a[q].z += hi.x * (1.0f / Y8_SCALE); a[q].w += hi.y * (1.0f / Y8_SCALE); }
;                 if (it0 + u * NGT < NI) { float* op = p.out + (size_t)mm[u] * DM + cc[u];
; #pragma unroll
;                     for (int q = 0; q < 4; ++q) *(f32x4*)(op + 4 * q) = a[q]; }
	v_lshlrev_b32_e32 v176, 16, v48
	v_and_b32_e32 v177, 0xffff0000, v48
	v_lshlrev_b32_e32 v178, 16, v49
	v_and_b32_e32 v179, 0xffff0000, v49
	v_cvt_pk_f32_fp8_e32 v[160:161], v88
	v_cvt_pk_f32_fp8_sdwa v[162:163], v88 src0_sel:WORD_1
	v_pk_fma_f32 v[176:177], v[160:161], s[10:11], v[176:177] op_sel_hi:[1,0,1]
	v_pk_fma_f32 v[178:179], v[162:163], s[10:11], v[178:179] op_sel_hi:[1,0,1]
	v_cvt_pk_f32_fp8_e32 v[164:165], v92
	v_cvt_pk_f32_fp8_sdwa v[166:167], v92 src0_sel:WORD_1
	v_pk_fma_f32 v[176:177], v[164:165], s[10:11], v[176:177] op_sel_hi:[1,0,1]
	v_pk_fma_f32 v[178:179], v[166:167], s[10:11], v[178:179] op_sel_hi:[1,0,1]
	v_cvt_pk_f32_fp8_e32 v[168:169], v96
	v_cvt_pk_f32_fp8_sdwa v[170:171], v96 src0_sel:WORD_1
	v_pk_fma_f32 v[176:177], v[168:169], s[10:11], v[176:177] op_sel_hi:[1,0,1]
	v_pk_fma_f32 v[178:179], v[170:171], s[10:11], v[178:179] op_sel_hi:[1,0,1]
	v_cvt_pk_f32_fp8_e32 v[172:173], v100
	v_cvt_pk_f32_fp8_sdwa v[174:175], v100 src0_sel:WORD_1
	v_pk_fma_f32 v[176:177], v[172:173], s[10:11], v[176:177] op_sel_hi:[1,0,1]
	v_pk_fma_f32 v[178:179], v[174:175], s[10:11], v[178:179] op_sel_hi:[1,0,1]
	global_store_dwordx4 v157, v[176:179], s[4:5]
	v_lshlrev_b32_e32 v180, 16, v50
	v_and_b32_e32 v181, 0xffff0000, v50
	v_lshlrev_b32_e32 v182, 16, v51
	v_and_b32_e32 v183, 0xffff0000, v51
	v_cvt_pk_f32_fp8_e32 v[160:161], v89
	v_cvt_pk_f32_fp8_sdwa v[162:163], v89 src0_sel:WORD_1
	v_pk_fma_f32 v[180:181], v[160:161], s[10:11], v[180:181] op_sel_hi:[1,0,1]
	v_pk_fma_f32 v[182:183], v[162:163], s[10:11], v[182:183] op_sel_hi:[1,0,1]
	v_cvt_pk_f32_fp8_e32 v[164:165], v93
	v_cvt_pk_f32_fp8_sdwa v[166:167], v93 src0_sel:WORD_1
	v_pk_fma_f32 v[180:181], v[164:165], s[10:11], v[180:181] op_sel_hi:[1,0,1]
	v_pk_fma_f32 v[182:183], v[166:167], s[10:11], v[182:183] op_sel_hi:[1,0,1]
	v_cvt_pk_f32_fp8_e32 v[168:169], v97
	v_cvt_pk_f32_fp8_sdwa v[170:171], v97 src0_sel:WORD_1
	v_pk_fma_f32 v[180:181], v[168:169], s[10:11], v[180:181] op_sel_hi:[1,0,1]
	v_pk_fma_f32 v[182:183], v[170:171], s[10:11], v[182:183] op_sel_hi:[1,0,1]
	v_cvt_pk_f32_fp8_e32 v[172:173], v101
	v_cvt_pk_f32_fp8_sdwa v[174:175], v101 src0_sel:WORD_1
	v_pk_fma_f32 v[180:181], v[172:173], s[10:11], v[180:181] op_sel_hi:[1,0,1]
	v_pk_fma_f32 v[182:183], v[174:175], s[10:11], v[182:183] op_sel_hi:[1,0,1]
	global_store_dwordx4 v157, v[180:183], s[4:5] offset:1024
	v_lshlrev_b32_e32 v184, 16, v52
	v_and_b32_e32 v185, 0xffff0000, v52
	v_lshlrev_b32_e32 v186, 16, v53
	v_and_b32_e32 v187, 0xffff0000, v53
	v_cvt_pk_f32_fp8_e32 v[160:161], v90
	v_cvt_pk_f32_fp8_sdwa v[162:163], v90 src0_sel:WORD_1
	v_pk_fma_f32 v[184:185], v[160:161], s[10:11], v[184:185] op_sel_hi:[1,0,1]
	v_pk_fma_f32 v[186:187], v[162:163], s[10:11], v[186:187] op_sel_hi:[1,0,1]
	v_cvt_pk_f32_fp8_e32 v[164:165], v94
	v_cvt_pk_f32_fp8_sdwa v[166:167], v94 src0_sel:WORD_1
	v_pk_fma_f32 v[184:185], v[164:165], s[10:11], v[184:185] op_sel_hi:[1,0,1]
	v_pk_fma_f32 v[186:187], v[166:167], s[10:11], v[186:187] op_sel_hi:[1,0,1]
	v_cvt_pk_f32_fp8_e32 v[168:169], v98
	v_cvt_pk_f32_fp8_sdwa v[170:171], v98 src0_sel:WORD_1
	v_pk_fma_f32 v[184:185], v[168:169], s[10:11], v[184:185] op_sel_hi:[1,0,1]
	v_pk_fma_f32 v[186:187], v[170:171], s[10:11], v[186:187] op_sel_hi:[1,0,1]
	v_cvt_pk_f32_fp8_e32 v[172:173], v102
	v_cvt_pk_f32_fp8_sdwa v[174:175], v102 src0_sel:WORD_1
	v_pk_fma_f32 v[184:185], v[172:173], s[10:11], v[184:185] op_sel_hi:[1,0,1]
	v_pk_fma_f32 v[186:187], v[174:175], s[10:11], v[186:187] op_sel_hi:[1,0,1]
	global_store_dwordx4 v157, v[184:187], s[4:5] offset:2048
	v_lshlrev_b32_e32 v188, 16, v54
	v_and_b32_e32 v189, 0xffff0000, v54
	v_lshlrev_b32_e32 v190, 16, v55
	v_and_b32_e32 v191, 0xffff0000, v55
	v_cvt_pk_f32_fp8_e32 v[160:161], v91
	v_cvt_pk_f32_fp8_sdwa v[162:163], v91 src0_sel:WORD_1
	v_pk_fma_f32 v[188:189], v[160:161], s[10:11], v[188:189] op_sel_hi:[1,0,1]
	v_pk_fma_f32 v[190:191], v[162:163], s[10:11], v[190:191] op_sel_hi:[1,0,1]
	v_cvt_pk_f32_fp8_e32 v[164:165], v95
	v_cvt_pk_f32_fp8_sdwa v[166:167], v95 src0_sel:WORD_1
	v_pk_fma_f32 v[188:189], v[164:165], s[10:11], v[188:189] op_sel_hi:[1,0,1]
	v_pk_fma_f32 v[190:191], v[166:167], s[10:11], v[190:191] op_sel_hi:[1,0,1]
	v_cvt_pk_f32_fp8_e32 v[168:169], v99
	v_cvt_pk_f32_fp8_sdwa v[170:171], v99 src0_sel:WORD_1
	v_pk_fma_f32 v[188:189], v[168:169], s[10:11], v[188:189] op_sel_hi:[1,0,1]
	v_pk_fma_f32 v[190:191], v[170:171], s[10:11], v[190:191] op_sel_hi:[1,0,1]
	v_cvt_pk_f32_fp8_e32 v[172:173], v103
	v_cvt_pk_f32_fp8_sdwa v[174:175], v103 src0_sel:WORD_1
	v_pk_fma_f32 v[188:189], v[172:173], s[10:11], v[188:189] op_sel_hi:[1,0,1]
	v_pk_fma_f32 v[190:191], v[174:175], s[10:11], v[190:191] op_sel_hi:[1,0,1]
	global_store_dwordx4 v157, v[188:191], s[4:5] offset:3072
	s_waitcnt vmcnt(48)
; __device__ __forceinline__ float bf_lo(unsigned w) { return __uint_as_float(w << 16); }
; __device__ __forceinline__ float bf_hi(unsigned w) { return __uint_as_float(w & 0xffff0000u); }
; __global__ void __launch_bounds__(512, 2) fwd_kernel(Params p) {
;     ...
;             for (int u = 0; u < UN; ++u) {
;                 f32x4 a[4];
;                 a[0] = (f32x4){bf_lo(xa[u].x), bf_hi(xa[u].x), bf_lo(xa[u].y), bf_hi(xa[u].y)}; a[1] = (f32x4){bf_lo(xa[u].z), bf_hi(xa[u].z), bf_lo(xa[u].w), bf_hi(xa[u].w)};
;                 a[2] = (f32x4){bf_lo(xb[u].x), bf_hi(xb[u].x), bf_lo(xb[u].y), bf_hi(xb[u].y)}; a[3] = (f32x4){bf_lo(xb[u].z), bf_hi(xb[u].z), bf_lo(xb[u].w), bf_hi(xb[u].w)};
; #pragma unroll
;                 for (int k = 0; k < 4; ++k)
; #pragma unroll
;                     for (int q = 0; q < 4; ++q) { const f32x2 lo = __builtin_amdgcn_cvt_pk_f32_fp8((int)y[u][k][q], false), hi = __builtin_amdgcn_cvt_pk_f32_fp8((int)y[u][k][q], true);
;                         a[q].x += lo.x * (1.0f / Y8_SCALE); a[q].y += lo.y * (1.0f / Y8_SCALE); a[q].z += hi.x * (1.0f / Y8_SCALE); a[q].w += hi.y * (1.0f / Y8_SCALE); }
;                 if (it0 + u * NGT < NI) { float* op = p.out + (size_t)mm[u] * DM + cc[u];
; #pragma unroll
;                     for (int q = 0; q < 4; ++q) *(f32x4*)(op + 4 * q) = a[q]; }
	v_lshlrev_b32_e32 v176, 16, v56
	v_and_b32_e32 v177, 0xffff0000, v56
	v_lshlrev_b32_e32 v178, 16, v57
	v_and_b32_e32 v179, 0xffff0000, v57
	v_cvt_pk_f32_fp8_e32 v[160:161], v104
	v_cvt_pk_f32_fp8_sdwa v[162:163], v104 src0_sel:WORD_1
	v_pk_fma_f32 v[176:177], v[160:161], s[10:11], v[176:177] op_sel_hi:[1,0,1]
	v_pk_fma_f32 v[178:179], v[162:163], s[10:11], v[178:179] op_sel_hi:[1,0,1]
	v_cvt_pk_f32_fp8_e32 v[164:165], v108
	v_cvt_pk_f32_fp8_sdwa v[166:167], v108 src0_sel:WORD_1
	v_pk_fma_f32 v[176:177], v[164:165], s[10:11], v[176:177] op_sel_hi:[1,0,1]
	v_pk_fma_f32 v[178:179], v[166:167], s[10:11], v[178:179] op_sel_hi:[1,0,1]
	v_cvt_pk_f32_fp8_e32 v[168:169], v112
	v_cvt_pk_f32_fp8_sdwa v[170:171], v112 src0_sel:WORD_1
	v_pk_fma_f32 v[176:177], v[168:169], s[10:11], v[176:177] op_sel_hi:[1,0,1]
	v_pk_fma_f32 v[178:179], v[170:171], s[10:11], v[178:179] op_sel_hi:[1,0,1]
	v_cvt_pk_f32_fp8_e32 v[172:173], v116
	v_cvt_pk_f32_fp8_sdwa v[174:175], v116 src0_sel:WORD_1
	v_pk_fma_f32 v[176:177], v[172:173], s[10:11], v[176:177] op_sel_hi:[1,0,1]
	v_pk_fma_f32 v[178:179], v[174:175], s[10:11], v[178:179] op_sel_hi:[1,0,1]
	global_store_dwordx4 v158, v[176:179], s[4:5]
	v_lshlrev_b32_e32 v180, 16, v58
	v_and_b32_e32 v181, 0xffff0000, v58
	v_lshlrev_b32_e32 v182, 16, v59
	v_and_b32_e32 v183, 0xffff0000, v59
	v_cvt_pk_f32_fp8_e32 v[160:161], v105
	v_cvt_pk_f32_fp8_sdwa v[162:163], v105 src0_sel:WORD_1
	v_pk_fma_f32 v[180:181], v[160:161], s[10:11], v[180:181] op_sel_hi:[1,0,1]
	v_pk_fma_f32 v[182:183], v[162:163], s[10:11], v[182:183] op_sel_hi:[1,0,1]
	v_cvt_pk_f32_fp8_e32 v[164:165], v109
	v_cvt_pk_f32_fp8_sdwa v[166:167], v109 src0_sel:WORD_1
	v_pk_fma_f32 v[180:181], v[164:165], s[10:11], v[180:181] op_sel_hi:[1,0,1]
	v_pk_fma_f32 v[182:183], v[166:167], s[10:11], v[182:183] op_sel_hi:[1,0,1]
	v_cvt_pk_f32_fp8_e32 v[168:169], v113
	v_cvt_pk_f32_fp8_sdwa v[170:171], v113 src0_sel:WORD_1
	v_pk_fma_f32 v[180:181], v[168:169], s[10:11], v[180:181] op_sel_hi:[1,0,1]
	v_pk_fma_f32 v[182:183], v[170:171], s[10:11], v[182:183] op_sel_hi:[1,0,1]
	v_cvt_pk_f32_fp8_e32 v[172:173], v117
	v_cvt_pk_f32_fp8_sdwa v[174:175], v117 src0_sel:WORD_1
	v_pk_fma_f32 v[180:181], v[172:173], s[10:11], v[180:181] op_sel_hi:[1,0,1]
	v_pk_fma_f32 v[182:183], v[174:175], s[10:11], v[182:183] op_sel_hi:[1,0,1]
	global_store_dwordx4 v158, v[180:183], s[4:5] offset:1024
	v_lshlrev_b32_e32 v184, 16, v60
	v_and_b32_e32 v185, 0xffff0000, v60
	v_lshlrev_b32_e32 v186, 16, v61
	v_and_b32_e32 v187, 0xffff0000, v61
	v_cvt_pk_f32_fp8_e32 v[160:161], v106
	v_cvt_pk_f32_fp8_sdwa v[162:163], v106 src0_sel:WORD_1
	v_pk_fma_f32 v[184:185], v[160:161], s[10:11], v[184:185] op_sel_hi:[1,0,1]
	v_pk_fma_f32 v[186:187], v[162:163], s[10:11], v[186:187] op_sel_hi:[1,0,1]
	v_cvt_pk_f32_fp8_e32 v[164:165], v110
	v_cvt_pk_f32_fp8_sdwa v[166:167], v110 src0_sel:WORD_1
	v_pk_fma_f32 v[184:185], v[164:165], s[10:11], v[184:185] op_sel_hi:[1,0,1]
	v_pk_fma_f32 v[186:187], v[166:167], s[10:11], v[186:187] op_sel_hi:[1,0,1]
	v_cvt_pk_f32_fp8_e32 v[168:169], v114
	v_cvt_pk_f32_fp8_sdwa v[170:171], v114 src0_sel:WORD_1
	v_pk_fma_f32 v[184:185], v[168:169], s[10:11], v[184:185] op_sel_hi:[1,0,1]
	v_pk_fma_f32 v[186:187], v[170:171], s[10:11], v[186:187] op_sel_hi:[1,0,1]
	v_cvt_pk_f32_fp8_e32 v[172:173], v118
	v_cvt_pk_f32_fp8_sdwa v[174:175], v118 src0_sel:WORD_1
	v_pk_fma_f32 v[184:185], v[172:173], s[10:11], v[184:185] op_sel_hi:[1,0,1]
	v_pk_fma_f32 v[186:187], v[174:175], s[10:11], v[186:187] op_sel_hi:[1,0,1]
	global_store_dwordx4 v158, v[184:187], s[4:5] offset:2048
	v_lshlrev_b32_e32 v188, 16, v62
	v_and_b32_e32 v189, 0xffff0000, v62
	v_lshlrev_b32_e32 v190, 16, v63
	v_and_b32_e32 v191, 0xffff0000, v63
	v_cvt_pk_f32_fp8_e32 v[160:161], v107
	v_cvt_pk_f32_fp8_sdwa v[162:163], v107 src0_sel:WORD_1
	v_pk_fma_f32 v[188:189], v[160:161], s[10:11], v[188:189] op_sel_hi:[1,0,1]
	v_pk_fma_f32 v[190:191], v[162:163], s[10:11], v[190:191] op_sel_hi:[1,0,1]
	v_cvt_pk_f32_fp8_e32 v[164:165], v111
	v_cvt_pk_f32_fp8_sdwa v[166:167], v111 src0_sel:WORD_1
	v_pk_fma_f32 v[188:189], v[164:165], s[10:11], v[188:189] op_sel_hi:[1,0,1]
	v_pk_fma_f32 v[190:191], v[166:167], s[10:11], v[190:191] op_sel_hi:[1,0,1]
	v_cvt_pk_f32_fp8_e32 v[168:169], v115
	v_cvt_pk_f32_fp8_sdwa v[170:171], v115 src0_sel:WORD_1
	v_pk_fma_f32 v[188:189], v[168:169], s[10:11], v[188:189] op_sel_hi:[1,0,1]
	v_pk_fma_f32 v[190:191], v[170:171], s[10:11], v[190:191] op_sel_hi:[1,0,1]
	v_cvt_pk_f32_fp8_e32 v[172:173], v119
	v_cvt_pk_f32_fp8_sdwa v[174:175], v119 src0_sel:WORD_1
	v_pk_fma_f32 v[188:189], v[172:173], s[10:11], v[188:189] op_sel_hi:[1,0,1]
	v_pk_fma_f32 v[190:191], v[174:175], s[10:11], v[190:191] op_sel_hi:[1,0,1]
	global_store_dwordx4 v158, v[188:191], s[4:5] offset:3072
	s_waitcnt vmcnt(36)
; __device__ __forceinline__ float bf_lo(unsigned w) { return __uint_as_float(w << 16); }
; __device__ __forceinline__ float bf_hi(unsigned w) { return __uint_as_float(w & 0xffff0000u); }
; __global__ void __launch_bounds__(512, 2) fwd_kernel(Params p) {
;     ...
;             for (int u = 0; u < UN; ++u)
; #pragma unroll
;                 for (int k = 0; k < 4; ++k) { const int pos = ts[ee[u][k]] * 256 + rk[u][k]; y[u][k] = *(const u32x4*)(Yb + (size_t)pos * DM + cc[u]); }
; #pragma unroll
;             for (int u = 0; u < UN; ++u) {
;                 f32x4 a[4];
;                 a[0] = (f32x4){bf_lo(xa[u].x), bf_hi(xa[u].x), bf_lo(xa[u].y), bf_hi(xa[u].y)}; a[1] = (f32x4){bf_lo(xa[u].z), bf_hi(xa[u].z), bf_lo(xa[u].w), bf_hi(xa[u].w)};
;                 a[2] = (f32x4){bf_lo(xb[u].x), bf_hi(xb[u].x), bf_lo(xb[u].y), bf_hi(xb[u].y)}; a[3] = (f32x4){bf_lo(xb[u].z), bf_hi(xb[u].z), bf_lo(xb[u].w), bf_hi(xb[u].w)};
; #pragma unroll
;                 for (int k = 0; k < 4; ++k)
; #pragma unroll
;                     for (int q = 0; q < 4; ++q) { const f32x2 lo = __builtin_amdgcn_cvt_pk_f32_fp8((int)y[u][k][q], false), hi = __builtin_amdgcn_cvt_pk_f32_fp8((int)y[u][k][q], true);
;                         a[q].x += lo.x * (1.0f / Y8_SCALE); a[q].y += lo.y * (1.0f / Y8_SCALE); a[q].z += hi.x * (1.0f / Y8_SCALE); a[q].w += hi.y * (1.0f / Y8_SCALE); }
;                 if (it0 + u * NGT < NI) { float* op = p.out + (size_t)mm[u] * DM + cc[u];
; #pragma unroll
;                     for (int q = 0; q < 4; ++q) *(f32x4*)(op + 4 * q) = a[q]; }
	v_lshlrev_b32_e32 v176, 16, v64
	v_and_b32_e32 v177, 0xffff0000, v64
	v_lshlrev_b32_e32 v178, 16, v65
	v_and_b32_e32 v179, 0xffff0000, v65
	v_cvt_pk_f32_fp8_e32 v[160:161], v120
	v_cvt_pk_f32_fp8_sdwa v[162:163], v120 src0_sel:WORD_1
	v_pk_fma_f32 v[176:177], v[160:161], s[10:11], v[176:177] op_sel_hi:[1,0,1]
	v_pk_fma_f32 v[178:179], v[162:163], s[10:11], v[178:179] op_sel_hi:[1,0,1]
	v_cvt_pk_f32_fp8_e32 v[164:165], v124
	v_cvt_pk_f32_fp8_sdwa v[166:167], v124 src0_sel:WORD_1
	v_pk_fma_f32 v[176:177], v[164:165], s[10:11], v[176:177] op_sel_hi:[1,0,1]
	v_pk_fma_f32 v[178:179], v[166:167], s[10:11], v[178:179] op_sel_hi:[1,0,1]
	v_cvt_pk_f32_fp8_e32 v[168:169], v128
	v_cvt_pk_f32_fp8_sdwa v[170:171], v128 src0_sel:WORD_1
	v_pk_fma_f32 v[176:177], v[168:169], s[10:11], v[176:177] op_sel_hi:[1,0,1]
	v_pk_fma_f32 v[178:179], v[170:171], s[10:11], v[178:179] op_sel_hi:[1,0,1]
	v_cvt_pk_f32_fp8_e32 v[172:173], v132
	v_cvt_pk_f32_fp8_sdwa v[174:175], v132 src0_sel:WORD_1
	v_pk_fma_f32 v[176:177], v[172:173], s[10:11], v[176:177] op_sel_hi:[1,0,1]
	v_pk_fma_f32 v[178:179], v[174:175], s[10:11], v[178:179] op_sel_hi:[1,0,1]
	global_store_dwordx4 v159, v[176:179], s[4:5]
	v_lshlrev_b32_e32 v180, 16, v66
	v_and_b32_e32 v181, 0xffff0000, v66
	v_lshlrev_b32_e32 v182, 16, v67
	v_and_b32_e32 v183, 0xffff0000, v67
	v_cvt_pk_f32_fp8_e32 v[160:161], v121
	v_cvt_pk_f32_fp8_sdwa v[162:163], v121 src0_sel:WORD_1
	v_pk_fma_f32 v[180:181], v[160:161], s[10:11], v[180:181] op_sel_hi:[1,0,1]
	v_pk_fma_f32 v[182:183], v[162:163], s[10:11], v[182:183] op_sel_hi:[1,0,1]
	v_cvt_pk_f32_fp8_e32 v[164:165], v125
	v_cvt_pk_f32_fp8_sdwa v[166:167], v125 src0_sel:WORD_1
	v_pk_fma_f32 v[180:181], v[164:165], s[10:11], v[180:181] op_sel_hi:[1,0,1]
	v_pk_fma_f32 v[182:183], v[166:167], s[10:11], v[182:183] op_sel_hi:[1,0,1]
	v_cvt_pk_f32_fp8_e32 v[168:169], v129
	v_cvt_pk_f32_fp8_sdwa v[170:171], v129 src0_sel:WORD_1
	v_pk_fma_f32 v[180:181], v[168:169], s[10:11], v[180:181] op_sel_hi:[1,0,1]
	v_pk_fma_f32 v[182:183], v[170:171], s[10:11], v[182:183] op_sel_hi:[1,0,1]
	v_cvt_pk_f32_fp8_e32 v[172:173], v133
	v_cvt_pk_f32_fp8_sdwa v[174:175], v133 src0_sel:WORD_1
	v_pk_fma_f32 v[180:181], v[172:173], s[10:11], v[180:181] op_sel_hi:[1,0,1]
	v_pk_fma_f32 v[182:183], v[174:175], s[10:11], v[182:183] op_sel_hi:[1,0,1]
	global_store_dwordx4 v159, v[180:183], s[4:5] offset:1024
	v_lshlrev_b32_e32 v184, 16, v68
	v_and_b32_e32 v185, 0xffff0000, v68
	v_lshlrev_b32_e32 v186, 16, v69
	v_and_b32_e32 v187, 0xffff0000, v69
	v_cvt_pk_f32_fp8_e32 v[160:161], v122
	v_cvt_pk_f32_fp8_sdwa v[162:163], v122 src0_sel:WORD_1
	v_pk_fma_f32 v[184:185], v[160:161], s[10:11], v[184:185] op_sel_hi:[1,0,1]
	v_pk_fma_f32 v[186:187], v[162:163], s[10:11], v[186:187] op_sel_hi:[1,0,1]
	v_cvt_pk_f32_fp8_e32 v[164:165], v126
	v_cvt_pk_f32_fp8_sdwa v[166:167], v126 src0_sel:WORD_1
	v_pk_fma_f32 v[184:185], v[164:165], s[10:11], v[184:185] op_sel_hi:[1,0,1]
	v_pk_fma_f32 v[186:187], v[166:167], s[10:11], v[186:187] op_sel_hi:[1,0,1]
	v_cvt_pk_f32_fp8_e32 v[168:169], v130
	v_cvt_pk_f32_fp8_sdwa v[170:171], v130 src0_sel:WORD_1
	v_pk_fma_f32 v[184:185], v[168:169], s[10:11], v[184:185] op_sel_hi:[1,0,1]
	v_pk_fma_f32 v[186:187], v[170:171], s[10:11], v[186:187] op_sel_hi:[1,0,1]
	v_cvt_pk_f32_fp8_e32 v[172:173], v134
	v_cvt_pk_f32_fp8_sdwa v[174:175], v134 src0_sel:WORD_1
	v_pk_fma_f32 v[184:185], v[172:173], s[10:11], v[184:185] op_sel_hi:[1,0,1]
	v_pk_fma_f32 v[186:187], v[174:175], s[10:11], v[186:187] op_sel_hi:[1,0,1]
	global_store_dwordx4 v159, v[184:187], s[4:5] offset:2048
	v_lshlrev_b32_e32 v188, 16, v70
	v_and_b32_e32 v189, 0xffff0000, v70
	v_lshlrev_b32_e32 v190, 16, v71
	v_and_b32_e32 v191, 0xffff0000, v71
	v_cvt_pk_f32_fp8_e32 v[160:161], v123
	v_cvt_pk_f32_fp8_sdwa v[162:163], v123 src0_sel:WORD_1
	v_pk_fma_f32 v[188:189], v[160:161], s[10:11], v[188:189] op_sel_hi:[1,0,1]
	v_pk_fma_f32 v[190:191], v[162:163], s[10:11], v[190:191] op_sel_hi:[1,0,1]
	v_cvt_pk_f32_fp8_e32 v[164:165], v127
	v_cvt_pk_f32_fp8_sdwa v[166:167], v127 src0_sel:WORD_1
	v_pk_fma_f32 v[188:189], v[164:165], s[10:11], v[188:189] op_sel_hi:[1,0,1]
	v_pk_fma_f32 v[190:191], v[166:167], s[10:11], v[190:191] op_sel_hi:[1,0,1]
	v_cvt_pk_f32_fp8_e32 v[168:169], v131
	v_cvt_pk_f32_fp8_sdwa v[170:171], v131 src0_sel:WORD_1
	v_pk_fma_f32 v[188:189], v[168:169], s[10:11], v[188:189] op_sel_hi:[1,0,1]
	v_pk_fma_f32 v[190:191], v[170:171], s[10:11], v[190:191] op_sel_hi:[1,0,1]
	v_cvt_pk_f32_fp8_e32 v[172:173], v135
	v_cvt_pk_f32_fp8_sdwa v[174:175], v135 src0_sel:WORD_1
	v_pk_fma_f32 v[188:189], v[172:173], s[10:11], v[188:189] op_sel_hi:[1,0,1]
	v_pk_fma_f32 v[190:191], v[174:175], s[10:11], v[190:191] op_sel_hi:[1,0,1]
	global_store_dwordx4 v159, v[188:191], s[4:5] offset:3072
	s_waitcnt vmcnt(28)
	v_lshl_add_u32 v200, v8, 2, s23
	v_lshl_add_u32 v201, v9, 2, s23
	v_lshl_add_u32 v202, v10, 2, s23
	v_lshl_add_u32 v203, v11, 2, s23
	v_lshl_add_u32 v204, v12, 2, s23
	v_lshl_add_u32 v205, v13, 2, s23
	v_lshl_add_u32 v206, v14, 2, s23
	v_lshl_add_u32 v207, v15, 2, s23
	v_lshl_add_u32 v208, v16, 2, s23
	v_lshl_add_u32 v209, v17, 2, s23
	v_lshl_add_u32 v210, v18, 2, s23
	v_lshl_add_u32 v211, v19, 2, s23
	v_lshl_add_u32 v212, v20, 2, s23
	v_lshl_add_u32 v213, v21, 2, s23
	v_lshl_add_u32 v214, v22, 2, s23
	v_lshl_add_u32 v215, v23, 2, s23
	ds_read_b32 v136, v200
	ds_read_b32 v137, v201
	ds_read_b32 v138, v202
	ds_read_b32 v139, v203
	ds_read_b32 v140, v204
	ds_read_b32 v141, v205
	ds_read_b32 v142, v206
	ds_read_b32 v143, v207
	ds_read_b32 v144, v208
	ds_read_b32 v145, v209
	ds_read_b32 v146, v210
	ds_read_b32 v147, v211
	ds_read_b32 v148, v212
	ds_read_b32 v149, v213
	ds_read_b32 v150, v214
	ds_read_b32 v151, v215
	v_add_u32_e32 v192, 0x3000, v3
	v_lshl_add_u32 v156, v192, 13, v6
	v_add_u32_e32 v193, 0x3400, v3
	v_lshl_add_u32 v157, v193, 13, v6
	v_add_u32_e32 v194, 0x3800, v3
	v_lshl_add_u32 v158, v194, 13, v6
	v_add_u32_e32 v195, 0x3c00, v3
	v_lshl_add_u32 v159, v195, 13, v6
	s_waitcnt lgkmcnt(12)
; __device__ __forceinline__ float bf_lo(unsigned w) { return __uint_as_float(w << 16); }
; __device__ __forceinline__ float bf_hi(unsigned w) { return __uint_as_float(w & 0xffff0000u); }
; __global__ void __launch_bounds__(512, 2) fwd_kernel(Params p) {
;     ...
;             for (int u = 0; u < UN; ++u)
; #pragma unroll
;                 for (int k = 0; k < 4; ++k) { const int pos = ts[ee[u][k]] * 256 + rk[u][k]; y[u][k] = *(const u32x4*)(Yb + (size_t)pos * DM + cc[u]); }
; #pragma unroll
;             for (int u = 0; u < UN; ++u) {
;                 f32x4 a[4];
;                 a[0] = (f32x4){bf_lo(xa[u].x), bf_hi(xa[u].x), bf_lo(xa[u].y), bf_hi(xa[u].y)}; a[1] = (f32x4){bf_lo(xa[u].z), bf_hi(xa[u].z), bf_lo(xa[u].w), bf_hi(xa[u].w)};
;                 a[2] = (f32x4){bf_lo(xb[u].x), bf_hi(xb[u].x), bf_lo(xb[u].y), bf_hi(xb[u].y)}; a[3] = (f32x4){bf_lo(xb[u].z), bf_hi(xb[u].z), bf_lo(xb[u].w), bf_hi(xb[u].w)};
; #pragma unroll
;                 for (int k = 0; k < 4; ++k)
; #pragma unroll
;                     for (int q = 0; q < 4; ++q) { const f32x2 lo = __builtin_amdgcn_cvt_pk_f32_fp8((int)y[u][k][q], false), hi = __builtin_amdgcn_cvt_pk_f32_fp8((int)y[u][k][q], true);
;                         a[q].x += lo.x * (1.0f / Y8_SCALE); a[q].y += lo.y * (1.0f / Y8_SCALE); a[q].z += hi.x * (1.0f / Y8_SCALE); a[q].w += hi.y * (1.0f / Y8_SCALE); }
;                 if (it0 + u * NGT < NI) { float* op = p.out + (size_t)mm[u] * DM + cc[u];
; #pragma unroll
;                     for (int q = 0; q < 4; ++q) *(f32x4*)(op + 4 * q) = a[q]; }
	v_lshl_add_u32 v136, v136, 8, v24
	v_lshl_add_u32 v137, v137, 8, v25
	v_lshl_add_u32 v138, v138, 8, v26
	v_lshl_add_u32 v139, v139, 8, v27
	v_lshl_add_u32 v136, v136, 11, v4
	v_lshl_add_u32 v137, v137, 11, v4
	v_lshl_add_u32 v138, v138, 11, v4
	v_lshl_add_u32 v139, v139, 11, v4
	global_load_dword v72, v136, s[6:7]
	global_load_dword v73, v136, s[6:7] offset:256
	global_load_dword v74, v136, s[6:7] offset:512
	global_load_dword v75, v136, s[6:7] offset:768
	global_load_dword v76, v137, s[6:7]
	global_load_dword v77, v137, s[6:7] offset:256
	global_load_dword v78, v137, s[6:7] offset:512
	global_load_dword v79, v137, s[6:7] offset:768
	global_load_dword v80, v138, s[6:7]
	global_load_dword v81, v138, s[6:7] offset:256
	global_load_dword v82, v138, s[6:7] offset:512
	global_load_dword v83, v138, s[6:7] offset:768
	global_load_dword v84, v139, s[6:7]
	global_load_dword v85, v139, s[6:7] offset:256
	global_load_dword v86, v139, s[6:7] offset:512
	global_load_dword v87, v139, s[6:7] offset:768
	s_waitcnt lgkmcnt(8)
	v_lshl_add_u32 v140, v140, 8, v28
	v_lshl_add_u32 v141, v141, 8, v29
	v_lshl_add_u32 v142, v142, 8, v30
	v_lshl_add_u32 v143, v143, 8, v31
	v_lshl_add_u32 v140, v140, 11, v4
	v_lshl_add_u32 v141, v141, 11, v4
	v_lshl_add_u32 v142, v142, 11, v4
	v_lshl_add_u32 v143, v143, 11, v4
	global_load_dword v88, v140, s[6:7]
	global_load_dword v89, v140, s[6:7] offset:256
	global_load_dword v90, v140, s[6:7] offset:512
	global_load_dword v91, v140, s[6:7] offset:768
	global_load_dword v92, v141, s[6:7]
	global_load_dword v93, v141, s[6:7] offset:256
	global_load_dword v94, v141, s[6:7] offset:512
	global_load_dword v95, v141, s[6:7] offset:768
	global_load_dword v96, v142, s[6:7]
	global_load_dword v97, v142, s[6:7] offset:256
	global_load_dword v98, v142, s[6:7] offset:512
	global_load_dword v99, v142, s[6:7] offset:768
	global_load_dword v100, v143, s[6:7]
	global_load_dword v101, v143, s[6:7] offset:256
	global_load_dword v102, v143, s[6:7] offset:512
	global_load_dword v103, v143, s[6:7] offset:768
	s_waitcnt lgkmcnt(4)
	v_lshl_add_u32 v144, v144, 8, v32
	v_lshl_add_u32 v145, v145, 8, v33
	v_lshl_add_u32 v146, v146, 8, v34
	v_lshl_add_u32 v147, v147, 8, v35
	v_lshl_add_u32 v144, v144, 11, v4
	v_lshl_add_u32 v145, v145, 11, v4
	v_lshl_add_u32 v146, v146, 11, v4
	v_lshl_add_u32 v147, v147, 11, v4
	global_load_dword v104, v144, s[6:7]
	global_load_dword v105, v144, s[6:7] offset:256
	global_load_dword v106, v144, s[6:7] offset:512
	global_load_dword v107, v144, s[6:7] offset:768
	global_load_dword v108, v145, s[6:7]
	global_load_dword v109, v145, s[6:7] offset:256
	global_load_dword v110, v145, s[6:7] offset:512
	global_load_dword v111, v145, s[6:7] offset:768
	global_load_dword v112, v146, s[6:7]
	global_load_dword v113, v146, s[6:7] offset:256
	global_load_dword v114, v146, s[6:7] offset:512
	global_load_dword v115, v146, s[6:7] offset:768
	global_load_dword v116, v147, s[6:7]
	global_load_dword v117, v147, s[6:7] offset:256
	global_load_dword v118, v147, s[6:7] offset:512
	global_load_dword v119, v147, s[6:7] offset:768
	s_waitcnt lgkmcnt(0)
	v_lshl_add_u32 v148, v148, 8, v36
	v_lshl_add_u32 v149, v149, 8, v37
	v_lshl_add_u32 v150, v150, 8, v38
	v_lshl_add_u32 v151, v151, 8, v39
	v_lshl_add_u32 v148, v148, 11, v4
	v_lshl_add_u32 v149, v149, 11, v4
	v_lshl_add_u32 v150, v150, 11, v4
	v_lshl_add_u32 v151, v151, 11, v4
	global_load_dword v120, v148, s[6:7]
	global_load_dword v121, v148, s[6:7] offset:256
	global_load_dword v122, v148, s[6:7] offset:512
	global_load_dword v123, v148, s[6:7] offset:768
	global_load_dword v124, v149, s[6:7]
	global_load_dword v125, v149, s[6:7] offset:256
	global_load_dword v126, v149, s[6:7] offset:512
	global_load_dword v127, v149, s[6:7] offset:768
	global_load_dword v128, v150, s[6:7]
	global_load_dword v129, v150, s[6:7] offset:256
	global_load_dword v130, v150, s[6:7] offset:512
	global_load_dword v131, v150, s[6:7] offset:768
	global_load_dword v132, v151, s[6:7]
	global_load_dword v133, v151, s[6:7] offset:256
	global_load_dword v134, v151, s[6:7] offset:512
	global_load_dword v135, v151, s[6:7] offset:768
	s_waitcnt vmcnt(48)
	v_lshlrev_b32_e32 v176, 16, v216
	v_and_b32_e32 v177, 0xffff0000, v216
	v_lshlrev_b32_e32 v178, 16, v217
	v_and_b32_e32 v179, 0xffff0000, v217
	v_cvt_pk_f32_fp8_e32 v[160:161], v72
	v_cvt_pk_f32_fp8_sdwa v[162:163], v72 src0_sel:WORD_1
	v_pk_fma_f32 v[176:177], v[160:161], s[10:11], v[176:177] op_sel_hi:[1,0,1]
	v_pk_fma_f32 v[178:179], v[162:163], s[10:11], v[178:179] op_sel_hi:[1,0,1]
	v_cvt_pk_f32_fp8_e32 v[164:165], v76
	v_cvt_pk_f32_fp8_sdwa v[166:167], v76 src0_sel:WORD_1
	v_pk_fma_f32 v[176:177], v[164:165], s[10:11], v[176:177] op_sel_hi:[1,0,1]
	v_pk_fma_f32 v[178:179], v[166:167], s[10:11], v[178:179] op_sel_hi:[1,0,1]
	v_cvt_pk_f32_fp8_e32 v[168:169], v80
	v_cvt_pk_f32_fp8_sdwa v[170:171], v80 src0_sel:WORD_1
	v_pk_fma_f32 v[176:177], v[168:169], s[10:11], v[176:177] op_sel_hi:[1,0,1]
	v_pk_fma_f32 v[178:179], v[170:171], s[10:11], v[178:179] op_sel_hi:[1,0,1]
	v_cvt_pk_f32_fp8_e32 v[172:173], v84
	v_cvt_pk_f32_fp8_sdwa v[174:175], v84 src0_sel:WORD_1
	v_pk_fma_f32 v[176:177], v[172:173], s[10:11], v[176:177] op_sel_hi:[1,0,1]
	v_pk_fma_f32 v[178:179], v[174:175], s[10:11], v[178:179] op_sel_hi:[1,0,1]
	global_store_dwordx4 v156, v[176:179], s[4:5]
	v_lshlrev_b32_e32 v180, 16, v218
	v_and_b32_e32 v181, 0xffff0000, v218
	v_lshlrev_b32_e32 v182, 16, v219
	v_and_b32_e32 v183, 0xffff0000, v219
	v_cvt_pk_f32_fp8_e32 v[160:161], v73
	v_cvt_pk_f32_fp8_sdwa v[162:163], v73 src0_sel:WORD_1
	v_pk_fma_f32 v[180:181], v[160:161], s[10:11], v[180:181] op_sel_hi:[1,0,1]
; __device__ __forceinline__ float bf_lo(unsigned w) { return __uint_as_float(w << 16); }
; __device__ __forceinline__ float bf_hi(unsigned w) { return __uint_as_float(w & 0xffff0000u); }
; __global__ void __launch_bounds__(512, 2) fwd_kernel(Params p) {
;     ...
;             for (int u = 0; u < UN; ++u) {
;                 f32x4 a[4];
;                 a[0] = (f32x4){bf_lo(xa[u].x), bf_hi(xa[u].x), bf_lo(xa[u].y), bf_hi(xa[u].y)}; a[1] = (f32x4){bf_lo(xa[u].z), bf_hi(xa[u].z), bf_lo(xa[u].w), bf_hi(xa[u].w)};
;                 a[2] = (f32x4){bf_lo(xb[u].x), bf_hi(xb[u].x), bf_lo(xb[u].y), bf_hi(xb[u].y)}; a[3] = (f32x4){bf_lo(xb[u].z), bf_hi(xb[u].z), bf_lo(xb[u].w), bf_hi(xb[u].w)};
; #pragma unroll
;                 for (int k = 0; k < 4; ++k)
; #pragma unroll
;                     for (int q = 0; q < 4; ++q) { const f32x2 lo = __builtin_amdgcn_cvt_pk_f32_fp8((int)y[u][k][q], false), hi = __builtin_amdgcn_cvt_pk_f32_fp8((int)y[u][k][q], true);
;                         a[q].x += lo.x * (1.0f / Y8_SCALE); a[q].y += lo.y * (1.0f / Y8_SCALE); a[q].z += hi.x * (1.0f / Y8_SCALE); a[q].w += hi.y * (1.0f / Y8_SCALE); }
;                 if (it0 + u * NGT < NI) { float* op = p.out + (size_t)mm[u] * DM + cc[u];
; #pragma unroll
;                     for (int q = 0; q < 4; ++q) *(f32x4*)(op + 4 * q) = a[q]; }
	v_pk_fma_f32 v[182:183], v[162:163], s[10:11], v[182:183] op_sel_hi:[1,0,1]
	v_cvt_pk_f32_fp8_e32 v[164:165], v77
	v_cvt_pk_f32_fp8_sdwa v[166:167], v77 src0_sel:WORD_1
	v_pk_fma_f32 v[180:181], v[164:165], s[10:11], v[180:181] op_sel_hi:[1,0,1]
	v_pk_fma_f32 v[182:183], v[166:167], s[10:11], v[182:183] op_sel_hi:[1,0,1]
	v_cvt_pk_f32_fp8_e32 v[168:169], v81
	v_cvt_pk_f32_fp8_sdwa v[170:171], v81 src0_sel:WORD_1
	v_pk_fma_f32 v[180:181], v[168:169], s[10:11], v[180:181] op_sel_hi:[1,0,1]
	v_pk_fma_f32 v[182:183], v[170:171], s[10:11], v[182:183] op_sel_hi:[1,0,1]
	v_cvt_pk_f32_fp8_e32 v[172:173], v85
	v_cvt_pk_f32_fp8_sdwa v[174:175], v85 src0_sel:WORD_1
	v_pk_fma_f32 v[180:181], v[172:173], s[10:11], v[180:181] op_sel_hi:[1,0,1]
	v_pk_fma_f32 v[182:183], v[174:175], s[10:11], v[182:183] op_sel_hi:[1,0,1]
	global_store_dwordx4 v156, v[180:183], s[4:5] offset:1024
	v_lshlrev_b32_e32 v184, 16, v220
	v_and_b32_e32 v185, 0xffff0000, v220
	v_lshlrev_b32_e32 v186, 16, v221
	v_and_b32_e32 v187, 0xffff0000, v221
	v_cvt_pk_f32_fp8_e32 v[160:161], v74
	v_cvt_pk_f32_fp8_sdwa v[162:163], v74 src0_sel:WORD_1
	v_pk_fma_f32 v[184:185], v[160:161], s[10:11], v[184:185] op_sel_hi:[1,0,1]
	v_pk_fma_f32 v[186:187], v[162:163], s[10:11], v[186:187] op_sel_hi:[1,0,1]
	v_cvt_pk_f32_fp8_e32 v[164:165], v78
	v_cvt_pk_f32_fp8_sdwa v[166:167], v78 src0_sel:WORD_1
	v_pk_fma_f32 v[184:185], v[164:165], s[10:11], v[184:185] op_sel_hi:[1,0,1]
	v_pk_fma_f32 v[186:187], v[166:167], s[10:11], v[186:187] op_sel_hi:[1,0,1]
	v_cvt_pk_f32_fp8_e32 v[168:169], v82
	v_cvt_pk_f32_fp8_sdwa v[170:171], v82 src0_sel:WORD_1
	v_pk_fma_f32 v[184:185], v[168:169], s[10:11], v[184:185] op_sel_hi:[1,0,1]
	v_pk_fma_f32 v[186:187], v[170:171], s[10:11], v[186:187] op_sel_hi:[1,0,1]
	v_cvt_pk_f32_fp8_e32 v[172:173], v86
	v_cvt_pk_f32_fp8_sdwa v[174:175], v86 src0_sel:WORD_1
	v_pk_fma_f32 v[184:185], v[172:173], s[10:11], v[184:185] op_sel_hi:[1,0,1]
	v_pk_fma_f32 v[186:187], v[174:175], s[10:11], v[186:187] op_sel_hi:[1,0,1]
	global_store_dwordx4 v156, v[184:187], s[4:5] offset:2048
	v_lshlrev_b32_e32 v188, 16, v222
	v_and_b32_e32 v189, 0xffff0000, v222
	v_lshlrev_b32_e32 v190, 16, v223
	v_and_b32_e32 v191, 0xffff0000, v223
	v_cvt_pk_f32_fp8_e32 v[160:161], v75
	v_cvt_pk_f32_fp8_sdwa v[162:163], v75 src0_sel:WORD_1
	v_pk_fma_f32 v[188:189], v[160:161], s[10:11], v[188:189] op_sel_hi:[1,0,1]
	v_pk_fma_f32 v[190:191], v[162:163], s[10:11], v[190:191] op_sel_hi:[1,0,1]
	v_cvt_pk_f32_fp8_e32 v[164:165], v79
	v_cvt_pk_f32_fp8_sdwa v[166:167], v79 src0_sel:WORD_1
	v_pk_fma_f32 v[188:189], v[164:165], s[10:11], v[188:189] op_sel_hi:[1,0,1]
	v_pk_fma_f32 v[190:191], v[166:167], s[10:11], v[190:191] op_sel_hi:[1,0,1]
	v_cvt_pk_f32_fp8_e32 v[168:169], v83
	v_cvt_pk_f32_fp8_sdwa v[170:171], v83 src0_sel:WORD_1
	v_pk_fma_f32 v[188:189], v[168:169], s[10:11], v[188:189] op_sel_hi:[1,0,1]
	v_pk_fma_f32 v[190:191], v[170:171], s[10:11], v[190:191] op_sel_hi:[1,0,1]
	v_cvt_pk_f32_fp8_e32 v[172:173], v87
	v_cvt_pk_f32_fp8_sdwa v[174:175], v87 src0_sel:WORD_1
	v_pk_fma_f32 v[188:189], v[172:173], s[10:11], v[188:189] op_sel_hi:[1,0,1]
	v_pk_fma_f32 v[190:191], v[174:175], s[10:11], v[190:191] op_sel_hi:[1,0,1]
	global_store_dwordx4 v156, v[188:191], s[4:5] offset:3072
	s_waitcnt vmcnt(36)
	v_lshlrev_b32_e32 v176, 16, v224
	v_and_b32_e32 v177, 0xffff0000, v224
	v_lshlrev_b32_e32 v178, 16, v225
	v_and_b32_e32 v179, 0xffff0000, v225
	v_cvt_pk_f32_fp8_e32 v[160:161], v88
	v_cvt_pk_f32_fp8_sdwa v[162:163], v88 src0_sel:WORD_1
	v_pk_fma_f32 v[176:177], v[160:161], s[10:11], v[176:177] op_sel_hi:[1,0,1]
	v_pk_fma_f32 v[178:179], v[162:163], s[10:11], v[178:179] op_sel_hi:[1,0,1]
	v_cvt_pk_f32_fp8_e32 v[164:165], v92
	v_cvt_pk_f32_fp8_sdwa v[166:167], v92 src0_sel:WORD_1
	v_pk_fma_f32 v[176:177], v[164:165], s[10:11], v[176:177] op_sel_hi:[1,0,1]
	v_pk_fma_f32 v[178:179], v[166:167], s[10:11], v[178:179] op_sel_hi:[1,0,1]
	v_cvt_pk_f32_fp8_e32 v[168:169], v96
	v_cvt_pk_f32_fp8_sdwa v[170:171], v96 src0_sel:WORD_1
	v_pk_fma_f32 v[176:177], v[168:169], s[10:11], v[176:177] op_sel_hi:[1,0,1]
	v_pk_fma_f32 v[178:179], v[170:171], s[10:11], v[178:179] op_sel_hi:[1,0,1]
	v_cvt_pk_f32_fp8_e32 v[172:173], v100
	v_cvt_pk_f32_fp8_sdwa v[174:175], v100 src0_sel:WORD_1
	v_pk_fma_f32 v[176:177], v[172:173], s[10:11], v[176:177] op_sel_hi:[1,0,1]
	v_pk_fma_f32 v[178:179], v[174:175], s[10:11], v[178:179] op_sel_hi:[1,0,1]
	global_store_dwordx4 v157, v[176:179], s[4:5]
	v_lshlrev_b32_e32 v180, 16, v226
	v_and_b32_e32 v181, 0xffff0000, v226
	v_lshlrev_b32_e32 v182, 16, v227
	v_and_b32_e32 v183, 0xffff0000, v227
	v_cvt_pk_f32_fp8_e32 v[160:161], v89
	v_cvt_pk_f32_fp8_sdwa v[162:163], v89 src0_sel:WORD_1
	v_pk_fma_f32 v[180:181], v[160:161], s[10:11], v[180:181] op_sel_hi:[1,0,1]
	v_pk_fma_f32 v[182:183], v[162:163], s[10:11], v[182:183] op_sel_hi:[1,0,1]
	v_cvt_pk_f32_fp8_e32 v[164:165], v93
	v_cvt_pk_f32_fp8_sdwa v[166:167], v93 src0_sel:WORD_1
	v_pk_fma_f32 v[180:181], v[164:165], s[10:11], v[180:181] op_sel_hi:[1,0,1]
	v_pk_fma_f32 v[182:183], v[166:167], s[10:11], v[182:183] op_sel_hi:[1,0,1]
	v_cvt_pk_f32_fp8_e32 v[168:169], v97
	v_cvt_pk_f32_fp8_sdwa v[170:171], v97 src0_sel:WORD_1
	v_pk_fma_f32 v[180:181], v[168:169], s[10:11], v[180:181] op_sel_hi:[1,0,1]
	v_pk_fma_f32 v[182:183], v[170:171], s[10:11], v[182:183] op_sel_hi:[1,0,1]
	v_cvt_pk_f32_fp8_e32 v[172:173], v101
	v_cvt_pk_f32_fp8_sdwa v[174:175], v101 src0_sel:WORD_1
	v_pk_fma_f32 v[180:181], v[172:173], s[10:11], v[180:181] op_sel_hi:[1,0,1]
	v_pk_fma_f32 v[182:183], v[174:175], s[10:11], v[182:183] op_sel_hi:[1,0,1]
	global_store_dwordx4 v157, v[180:183], s[4:5] offset:1024
; __device__ __forceinline__ float bf_lo(unsigned w) { return __uint_as_float(w << 16); }
; __device__ __forceinline__ float bf_hi(unsigned w) { return __uint_as_float(w & 0xffff0000u); }
; __global__ void __launch_bounds__(512, 2) fwd_kernel(Params p) {
;     ...
;             for (int u = 0; u < UN; ++u) {
;                 f32x4 a[4];
;                 a[0] = (f32x4){bf_lo(xa[u].x), bf_hi(xa[u].x), bf_lo(xa[u].y), bf_hi(xa[u].y)}; a[1] = (f32x4){bf_lo(xa[u].z), bf_hi(xa[u].z), bf_lo(xa[u].w), bf_hi(xa[u].w)};
;                 a[2] = (f32x4){bf_lo(xb[u].x), bf_hi(xb[u].x), bf_lo(xb[u].y), bf_hi(xb[u].y)}; a[3] = (f32x4){bf_lo(xb[u].z), bf_hi(xb[u].z), bf_lo(xb[u].w), bf_hi(xb[u].w)};
; #pragma unroll
;                 for (int k = 0; k < 4; ++k)
; #pragma unroll
;                     for (int q = 0; q < 4; ++q) { const f32x2 lo = __builtin_amdgcn_cvt_pk_f32_fp8((int)y[u][k][q], false), hi = __builtin_amdgcn_cvt_pk_f32_fp8((int)y[u][k][q], true);
;                         a[q].x += lo.x * (1.0f / Y8_SCALE); a[q].y += lo.y * (1.0f / Y8_SCALE); a[q].z += hi.x * (1.0f / Y8_SCALE); a[q].w += hi.y * (1.0f / Y8_SCALE); }
;                 if (it0 + u * NGT < NI) { float* op = p.out + (size_t)mm[u] * DM + cc[u];
; #pragma unroll
;                     for (int q = 0; q < 4; ++q) *(f32x4*)(op + 4 * q) = a[q]; }
	v_lshlrev_b32_e32 v184, 16, v228
	v_and_b32_e32 v185, 0xffff0000, v228
	v_lshlrev_b32_e32 v186, 16, v229
	v_and_b32_e32 v187, 0xffff0000, v229
	v_cvt_pk_f32_fp8_e32 v[160:161], v90
	v_cvt_pk_f32_fp8_sdwa v[162:163], v90 src0_sel:WORD_1
	v_pk_fma_f32 v[184:185], v[160:161], s[10:11], v[184:185] op_sel_hi:[1,0,1]
	v_pk_fma_f32 v[186:187], v[162:163], s[10:11], v[186:187] op_sel_hi:[1,0,1]
	v_cvt_pk_f32_fp8_e32 v[164:165], v94
	v_cvt_pk_f32_fp8_sdwa v[166:167], v94 src0_sel:WORD_1
	v_pk_fma_f32 v[184:185], v[164:165], s[10:11], v[184:185] op_sel_hi:[1,0,1]
	v_pk_fma_f32 v[186:187], v[166:167], s[10:11], v[186:187] op_sel_hi:[1,0,1]
	v_cvt_pk_f32_fp8_e32 v[168:169], v98
	v_cvt_pk_f32_fp8_sdwa v[170:171], v98 src0_sel:WORD_1
	v_pk_fma_f32 v[184:185], v[168:169], s[10:11], v[184:185] op_sel_hi:[1,0,1]
	v_pk_fma_f32 v[186:187], v[170:171], s[10:11], v[186:187] op_sel_hi:[1,0,1]
	v_cvt_pk_f32_fp8_e32 v[172:173], v102
	v_cvt_pk_f32_fp8_sdwa v[174:175], v102 src0_sel:WORD_1
	v_pk_fma_f32 v[184:185], v[172:173], s[10:11], v[184:185] op_sel_hi:[1,0,1]
	v_pk_fma_f32 v[186:187], v[174:175], s[10:11], v[186:187] op_sel_hi:[1,0,1]
	global_store_dwordx4 v157, v[184:187], s[4:5] offset:2048
	v_lshlrev_b32_e32 v188, 16, v230
	v_and_b32_e32 v189, 0xffff0000, v230
	v_lshlrev_b32_e32 v190, 16, v231
	v_and_b32_e32 v191, 0xffff0000, v231
	v_cvt_pk_f32_fp8_e32 v[160:161], v91
	v_cvt_pk_f32_fp8_sdwa v[162:163], v91 src0_sel:WORD_1
	v_pk_fma_f32 v[188:189], v[160:161], s[10:11], v[188:189] op_sel_hi:[1,0,1]
	v_pk_fma_f32 v[190:191], v[162:163], s[10:11], v[190:191] op_sel_hi:[1,0,1]
	v_cvt_pk_f32_fp8_e32 v[164:165], v95
	v_cvt_pk_f32_fp8_sdwa v[166:167], v95 src0_sel:WORD_1
	v_pk_fma_f32 v[188:189], v[164:165], s[10:11], v[188:189] op_sel_hi:[1,0,1]
	v_pk_fma_f32 v[190:191], v[166:167], s[10:11], v[190:191] op_sel_hi:[1,0,1]
	v_cvt_pk_f32_fp8_e32 v[168:169], v99
	v_cvt_pk_f32_fp8_sdwa v[170:171], v99 src0_sel:WORD_1
	v_pk_fma_f32 v[188:189], v[168:169], s[10:11], v[188:189] op_sel_hi:[1,0,1]
	v_pk_fma_f32 v[190:191], v[170:171], s[10:11], v[190:191] op_sel_hi:[1,0,1]
	v_cvt_pk_f32_fp8_e32 v[172:173], v103
	v_cvt_pk_f32_fp8_sdwa v[174:175], v103 src0_sel:WORD_1
	v_pk_fma_f32 v[188:189], v[172:173], s[10:11], v[188:189] op_sel_hi:[1,0,1]
	v_pk_fma_f32 v[190:191], v[174:175], s[10:11], v[190:191] op_sel_hi:[1,0,1]
	global_store_dwordx4 v157, v[188:191], s[4:5] offset:3072
	s_waitcnt vmcnt(24)
	v_lshlrev_b32_e32 v176, 16, v232
	v_and_b32_e32 v177, 0xffff0000, v232
	v_lshlrev_b32_e32 v178, 16, v233
	v_and_b32_e32 v179, 0xffff0000, v233
	v_cvt_pk_f32_fp8_e32 v[160:161], v104
	v_cvt_pk_f32_fp8_sdwa v[162:163], v104 src0_sel:WORD_1
	v_pk_fma_f32 v[176:177], v[160:161], s[10:11], v[176:177] op_sel_hi:[1,0,1]
	v_pk_fma_f32 v[178:179], v[162:163], s[10:11], v[178:179] op_sel_hi:[1,0,1]
	v_cvt_pk_f32_fp8_e32 v[164:165], v108
	v_cvt_pk_f32_fp8_sdwa v[166:167], v108 src0_sel:WORD_1
	v_pk_fma_f32 v[176:177], v[164:165], s[10:11], v[176:177] op_sel_hi:[1,0,1]
	v_pk_fma_f32 v[178:179], v[166:167], s[10:11], v[178:179] op_sel_hi:[1,0,1]
	v_cvt_pk_f32_fp8_e32 v[168:169], v112
	v_cvt_pk_f32_fp8_sdwa v[170:171], v112 src0_sel:WORD_1
	v_pk_fma_f32 v[176:177], v[168:169], s[10:11], v[176:177] op_sel_hi:[1,0,1]
	v_pk_fma_f32 v[178:179], v[170:171], s[10:11], v[178:179] op_sel_hi:[1,0,1]
	v_cvt_pk_f32_fp8_e32 v[172:173], v116
	v_cvt_pk_f32_fp8_sdwa v[174:175], v116 src0_sel:WORD_1
	v_pk_fma_f32 v[176:177], v[172:173], s[10:11], v[176:177] op_sel_hi:[1,0,1]
	v_pk_fma_f32 v[178:179], v[174:175], s[10:11], v[178:179] op_sel_hi:[1,0,1]
	global_store_dwordx4 v158, v[176:179], s[4:5]
	v_lshlrev_b32_e32 v180, 16, v234
	v_and_b32_e32 v181, 0xffff0000, v234
	v_lshlrev_b32_e32 v182, 16, v235
	v_and_b32_e32 v183, 0xffff0000, v235
	v_cvt_pk_f32_fp8_e32 v[160:161], v105
	v_cvt_pk_f32_fp8_sdwa v[162:163], v105 src0_sel:WORD_1
	v_pk_fma_f32 v[180:181], v[160:161], s[10:11], v[180:181] op_sel_hi:[1,0,1]
	v_pk_fma_f32 v[182:183], v[162:163], s[10:11], v[182:183] op_sel_hi:[1,0,1]
	v_cvt_pk_f32_fp8_e32 v[164:165], v109
	v_cvt_pk_f32_fp8_sdwa v[166:167], v109 src0_sel:WORD_1
	v_pk_fma_f32 v[180:181], v[164:165], s[10:11], v[180:181] op_sel_hi:[1,0,1]
	v_pk_fma_f32 v[182:183], v[166:167], s[10:11], v[182:183] op_sel_hi:[1,0,1]
	v_cvt_pk_f32_fp8_e32 v[168:169], v113
	v_cvt_pk_f32_fp8_sdwa v[170:171], v113 src0_sel:WORD_1
	v_pk_fma_f32 v[180:181], v[168:169], s[10:11], v[180:181] op_sel_hi:[1,0,1]
	v_pk_fma_f32 v[182:183], v[170:171], s[10:11], v[182:183] op_sel_hi:[1,0,1]
	v_cvt_pk_f32_fp8_e32 v[172:173], v117
	v_cvt_pk_f32_fp8_sdwa v[174:175], v117 src0_sel:WORD_1
	v_pk_fma_f32 v[180:181], v[172:173], s[10:11], v[180:181] op_sel_hi:[1,0,1]
	v_pk_fma_f32 v[182:183], v[174:175], s[10:11], v[182:183] op_sel_hi:[1,0,1]
	global_store_dwordx4 v158, v[180:183], s[4:5] offset:1024
	v_lshlrev_b32_e32 v184, 16, v236
	v_and_b32_e32 v185, 0xffff0000, v236
	v_lshlrev_b32_e32 v186, 16, v237
	v_and_b32_e32 v187, 0xffff0000, v237
	v_cvt_pk_f32_fp8_e32 v[160:161], v106
	v_cvt_pk_f32_fp8_sdwa v[162:163], v106 src0_sel:WORD_1
	v_pk_fma_f32 v[184:185], v[160:161], s[10:11], v[184:185] op_sel_hi:[1,0,1]
	v_pk_fma_f32 v[186:187], v[162:163], s[10:11], v[186:187] op_sel_hi:[1,0,1]
	v_cvt_pk_f32_fp8_e32 v[164:165], v110
	v_cvt_pk_f32_fp8_sdwa v[166:167], v110 src0_sel:WORD_1
	v_pk_fma_f32 v[184:185], v[164:165], s[10:11], v[184:185] op_sel_hi:[1,0,1]
	v_pk_fma_f32 v[186:187], v[166:167], s[10:11], v[186:187] op_sel_hi:[1,0,1]
	v_cvt_pk_f32_fp8_e32 v[168:169], v114
	v_cvt_pk_f32_fp8_sdwa v[170:171], v114 src0_sel:WORD_1
	v_pk_fma_f32 v[184:185], v[168:169], s[10:11], v[184:185] op_sel_hi:[1,0,1]
; __device__ __forceinline__ float bf_lo(unsigned w) { return __uint_as_float(w << 16); }
; __device__ __forceinline__ float bf_hi(unsigned w) { return __uint_as_float(w & 0xffff0000u); }
; __global__ void __launch_bounds__(512, 2) fwd_kernel(Params p) {
;     ...
;             for (int u = 0; u < UN; ++u) {
;                 f32x4 a[4];
;                 a[0] = (f32x4){bf_lo(xa[u].x), bf_hi(xa[u].x), bf_lo(xa[u].y), bf_hi(xa[u].y)}; a[1] = (f32x4){bf_lo(xa[u].z), bf_hi(xa[u].z), bf_lo(xa[u].w), bf_hi(xa[u].w)};
;                 a[2] = (f32x4){bf_lo(xb[u].x), bf_hi(xb[u].x), bf_lo(xb[u].y), bf_hi(xb[u].y)}; a[3] = (f32x4){bf_lo(xb[u].z), bf_hi(xb[u].z), bf_lo(xb[u].w), bf_hi(xb[u].w)};
; #pragma unroll
;                 for (int k = 0; k < 4; ++k)
; #pragma unroll
;                     for (int q = 0; q < 4; ++q) { const f32x2 lo = __builtin_amdgcn_cvt_pk_f32_fp8((int)y[u][k][q], false), hi = __builtin_amdgcn_cvt_pk_f32_fp8((int)y[u][k][q], true);
;                         a[q].x += lo.x * (1.0f / Y8_SCALE); a[q].y += lo.y * (1.0f / Y8_SCALE); a[q].z += hi.x * (1.0f / Y8_SCALE); a[q].w += hi.y * (1.0f / Y8_SCALE); }
;                 if (it0 + u * NGT < NI) { float* op = p.out + (size_t)mm[u] * DM + cc[u];
; #pragma unroll
;                     for (int q = 0; q < 4; ++q) *(f32x4*)(op + 4 * q) = a[q]; }
	v_pk_fma_f32 v[186:187], v[170:171], s[10:11], v[186:187] op_sel_hi:[1,0,1]
	v_cvt_pk_f32_fp8_e32 v[172:173], v118
	v_cvt_pk_f32_fp8_sdwa v[174:175], v118 src0_sel:WORD_1
	v_pk_fma_f32 v[184:185], v[172:173], s[10:11], v[184:185] op_sel_hi:[1,0,1]
	v_pk_fma_f32 v[186:187], v[174:175], s[10:11], v[186:187] op_sel_hi:[1,0,1]
	global_store_dwordx4 v158, v[184:187], s[4:5] offset:2048
	v_lshlrev_b32_e32 v188, 16, v238
	v_and_b32_e32 v189, 0xffff0000, v238
	v_lshlrev_b32_e32 v190, 16, v239
	v_and_b32_e32 v191, 0xffff0000, v239
	v_cvt_pk_f32_fp8_e32 v[160:161], v107
	v_cvt_pk_f32_fp8_sdwa v[162:163], v107 src0_sel:WORD_1
	v_pk_fma_f32 v[188:189], v[160:161], s[10:11], v[188:189] op_sel_hi:[1,0,1]
	v_pk_fma_f32 v[190:191], v[162:163], s[10:11], v[190:191] op_sel_hi:[1,0,1]
	v_cvt_pk_f32_fp8_e32 v[164:165], v111
	v_cvt_pk_f32_fp8_sdwa v[166:167], v111 src0_sel:WORD_1
	v_pk_fma_f32 v[188:189], v[164:165], s[10:11], v[188:189] op_sel_hi:[1,0,1]
	v_pk_fma_f32 v[190:191], v[166:167], s[10:11], v[190:191] op_sel_hi:[1,0,1]
	v_cvt_pk_f32_fp8_e32 v[168:169], v115
	v_cvt_pk_f32_fp8_sdwa v[170:171], v115 src0_sel:WORD_1
	v_pk_fma_f32 v[188:189], v[168:169], s[10:11], v[188:189] op_sel_hi:[1,0,1]
	v_pk_fma_f32 v[190:191], v[170:171], s[10:11], v[190:191] op_sel_hi:[1,0,1]
	v_cvt_pk_f32_fp8_e32 v[172:173], v119
	v_cvt_pk_f32_fp8_sdwa v[174:175], v119 src0_sel:WORD_1
	v_pk_fma_f32 v[188:189], v[172:173], s[10:11], v[188:189] op_sel_hi:[1,0,1]
	v_pk_fma_f32 v[190:191], v[174:175], s[10:11], v[190:191] op_sel_hi:[1,0,1]
	global_store_dwordx4 v158, v[188:191], s[4:5] offset:3072
	s_waitcnt vmcnt(12)
	v_lshlrev_b32_e32 v176, 16, v240
	v_and_b32_e32 v177, 0xffff0000, v240
	v_lshlrev_b32_e32 v178, 16, v241
	v_and_b32_e32 v179, 0xffff0000, v241
	v_cvt_pk_f32_fp8_e32 v[160:161], v120
	v_cvt_pk_f32_fp8_sdwa v[162:163], v120 src0_sel:WORD_1
	v_pk_fma_f32 v[176:177], v[160:161], s[10:11], v[176:177] op_sel_hi:[1,0,1]
	v_pk_fma_f32 v[178:179], v[162:163], s[10:11], v[178:179] op_sel_hi:[1,0,1]
	v_cvt_pk_f32_fp8_e32 v[164:165], v124
	v_cvt_pk_f32_fp8_sdwa v[166:167], v124 src0_sel:WORD_1
	v_pk_fma_f32 v[176:177], v[164:165], s[10:11], v[176:177] op_sel_hi:[1,0,1]
	v_pk_fma_f32 v[178:179], v[166:167], s[10:11], v[178:179] op_sel_hi:[1,0,1]
	v_cvt_pk_f32_fp8_e32 v[168:169], v128
	v_cvt_pk_f32_fp8_sdwa v[170:171], v128 src0_sel:WORD_1
	v_pk_fma_f32 v[176:177], v[168:169], s[10:11], v[176:177] op_sel_hi:[1,0,1]
	v_pk_fma_f32 v[178:179], v[170:171], s[10:11], v[178:179] op_sel_hi:[1,0,1]
	v_cvt_pk_f32_fp8_e32 v[172:173], v132
	v_cvt_pk_f32_fp8_sdwa v[174:175], v132 src0_sel:WORD_1
	v_pk_fma_f32 v[176:177], v[172:173], s[10:11], v[176:177] op_sel_hi:[1,0,1]
	v_pk_fma_f32 v[178:179], v[174:175], s[10:11], v[178:179] op_sel_hi:[1,0,1]
	global_store_dwordx4 v159, v[176:179], s[4:5]
	v_lshlrev_b32_e32 v180, 16, v242
	v_and_b32_e32 v181, 0xffff0000, v242
	v_lshlrev_b32_e32 v182, 16, v243
	v_and_b32_e32 v183, 0xffff0000, v243
	v_cvt_pk_f32_fp8_e32 v[160:161], v121
	v_cvt_pk_f32_fp8_sdwa v[162:163], v121 src0_sel:WORD_1
	v_pk_fma_f32 v[180:181], v[160:161], s[10:11], v[180:181] op_sel_hi:[1,0,1]
	v_pk_fma_f32 v[182:183], v[162:163], s[10:11], v[182:183] op_sel_hi:[1,0,1]
	v_cvt_pk_f32_fp8_e32 v[164:165], v125
	v_cvt_pk_f32_fp8_sdwa v[166:167], v125 src0_sel:WORD_1
	v_pk_fma_f32 v[180:181], v[164:165], s[10:11], v[180:181] op_sel_hi:[1,0,1]
	v_pk_fma_f32 v[182:183], v[166:167], s[10:11], v[182:183] op_sel_hi:[1,0,1]
	v_cvt_pk_f32_fp8_e32 v[168:169], v129
	v_cvt_pk_f32_fp8_sdwa v[170:171], v129 src0_sel:WORD_1
	v_pk_fma_f32 v[180:181], v[168:169], s[10:11], v[180:181] op_sel_hi:[1,0,1]
	v_pk_fma_f32 v[182:183], v[170:171], s[10:11], v[182:183] op_sel_hi:[1,0,1]
	v_cvt_pk_f32_fp8_e32 v[172:173], v133
	v_cvt_pk_f32_fp8_sdwa v[174:175], v133 src0_sel:WORD_1
	v_pk_fma_f32 v[180:181], v[172:173], s[10:11], v[180:181] op_sel_hi:[1,0,1]
	v_pk_fma_f32 v[182:183], v[174:175], s[10:11], v[182:183] op_sel_hi:[1,0,1]
	global_store_dwordx4 v159, v[180:183], s[4:5] offset:1024
	v_lshlrev_b32_e32 v184, 16, v244
	v_and_b32_e32 v185, 0xffff0000, v244
	v_lshlrev_b32_e32 v186, 16, v245
	v_and_b32_e32 v187, 0xffff0000, v245
	v_cvt_pk_f32_fp8_e32 v[160:161], v122
	v_cvt_pk_f32_fp8_sdwa v[162:163], v122 src0_sel:WORD_1
	v_pk_fma_f32 v[184:185], v[160:161], s[10:11], v[184:185] op_sel_hi:[1,0,1]
	v_pk_fma_f32 v[186:187], v[162:163], s[10:11], v[186:187] op_sel_hi:[1,0,1]
	v_cvt_pk_f32_fp8_e32 v[164:165], v126
	v_cvt_pk_f32_fp8_sdwa v[166:167], v126 src0_sel:WORD_1
	v_pk_fma_f32 v[184:185], v[164:165], s[10:11], v[184:185] op_sel_hi:[1,0,1]
	v_pk_fma_f32 v[186:187], v[166:167], s[10:11], v[186:187] op_sel_hi:[1,0,1]
	v_cvt_pk_f32_fp8_e32 v[168:169], v130
	v_cvt_pk_f32_fp8_sdwa v[170:171], v130 src0_sel:WORD_1
	v_pk_fma_f32 v[184:185], v[168:169], s[10:11], v[184:185] op_sel_hi:[1,0,1]
	v_pk_fma_f32 v[186:187], v[170:171], s[10:11], v[186:187] op_sel_hi:[1,0,1]
	v_cvt_pk_f32_fp8_e32 v[172:173], v134
	v_cvt_pk_f32_fp8_sdwa v[174:175], v134 src0_sel:WORD_1
	v_pk_fma_f32 v[184:185], v[172:173], s[10:11], v[184:185] op_sel_hi:[1,0,1]
	v_pk_fma_f32 v[186:187], v[174:175], s[10:11], v[186:187] op_sel_hi:[1,0,1]
	global_store_dwordx4 v159, v[184:187], s[4:5] offset:2048
	v_lshlrev_b32_e32 v188, 16, v246
	v_and_b32_e32 v189, 0xffff0000, v246
	v_lshlrev_b32_e32 v190, 16, v247
	v_and_b32_e32 v191, 0xffff0000, v247
	v_cvt_pk_f32_fp8_e32 v[160:161], v123
	v_cvt_pk_f32_fp8_sdwa v[162:163], v123 src0_sel:WORD_1
	v_pk_fma_f32 v[188:189], v[160:161], s[10:11], v[188:189] op_sel_hi:[1,0,1]
	v_pk_fma_f32 v[190:191], v[162:163], s[10:11], v[190:191] op_sel_hi:[1,0,1]
	v_cvt_pk_f32_fp8_e32 v[164:165], v127
	v_cvt_pk_f32_fp8_sdwa v[166:167], v127 src0_sel:WORD_1
	v_pk_fma_f32 v[188:189], v[164:165], s[10:11], v[188:189] op_sel_hi:[1,0,1]
	v_pk_fma_f32 v[190:191], v[166:167], s[10:11], v[190:191] op_sel_hi:[1,0,1]
	v_cvt_pk_f32_fp8_e32 v[168:169], v131
	v_cvt_pk_f32_fp8_sdwa v[170:171], v131 src0_sel:WORD_1
	v_pk_fma_f32 v[188:189], v[168:169], s[10:11], v[188:189] op_sel_hi:[1,0,1]
	v_pk_fma_f32 v[190:191], v[170:171], s[10:11], v[190:191] op_sel_hi:[1,0,1]
	v_cvt_pk_f32_fp8_e32 v[172:173], v135
	v_cvt_pk_f32_fp8_sdwa v[174:175], v135 src0_sel:WORD_1
	v_pk_fma_f32 v[188:189], v[172:173], s[10:11], v[188:189] op_sel_hi:[1,0,1]
	v_pk_fma_f32 v[190:191], v[174:175], s[10:11], v[190:191] op_sel_hi:[1,0,1]
	global_store_dwordx4 v159, v[188:191], s[4:5] offset:3072
	s_branch .LBB0_1207
